# bundle9 + ALL global stores write-through (sc1), incl. dword/dwordx2
# baseline (speedup 1.0000x reference)
.LBB0_9:
	s_mul_hi_i32 s4, s20, 0x88888889
	s_add_i32 s4, s4, s20
	s_lshr_b32 s5, s4, 31
	s_ashr_i32 s4, s4, 11
	s_add_i32 s16, s4, s5
	s_mul_i32 s4, s16, 0xfffff100
	s_add_i32 s81, s20, s4
	s_cmpk_gt_i32 s81, 0x2ff
	s_mov_b64 s[4:5], -1
	s_cbranch_scc0 .LBB0_29
	s_cmpk_gt_u32 s81, 0x4ff
	s_cbranch_scc0 .LBB0_26
	s_cmpk_gt_u32 s81, 0x6ff
	s_cbranch_scc0 .LBB0_23
	s_ashr_i32 s17, s16, 31
	s_cmpk_gt_u32 s81, 0xcff
	s_cbranch_scc0 .LBB0_14
	s_lshl_b64 s[18:19], s[16:17], 20
	s_lshl_b64 s[4:5], s[16:17], 22
	s_add_u32 s82, s12, s4
	s_addc_u32 s83, s13, s5
	v_readlane_b32 s4, v254, 10
	s_add_u32 s5, s4, s18
	v_readlane_b32 s4, v254, 11
	s_addc_u32 s14, s4, s19
	s_mul_i32 s4, s16, 0xffffe200
	s_add_i32 s4, s28, s4
	s_and_b32 s17, s4, 0x7fffffc0
	s_and_b32 s4, s26, 0x3e0
	s_addk_i32 s17, 0xe600
	s_lshl_b32 s18, s4, 2
	v_or_b32_e32 v2, s17, v26
	s_add_u32 s18, s82, s18
	s_addc_u32 s19, s83, 0
	v_mov_b32_e32 v7, v3
	v_or_b32_e32 v12, 2, v2
	v_mov_b32_e32 v13, v3
	v_or_b32_e32 v14, 4, v2
	v_mov_b32_e32 v15, v3
	v_or_b32_e32 v16, 6, v2
	v_mov_b32_e32 v17, v3
	v_or_b32_e32 v18, 8, v2
	v_mov_b32_e32 v19, v3
	v_or_b32_e32 v20, 10, v2
	v_mov_b32_e32 v21, v3
	v_or_b32_e32 v22, 12, v2
	v_mov_b32_e32 v23, v3
	v_lshl_add_u64 v[8:9], s[18:19], 0, v[6:7]
	v_lshlrev_b64 v[10:11], 12, v[2:3]
	v_lshlrev_b64 v[12:13], 12, v[12:13]
	v_lshlrev_b64 v[14:15], 12, v[14:15]
	v_lshlrev_b64 v[16:17], 12, v[16:17]
	v_lshlrev_b64 v[18:19], 12, v[18:19]
	v_lshlrev_b64 v[20:21], 12, v[20:21]
	v_lshlrev_b64 v[22:23], 12, v[22:23]
	v_or_b32_e32 v24, 14, v2
	v_mov_b32_e32 v25, v3
	v_lshl_add_u64 v[10:11], v[8:9], 0, v[10:11]
	v_lshl_add_u64 v[12:13], v[8:9], 0, v[12:13]
	v_lshl_add_u64 v[14:15], v[8:9], 0, v[14:15]
	v_lshl_add_u64 v[16:17], v[8:9], 0, v[16:17]
	v_lshl_add_u64 v[18:19], v[8:9], 0, v[18:19]
	v_lshl_add_u64 v[20:21], v[8:9], 0, v[20:21]
	v_lshl_add_u64 v[22:23], v[8:9], 0, v[22:23]
	v_lshlrev_b64 v[24:25], 12, v[24:25]
	v_lshl_add_u64 v[24:25], v[8:9], 0, v[24:25]
	global_load_dword v7, v[10:11], off nt
	global_load_dword v77, v[12:13], off nt
	global_load_dword v78, v[14:15], off nt
	global_load_dword v79, v[16:17], off nt
	global_load_dword v80, v[18:19], off nt
	global_load_dword v81, v[20:21], off nt
	global_load_dword v82, v[22:23], off nt
	global_load_dword v83, v[24:25], off nt
	v_or_b32_e32 v10, 16, v2
	v_mov_b32_e32 v11, v3
	v_or_b32_e32 v12, 18, v2
	v_mov_b32_e32 v13, v3
	v_or_b32_e32 v14, 20, v2
	v_mov_b32_e32 v15, v3
	v_or_b32_e32 v16, 22, v2
	v_mov_b32_e32 v17, v3
	v_or_b32_e32 v18, 24, v2
	v_mov_b32_e32 v19, v3
	v_or_b32_e32 v20, 26, v2
	v_mov_b32_e32 v21, v3
	v_or_b32_e32 v22, 28, v2
	v_mov_b32_e32 v23, v3
	v_lshlrev_b64 v[10:11], 12, v[10:11]
	v_lshlrev_b64 v[12:13], 12, v[12:13]
	v_lshlrev_b64 v[14:15], 12, v[14:15]
	v_lshlrev_b64 v[16:17], 12, v[16:17]
	v_lshlrev_b64 v[18:19], 12, v[18:19]
	v_lshlrev_b64 v[20:21], 12, v[20:21]
	v_lshlrev_b64 v[22:23], 12, v[22:23]
	v_or_b32_e32 v24, 30, v2
	v_mov_b32_e32 v25, v3
	v_lshl_add_u64 v[10:11], v[8:9], 0, v[10:11]
	v_lshl_add_u64 v[12:13], v[8:9], 0, v[12:13]
	v_lshl_add_u64 v[14:15], v[8:9], 0, v[14:15]
	v_lshl_add_u64 v[16:17], v[8:9], 0, v[16:17]
	v_lshl_add_u64 v[18:19], v[8:9], 0, v[18:19]
	v_lshl_add_u64 v[20:21], v[8:9], 0, v[20:21]
	v_lshl_add_u64 v[22:23], v[8:9], 0, v[22:23]
	v_lshlrev_b64 v[24:25], 12, v[24:25]
	v_lshl_add_u64 v[24:25], v[8:9], 0, v[24:25]
	global_load_dword v84, v[10:11], off nt
	global_load_dword v85, v[12:13], off nt
	global_load_dword v86, v[14:15], off nt
	global_load_dword v87, v[16:17], off nt
	global_load_dword v88, v[18:19], off nt
	global_load_dword v89, v[20:21], off nt
	global_load_dword v90, v[22:23], off nt
	global_load_dword v91, v[24:25], off nt
	v_or_b32_e32 v10, 32, v2
	v_mov_b32_e32 v11, v3
	v_or_b32_e32 v12, 34, v2
	v_mov_b32_e32 v13, v3
	v_or_b32_e32 v14, 36, v2
	v_mov_b32_e32 v15, v3
	v_or_b32_e32 v16, 38, v2
	v_mov_b32_e32 v17, v3
	v_or_b32_e32 v18, 40, v2
	v_mov_b32_e32 v19, v3
	v_or_b32_e32 v20, 42, v2
	v_mov_b32_e32 v21, v3
	v_or_b32_e32 v22, 44, v2
	v_mov_b32_e32 v23, v3
	v_lshlrev_b64 v[10:11], 12, v[10:11]
	v_lshlrev_b64 v[12:13], 12, v[12:13]
	v_lshlrev_b64 v[14:15], 12, v[14:15]
	v_lshlrev_b64 v[16:17], 12, v[16:17]
	v_lshlrev_b64 v[18:19], 12, v[18:19]
	v_lshlrev_b64 v[20:21], 12, v[20:21]
	v_lshlrev_b64 v[22:23], 12, v[22:23]
	v_or_b32_e32 v24, 46, v2
	v_mov_b32_e32 v25, v3
	v_lshl_add_u64 v[10:11], v[8:9], 0, v[10:11]
	v_lshl_add_u64 v[12:13], v[8:9], 0, v[12:13]
	v_lshl_add_u64 v[14:15], v[8:9], 0, v[14:15]
	v_lshl_add_u64 v[16:17], v[8:9], 0, v[16:17]
	v_lshl_add_u64 v[18:19], v[8:9], 0, v[18:19]
	v_lshl_add_u64 v[20:21], v[8:9], 0, v[20:21]
	v_lshl_add_u64 v[22:23], v[8:9], 0, v[22:23]
	v_lshlrev_b64 v[24:25], 12, v[24:25]
	v_lshl_add_u64 v[24:25], v[8:9], 0, v[24:25]
	global_load_dword v92, v[10:11], off nt
	global_load_dword v93, v[12:13], off nt
	global_load_dword v94, v[14:15], off nt
	global_load_dword v95, v[16:17], off nt
	global_load_dword v96, v[18:19], off nt
	global_load_dword v97, v[20:21], off nt
	global_load_dword v98, v[22:23], off nt
	global_load_dword v99, v[24:25], off nt
	v_or_b32_e32 v10, 48, v2
	v_mov_b32_e32 v11, v3
	v_or_b32_e32 v12, 50, v2
	v_mov_b32_e32 v13, v3
	v_or_b32_e32 v14, 52, v2
	v_mov_b32_e32 v15, v3
	v_or_b32_e32 v16, 54, v2
	v_mov_b32_e32 v17, v3
	v_or_b32_e32 v18, 56, v2
	v_mov_b32_e32 v19, v3
	v_or_b32_e32 v20, 58, v2
	v_mov_b32_e32 v21, v3
	v_or_b32_e32 v22, 60, v2
	v_mov_b32_e32 v23, v3
	v_or_b32_e32 v2, 62, v2
	v_lshlrev_b64 v[10:11], 12, v[10:11]
	v_lshlrev_b64 v[12:13], 12, v[12:13]
	v_lshlrev_b64 v[14:15], 12, v[14:15]
	v_lshlrev_b64 v[16:17], 12, v[16:17]
	v_lshlrev_b64 v[18:19], 12, v[18:19]
	v_lshlrev_b64 v[20:21], 12, v[20:21]
	v_lshlrev_b64 v[22:23], 12, v[22:23]
	v_lshlrev_b64 v[24:25], 12, v[2:3]
	v_lshl_add_u64 v[10:11], v[8:9], 0, v[10:11]
	v_lshl_add_u64 v[12:13], v[8:9], 0, v[12:13]
	v_lshl_add_u64 v[14:15], v[8:9], 0, v[14:15]
	v_lshl_add_u64 v[16:17], v[8:9], 0, v[16:17]
	v_lshl_add_u64 v[18:19], v[8:9], 0, v[18:19]
	v_lshl_add_u64 v[20:21], v[8:9], 0, v[20:21]
	v_lshl_add_u64 v[22:23], v[8:9], 0, v[22:23]
	v_lshl_add_u64 v[8:9], v[8:9], 0, v[24:25]
	global_load_dword v2, v[10:11], off nt
	s_nop 0
	global_load_dword v10, v[12:13], off nt
	global_load_dword v11, v[14:15], off nt
	s_nop 0
	global_load_dword v12, v[16:17], off nt
	global_load_dword v13, v[18:19], off nt
	global_load_dword v14, v[20:21], off nt
	global_load_dword v15, v[22:23], off nt
	s_nop 0
	global_load_dword v8, v[8:9], off nt
	s_waitcnt vmcnt(30)
	ds_write2_b32 v27, v7, v77 offset1:66
	s_waitcnt vmcnt(28)
	ds_write2_b32 v27, v78, v79 offset0:132 offset1:198
	s_waitcnt vmcnt(26)
	ds_write2_b32 v38, v80, v81 offset0:8 offset1:74
	s_waitcnt vmcnt(24)
	ds_write2_b32 v38, v82, v83 offset0:140 offset1:206
	s_waitcnt vmcnt(22)
	ds_write2_b32 v39, v84, v85 offset0:16 offset1:82
	s_waitcnt vmcnt(20)
	ds_write2_b32 v39, v86, v87 offset0:148 offset1:214
	s_waitcnt vmcnt(18)
	ds_write2_b32 v40, v88, v89 offset0:24 offset1:90
	s_waitcnt vmcnt(16)
	ds_write2_b32 v40, v90, v91 offset0:156 offset1:222
	s_waitcnt vmcnt(14)
	ds_write2_b32 v41, v92, v93 offset0:32 offset1:98
	s_waitcnt vmcnt(12)
	ds_write2_b32 v41, v94, v95 offset0:164 offset1:230
	s_waitcnt vmcnt(10)
	ds_write2_b32 v42, v96, v97 offset0:40 offset1:106
	s_waitcnt vmcnt(8)
	ds_write2_b32 v42, v98, v99 offset0:172 offset1:238
	s_waitcnt vmcnt(6)
	ds_write2_b32 v43, v2, v10 offset0:48 offset1:114
	s_waitcnt vmcnt(4)
	ds_write2_b32 v43, v11, v12 offset0:180 offset1:246
	s_waitcnt vmcnt(2)
	ds_write2_b32 v44, v13, v14 offset0:56 offset1:122
	s_waitcnt vmcnt(0)
	ds_write2_b32 v44, v15, v8 offset0:188 offset1:254
	s_waitcnt lgkmcnt(0)
	ds_read2_b32 v[10:11], v29 offset0:33 offset1:41
	ds_read2_b32 v[12:13], v29 offset0:66 offset1:74
	ds_read2_b32 v[14:15], v29 offset0:99 offset1:107
	ds_read2_b32 v[16:17], v29 offset1:8
	ds_read2_b32 v[18:19], v29 offset0:132 offset1:140
	ds_read2_b32 v[20:21], v29 offset0:165 offset1:173
	ds_read2_b32 v[22:23], v29 offset0:198 offset1:206
	ds_read2_b32 v[24:25], v29 offset0:231 offset1:239
	s_waitcnt lgkmcnt(4)
	v_mul_f32_e32 v2, 0x42000000, v16
	v_mul_f32_e32 v7, 0x42000000, v10
	v_med3_f32 v2, v2, s30, v45
	v_med3_f32 v7, v7, s30, v45
	v_mov_b32_e32 v78, v3
	v_cvt_pk_fp8_f32 v78, v2, v7
	v_mul_f32_e32 v10, 0x42000000, v12
	v_mul_f32_e32 v2, 0x42000000, v14
	v_med3_f32 v7, v10, s30, v45
	v_med3_f32 v2, v2, s30, v45
	v_cvt_pk_fp8_f32 v78, v7, v2 op_sel:[0,0,1]
	s_waitcnt lgkmcnt(3)
	v_mul_f32_e32 v2, 0x42000000, v18
	s_waitcnt lgkmcnt(2)
	v_mul_f32_e32 v7, 0x42000000, v20
	v_med3_f32 v2, v2, s30, v45
	v_med3_f32 v7, v7, s30, v45
	v_mov_b32_e32 v79, v3
	v_cvt_pk_fp8_f32 v79, v2, v7
	s_waitcnt lgkmcnt(1)
	v_mul_f32_e32 v10, 0x42000000, v22
	s_waitcnt lgkmcnt(0)
	v_mul_f32_e32 v2, 0x42000000, v24
	s_add_u32 s18, s5, s17
	v_med3_f32 v7, v10, s30, v45
	v_med3_f32 v2, v2, s30, v45
	s_addc_u32 s19, s14, 0
	v_cvt_pk_fp8_f32 v79, v7, v2 op_sel:[0,0,1]
	v_or_b32_e32 v2, s4, v28
	v_lshl_add_u64 v[8:9], s[18:19], 0, v[4:5]
	v_lshlrev_b32_e32 v2, 10, v2
	v_lshl_add_u64 v[80:81], v[8:9], 0, v[2:3]
	v_mul_f32_e32 v2, 0x42000000, v17
	v_mul_f32_e32 v7, 0x42000000, v11
	v_med3_f32 v2, v2, s30, v45
	v_med3_f32 v7, v7, s30, v45
	v_mov_b32_e32 v10, v3
	v_cvt_pk_fp8_f32 v10, v2, v7
	v_mul_f32_e32 v11, 0x42000000, v13
	v_mul_f32_e32 v2, 0x42000000, v15
	v_med3_f32 v7, v11, s30, v45
	v_med3_f32 v2, v2, s30, v45
	v_cvt_pk_fp8_f32 v10, v7, v2 op_sel:[0,0,1]
	v_mul_f32_e32 v2, 0x42000000, v19
	v_mul_f32_e32 v7, 0x42000000, v21
	v_med3_f32 v2, v2, s30, v45
	v_med3_f32 v7, v7, s30, v45
	v_mov_b32_e32 v11, v3
	v_cvt_pk_fp8_f32 v11, v2, v7
	v_mul_f32_e32 v12, 0x42000000, v23
	v_mul_f32_e32 v2, 0x42000000, v25
	v_med3_f32 v7, v12, s30, v45
	v_med3_f32 v2, v2, s30, v45
	v_cvt_pk_fp8_f32 v11, v7, v2 op_sel:[0,0,1]
	v_or_b32_e32 v2, s4, v30
	v_lshlrev_b32_e32 v2, 10, v2
	v_lshl_add_u64 v[12:13], v[8:9], 0, v[2:3]
	global_store_dwordx2 v[80:81], v[78:79], off sc1
	global_store_dwordx2 v[12:13], v[10:11], off sc1
	ds_read2_b32 v[10:11], v29 offset0:49 offset1:57
	ds_read2_b32 v[12:13], v29 offset0:82 offset1:90
	ds_read2_b32 v[14:15], v29 offset0:115 offset1:123
	ds_read2_b32 v[16:17], v29 offset0:16 offset1:24
	ds_read2_b32 v[18:19], v29 offset0:148 offset1:156
	ds_read2_b32 v[20:21], v29 offset0:181 offset1:189
	ds_read2_b32 v[22:23], v29 offset0:214 offset1:222
	ds_read2_b32 v[24:25], v29 offset0:247 offset1:255
	s_waitcnt lgkmcnt(4)
	v_mul_f32_e32 v2, 0x42000000, v16
	v_mul_f32_e32 v7, 0x42000000, v10
	v_med3_f32 v2, v2, s30, v45
	v_med3_f32 v7, v7, s30, v45
	v_mov_b32_e32 v78, v3
	v_cvt_pk_fp8_f32 v78, v2, v7
	v_mul_f32_e32 v10, 0x42000000, v12
	v_mul_f32_e32 v2, 0x42000000, v14
	v_med3_f32 v7, v10, s30, v45
	v_med3_f32 v2, v2, s30, v45
	v_cvt_pk_fp8_f32 v78, v7, v2 op_sel:[0,0,1]
	s_waitcnt lgkmcnt(3)
	v_mul_f32_e32 v2, 0x42000000, v18
	s_waitcnt lgkmcnt(2)
	v_mul_f32_e32 v7, 0x42000000, v20
	v_med3_f32 v2, v2, s30, v45
	v_med3_f32 v7, v7, s30, v45
	v_mov_b32_e32 v79, v3
	v_cvt_pk_fp8_f32 v79, v2, v7
	s_waitcnt lgkmcnt(1)
	v_mul_f32_e32 v10, 0x42000000, v22
	s_waitcnt lgkmcnt(0)
	v_mul_f32_e32 v2, 0x42000000, v24
	v_med3_f32 v7, v10, s30, v45
	v_med3_f32 v2, v2, s30, v45
	v_cvt_pk_fp8_f32 v79, v7, v2 op_sel:[0,0,1]
	v_or_b32_e32 v2, s4, v31
	v_lshlrev_b32_e32 v2, 10, v2
	v_lshl_add_u64 v[80:81], v[8:9], 0, v[2:3]
	v_mul_f32_e32 v2, 0x42000000, v17
	v_mul_f32_e32 v7, 0x42000000, v11
	v_med3_f32 v2, v2, s30, v45
	v_med3_f32 v7, v7, s30, v45
	v_mov_b32_e32 v10, v3
	v_cvt_pk_fp8_f32 v10, v2, v7
	v_mul_f32_e32 v11, 0x42000000, v13
	v_mul_f32_e32 v2, 0x42000000, v15
	v_med3_f32 v7, v11, s30, v45
	v_med3_f32 v2, v2, s30, v45
	v_cvt_pk_fp8_f32 v10, v7, v2 op_sel:[0,0,1]
	v_mul_f32_e32 v2, 0x42000000, v19
	v_mul_f32_e32 v7, 0x42000000, v21
	v_med3_f32 v2, v2, s30, v45
	v_med3_f32 v7, v7, s30, v45
	v_mov_b32_e32 v11, v3
	v_cvt_pk_fp8_f32 v11, v2, v7
	v_mul_f32_e32 v12, 0x42000000, v23
	v_mul_f32_e32 v2, 0x42000000, v25
	v_med3_f32 v7, v12, s30, v45
	v_med3_f32 v2, v2, s30, v45
	v_cvt_pk_fp8_f32 v11, v7, v2 op_sel:[0,0,1]
	v_or_b32_e32 v2, s4, v32
	v_lshlrev_b32_e32 v2, 10, v2
	v_lshl_add_u64 v[8:9], v[8:9], 0, v[2:3]
	global_store_dwordx2 v[80:81], v[78:79], off sc1
	global_store_dwordx2 v[8:9], v[10:11], off sc1
	s_waitcnt lgkmcnt(0)
	s_mov_b64 s[4:5], 0

.LBB0_19:
	s_waitcnt lgkmcnt(3)
	v_mul_f32_e32 v7, 0x42000000, v14
	v_mul_f32_e32 v14, 0x42000000, v15
	s_waitcnt lgkmcnt(2)
	v_mul_f32_e32 v15, 0x42000000, v12
	v_med3_f32 v7, v7, s30, v45
	v_med3_f32 v14, v14, s30, v45
	v_mov_b32_e32 v12, 0
	v_cvt_pk_fp8_f32 v12, v7, v14
	v_mul_f32_e32 v7, 0x42000000, v13
	v_med3_f32 v13, v15, s30, v45
	v_med3_f32 v7, v7, s30, v45
	v_cvt_pk_fp8_f32 v12, v13, v7 op_sel:[0,0,1]
	s_waitcnt lgkmcnt(1)
	v_mul_f32_e32 v7, 0x42000000, v10
	v_mul_f32_e32 v10, 0x42000000, v11
	v_med3_f32 v7, v7, s30, v45
	v_med3_f32 v10, v10, s30, v45
	v_mov_b32_e32 v13, 0
	v_cvt_pk_fp8_f32 v13, v7, v10
	s_mul_i32 s82, s16, 0x300000
	v_readlane_b32 s83, v254, 8
	s_mul_hi_i32 s19, s16, 0x300000
	s_add_u32 s82, s83, s82
	v_readlane_b32 s83, v254, 9
	s_waitcnt lgkmcnt(0)
	v_mul_f32_e32 v8, 0x42000000, v8
	v_mul_f32_e32 v7, 0x42000000, v9
	s_addc_u32 s19, s83, s19
	s_and_b32 s17, s17, 0xffff
	v_med3_f32 v8, v8, s30, v45
	v_med3_f32 v7, v7, s30, v45
	s_add_u32 s82, s82, s17
	v_cvt_pk_fp8_f32 v13, v8, v7 op_sel:[0,0,1]
	s_addc_u32 s83, s19, 0
	v_lshl_add_u64 v[8:9], s[82:83], 0, v[4:5]
	v_lshlrev_b64 v[10:11], 10, v[2:3]
	v_lshl_add_u64 v[10:11], v[8:9], 0, v[10:11]
	global_store_dwordx2 v[10:11], v[12:13], off sc1
	ds_read2_b32 v[20:21], v29 offset0:41 offset1:49
	ds_read2_b32 v[22:23], v29 offset0:74 offset1:82
	ds_read2_b32 v[12:13], v29 offset0:107 offset1:115
	ds_read2_b32 v[24:25], v29 offset0:8 offset1:16
	ds_read2_b32 v[14:15], v29 offset0:140 offset1:148
	ds_read2_b32 v[16:17], v29 offset0:173 offset1:181
	ds_read2_b32 v[18:19], v29 offset0:206 offset1:214
	ds_read2_b32 v[10:11], v29 offset0:239 offset1:247
	s_waitcnt lgkmcnt(4)
	v_mul_f32_e32 v2, 0x42000000, v24
	v_mul_f32_e32 v7, 0x42000000, v20
	v_med3_f32 v2, v2, s30, v45
	v_med3_f32 v7, v7, s30, v45
	v_mov_b32_e32 v78, v3
	v_cvt_pk_fp8_f32 v78, v2, v7
	v_mul_f32_e32 v20, 0x42000000, v22
	v_mul_f32_e32 v2, 0x42000000, v12
	v_med3_f32 v7, v20, s30, v45
	v_med3_f32 v2, v2, s30, v45
	v_cvt_pk_fp8_f32 v78, v7, v2 op_sel:[0,0,1]
	s_waitcnt lgkmcnt(3)
	v_mul_f32_e32 v2, 0x42000000, v14
	s_waitcnt lgkmcnt(2)
	v_mul_f32_e32 v7, 0x42000000, v16
	v_med3_f32 v2, v2, s30, v45
	v_med3_f32 v7, v7, s30, v45
	v_mov_b32_e32 v79, v3
	v_cvt_pk_fp8_f32 v79, v2, v7
	s_waitcnt lgkmcnt(1)
	v_mul_f32_e32 v12, 0x42000000, v18
	s_waitcnt lgkmcnt(0)
	v_mul_f32_e32 v2, 0x42000000, v10
	v_med3_f32 v7, v12, s30, v45
	v_med3_f32 v2, v2, s30, v45
	v_cvt_pk_fp8_f32 v79, v7, v2 op_sel:[0,0,1]
	v_or_b32_e32 v2, s18, v35
	v_cndmask_b32_e64 v2, v30, v2, s[4:5]
	v_or_b32_e32 v2, s14, v2
	v_lshlrev_b32_e32 v2, 10, v2
	v_lshl_add_u64 v[80:81], v[8:9], 0, v[2:3]
	s_andn2_b64 vcc, exec, s[4:5]
	v_or_b32_e32 v2, s14, v31
	global_store_dwordx2 v[80:81], v[78:79], off sc1
	s_cbranch_vccnz .LBB0_21
	v_lshrrev_b32_e32 v2, 2, v2
	s_and_b32 s17, s14, 0xfc0
	v_and_b32_e32 v2, 12, v2
	v_or3_b32 v2, s17, v2, v36
.LBB0_21:
	v_mul_f32_e32 v7, 0x42000000, v25
	v_mul_f32_e32 v10, 0x42000000, v21
	v_med3_f32 v7, v7, s30, v45
	v_med3_f32 v10, v10, s30, v45
	v_mov_b32_e32 v12, v3
	v_cvt_pk_fp8_f32 v12, v7, v10
	v_mul_f32_e32 v14, 0x42000000, v23
	v_mul_f32_e32 v7, 0x42000000, v13
	v_med3_f32 v10, v14, s30, v45
	v_med3_f32 v7, v7, s30, v45
	v_cvt_pk_fp8_f32 v12, v10, v7 op_sel:[0,0,1]
	v_mul_f32_e32 v7, 0x42000000, v15
	v_mul_f32_e32 v10, 0x42000000, v17
	v_med3_f32 v7, v7, s30, v45
	v_med3_f32 v10, v10, s30, v45
	v_mov_b32_e32 v13, v3
	v_cvt_pk_fp8_f32 v13, v7, v10
	v_mul_f32_e32 v14, 0x42000000, v19
	v_mul_f32_e32 v7, 0x42000000, v11
	v_med3_f32 v10, v14, s30, v45
	v_med3_f32 v7, v7, s30, v45
	v_cvt_pk_fp8_f32 v13, v10, v7 op_sel:[0,0,1]
	v_lshlrev_b32_e32 v2, 10, v2
	v_lshl_add_u64 v[10:11], v[8:9], 0, v[2:3]
	v_or_b32_e32 v2, s14, v32
	global_store_dwordx2 v[10:11], v[12:13], off sc1
	ds_read2_b32 v[10:11], v29 offset0:24 offset1:57
	ds_read2_b32 v[12:13], v29 offset0:90 offset1:123
	ds_read2_b32 v[14:15], v29 offset0:156 offset1:189
	ds_read2_b32 v[16:17], v29 offset0:222 offset1:255
	s_waitcnt lgkmcnt(3)
	v_mul_f32_e32 v7, 0x42000000, v10
	v_mul_f32_e32 v10, 0x42000000, v11
	s_waitcnt lgkmcnt(2)
	v_mul_f32_e32 v11, 0x42000000, v12
	v_med3_f32 v7, v7, s30, v45
	v_med3_f32 v12, v10, s30, v45
	v_mov_b32_e32 v10, v3
	v_cvt_pk_fp8_f32 v10, v7, v12
	v_mul_f32_e32 v7, 0x42000000, v13
	v_med3_f32 v11, v11, s30, v45
	v_med3_f32 v7, v7, s30, v45
	v_cvt_pk_fp8_f32 v10, v11, v7 op_sel:[0,0,1]
	s_waitcnt lgkmcnt(1)
	v_mul_f32_e32 v7, 0x42000000, v14
	v_mul_f32_e32 v11, 0x42000000, v15
	v_med3_f32 v7, v7, s30, v45
	v_med3_f32 v13, v11, s30, v45
	v_mov_b32_e32 v11, v3
	v_cvt_pk_fp8_f32 v11, v7, v13
	s_waitcnt lgkmcnt(0)
	v_mul_f32_e32 v12, 0x42000000, v16
	v_mul_f32_e32 v7, 0x42000000, v17
	v_med3_f32 v12, v12, s30, v45
	v_med3_f32 v7, v7, s30, v45
	v_cvt_pk_fp8_f32 v11, v12, v7 op_sel:[0,0,1]
	v_lshrrev_b32_e32 v7, 2, v2
	v_and_b32_e32 v7, 12, v7
	v_or3_b32 v7, v7, v37, s14
	v_cndmask_b32_e64 v2, v2, v7, s[4:5]
	v_lshlrev_b32_e32 v2, 10, v2
	v_lshl_add_u64 v[8:9], v[8:9], 0, v[2:3]
	global_store_dwordx2 v[8:9], v[10:11], off sc1
	s_waitcnt lgkmcnt(0)

.LBB0_87:
	v_ashrrev_i32_e32 v6, 3, v9
	v_ashrrev_i32_e32 v7, 31, v6
	v_lshl_add_u64 v[10:11], v[6:7], 2, s[0:1]
	global_load_dword v10, v[10:11], off
	v_add_u32_e32 v9, s63, v9
	v_cmp_lt_i32_e32 vcc, s8, v9
	v_lshlrev_b64 v[6:7], 6, v[6:7]
	s_or_b64 s[6:7], vcc, s[6:7]
	v_lshl_add_u64 v[6:7], v[2:3], 0, v[6:7]
	s_waitcnt vmcnt(0)
	v_cvt_f64_i32_e32 v[10:11], v10
	v_mul_f64 v[12:13], v[4:5], v[10:11]
	v_rndne_f64_e32 v[12:13], v[12:13]
	v_fma_f64 v[10:11], v[4:5], v[10:11], -v[12:13]
	v_cvt_f32_f64_e32 v10, v[10:11]
	v_cos_f32_e32 v11, v10
	v_sin_f32_e32 v10, v10
	global_store_dword v[6:7], v11, off sc1
	global_store_dword v[6:7], v10, off offset:32 sc1
	s_andn2_b64 exec, exec, s[6:7]
	s_cbranch_execnz .LBB0_87

.LBB0_107:
	global_load_dword v5, v[0:1], off
	v_and_b32_e32 v7, 0x3fffff80, v4
	v_ashrrev_i32_e32 v6, 7, v4
	v_add_u32_e32 v16, 0x200, v4
	v_lshl_add_u32 v22, v7, 2, v36
	v_cmp_lt_i32_e64 s[4:5], s27, v4
	v_ashrrev_i32_e32 v7, 31, v6
	v_mov_b32_e32 v4, v16
	ds_read2st64_b32 v[16:17], v22 offset0:128 offset1:144
	ds_read2st64_b32 v[18:19], v22 offset0:160 offset1:176
	ds_read2st64_b32 v[20:21], v22 offset0:192 offset1:208
	ds_read2st64_b32 v[22:23], v22 offset0:224 offset1:240
	v_lshl_add_u64 v[6:7], s[8:9], 0, v[6:7]
	s_or_b64 s[6:7], s[4:5], s[6:7]
	v_mad_u64_u32 v[24:25], s[4:5], v6, s3, v[2:3]
	s_waitcnt lgkmcnt(3)
	v_add_f32_e32 v6, 0, v16
	v_add_f32_e32 v6, v6, v17
	s_waitcnt lgkmcnt(2)
	v_add_f32_e32 v6, v6, v18
	v_add_f32_e32 v6, v6, v19
	s_waitcnt lgkmcnt(1)
	v_add_f32_e32 v6, v6, v20
	v_add_f32_e32 v6, v6, v21
	s_waitcnt lgkmcnt(0)
	v_add_f32_e32 v6, v6, v22
	v_add_f32_e32 v6, v6, v23
	v_mad_i32_i24 v25, v7, s3, v25
	s_waitcnt vmcnt(0)
	v_add_f32_e32 v5, v6, v5
	global_store_dword v[24:25], v5, off sc1
	s_andn2_b64 exec, exec, s[6:7]
	s_cbranch_execnz .LBB0_107
	s_branch .LBB0_102

.LBB0_210:
	s_and_b64 vcc, exec, s[4:5]
	s_cbranch_vccnz .LBB0_212
	s_waitcnt vmcnt(6)
	v_cvt_pk_f32_fp8_e32 v[94:95], v64
	v_cvt_pk_f32_fp8_sdwa v[92:93], v64 src0_sel:WORD_1
	v_cvt_pk_f32_fp8_e32 v[114:115], v100
	v_cvt_pk_f32_fp8_sdwa v[116:117], v100 src0_sel:WORD_1
	v_pk_mul_f32 v[94:95], s[10:11], v[94:95] op_sel_hi:[0,1]
	v_pk_mul_f32 v[92:93], s[10:11], v[92:93] op_sel_hi:[0,1]
	v_pk_fma_f32 v[94:95], s[8:9], v[114:115], v[94:95] op_sel_hi:[0,1,1]
	v_pk_fma_f32 v[92:93], s[8:9], v[116:117], v[92:93] op_sel_hi:[0,1,1]
	s_waitcnt vmcnt(3)
	v_pk_fma_f32 v[44:45], v[50:51], v[94:95], v[44:45]
	v_cvt_pk_f32_fp8_e32 v[94:95], v98
	v_pk_fma_f32 v[46:47], v[52:53], v[92:93], v[46:47]
	v_cvt_pk_f32_fp8_sdwa v[92:93], v98 src0_sel:WORD_1
	v_cvt_pk_f32_fp8_e32 v[114:115], v101
	v_cvt_pk_f32_fp8_sdwa v[116:117], v101 src0_sel:WORD_1
	v_pk_mul_f32 v[94:95], s[10:11], v[94:95] op_sel_hi:[0,1]
	v_pk_mul_f32 v[92:93], s[10:11], v[92:93] op_sel_hi:[0,1]
	v_pk_fma_f32 v[94:95], s[8:9], v[114:115], v[94:95] op_sel_hi:[0,1,1]
	v_pk_fma_f32 v[92:93], s[8:9], v[116:117], v[92:93] op_sel_hi:[0,1,1]
	s_waitcnt vmcnt(2)
	v_pk_fma_f32 v[40:41], v[48:49], v[94:95], v[40:41]
	v_cvt_pk_f32_fp8_e32 v[94:95], v99
	v_pk_fma_f32 v[42:43], v[54:55], v[92:93], v[42:43]
	v_cvt_pk_f32_fp8_sdwa v[92:93], v99 src0_sel:WORD_1
	v_cvt_pk_f32_fp8_e32 v[114:115], v102
	v_cvt_pk_f32_fp8_sdwa v[116:117], v102 src0_sel:WORD_1
	v_pk_mul_f32 v[94:95], s[10:11], v[94:95] op_sel_hi:[0,1]
	v_pk_mul_f32 v[92:93], s[10:11], v[92:93] op_sel_hi:[0,1]
	v_pk_fma_f32 v[94:95], s[8:9], v[114:115], v[94:95] op_sel_hi:[0,1,1]
	v_pk_fma_f32 v[92:93], s[8:9], v[116:117], v[92:93] op_sel_hi:[0,1,1]
	s_waitcnt vmcnt(1)
	v_pk_fma_f32 v[36:37], v[58:59], v[94:95], v[36:37]
	v_cvt_pk_f32_fp8_e32 v[94:95], v103
	v_pk_fma_f32 v[38:39], v[60:61], v[92:93], v[38:39]
	v_cvt_pk_f32_fp8_sdwa v[92:93], v103 src0_sel:WORD_1
	s_waitcnt vmcnt(0)
	v_cvt_pk_f32_fp8_e32 v[114:115], v104
	v_cvt_pk_f32_fp8_sdwa v[116:117], v104 src0_sel:WORD_1
	v_pk_mul_f32 v[94:95], s[10:11], v[94:95] op_sel_hi:[0,1]
	v_pk_mul_f32 v[92:93], s[10:11], v[92:93] op_sel_hi:[0,1]
	v_pk_fma_f32 v[94:95], s[8:9], v[114:115], v[94:95] op_sel_hi:[0,1,1]
	v_pk_fma_f32 v[92:93], s[8:9], v[116:117], v[92:93] op_sel_hi:[0,1,1]
	v_pk_fma_f32 v[32:33], v[56:57], v[94:95], v[32:33]
	v_add_co_u32_e32 v94, vcc, s74, v90
	v_pk_fma_f32 v[34:35], v[62:63], v[92:93], v[34:35]
	v_cvt_pk_f16_f32 v93, v46, v47
	v_cvt_pk_f16_f32 v92, v44, v45
	v_addc_co_u32_e32 v95, vcc, 0, v91, vcc
	global_store_dwordx2 v[94:95], v[92:93], off nt sc1
	v_cvt_pk_f16_f32 v93, v42, v43
	v_cvt_pk_f16_f32 v92, v40, v41
	global_store_dwordx2 v[94:95], v[92:93], off offset:512 nt sc1
	v_cvt_pk_f16_f32 v93, v38, v39
	v_cvt_pk_f16_f32 v92, v36, v37
	global_store_dwordx2 v[94:95], v[92:93], off offset:1024 nt sc1
	v_cvt_pk_f16_f32 v93, v34, v35
	v_cvt_pk_f16_f32 v92, v32, v33
	global_store_dwordx2 v[94:95], v[92:93], off offset:1536 nt sc1
.LBB0_212:
	s_waitcnt vmcnt(3)
	v_pk_mul_f32 v[92:93], v[46:47], v[46:47]
	v_pk_mul_f32 v[94:95], v[44:45], v[44:45]
	s_andn2_b64 vcc, exec, s[50:51]
	v_pk_mov_b32 v[114:115], v[94:95], v[92:93] op_sel:[1,0]
	v_mov_b32_e32 v95, v93
	v_pk_add_f32 v[92:93], v[114:115], v[94:95]
	s_waitcnt vmcnt(2)
	v_pk_mul_f32 v[94:95], v[42:43], v[42:43]
	v_pk_add_f32 v[92:93], v[92:93], v[92:93] op_sel_hi:[0,1]
	v_pk_mul_f32 v[114:115], v[40:41], v[40:41]
	s_waitcnt vmcnt(1)
	v_mul_f32_e32 v92, v36, v36
	v_pk_mov_b32 v[116:117], v[114:115], v[94:95] op_sel:[1,0]
	v_mov_b32_e32 v115, v95
	v_pk_add_f32 v[94:95], v[116:117], v[114:115]
	v_pk_fma_f32 v[114:115], v[36:37], v[36:37], v[92:93] op_sel_hi:[1,1,0]
	v_mul_f32_e32 v92, v38, v38
	v_pk_add_f32 v[94:95], v[94:95], v[94:95] op_sel_hi:[0,1]
	v_pk_fma_f32 v[116:117], v[38:39], v[38:39], v[92:93] op_sel_hi:[1,1,0]
	s_waitcnt vmcnt(0)
	v_mul_f32_e32 v114, v32, v32
	v_mul_f32_e32 v116, v33, v33
	v_mul_f32_e32 v94, v34, v34
	v_mul_f32_e32 v92, v35, v35
	v_pk_add_f32 v[114:115], v[114:115], v[116:117]
	v_pk_add_f32 v[92:93], v[94:95], v[92:93]
	s_nop 0
	v_pk_add_f32 v[92:93], v[114:115], v[92:93]
	s_nop 0
	v_add_f32_e32 v92, v92, v93
	s_nop 1
	v_add_f32_dpp v92, v92, v92 quad_perm:[1,0,3,2] row_mask:0xf bank_mask:0xf bound_ctrl:1
	s_nop 1
	v_add_f32_dpp v92, v92, v92 quad_perm:[2,3,0,1] row_mask:0xf bank_mask:0xf bound_ctrl:1
	s_nop 1
	v_add_f32_dpp v92, v92, v92 row_half_mirror row_mask:0xf bank_mask:0xf bound_ctrl:1
	s_nop 1
	v_add_f32_dpp v92, v92, v92 row_mirror row_mask:0xf bank_mask:0xf bound_ctrl:1
	s_nop 0
	v_readlane_b32 s12, v92, 16
	v_readlane_b32 s13, v92, 48
	v_readlane_b32 s6, v92, 0
	v_readlane_b32 s7, v92, 32
	v_mov_b32_e32 v92, s12
	v_mov_b32_e32 v93, s13
	v_pk_add_f32 v[92:93], s[6:7], v[92:93]
	s_mov_b64 s[12:13], -1
	v_add_f32_e32 v92, v92, v93
	v_fmamk_f32 v92, v92, 0x3a800000, v229
	v_rsq_f32_e32 v94, v92
	v_lshl_add_u64 v[92:93], s[42:43], 0, v[86:87]
	v_pk_mul_f32 v[114:115], v[44:45], v[94:95] op_sel_hi:[1,0]
	v_pk_mul_f32 v[44:45], v[46:47], v[94:95] op_sel_hi:[1,0]
	v_cndmask_b32_e64 v95, 0, 1, s[50:51]
	v_pk_fma_f32 v[44:45], v[78:79], v[44:45], v[2:3]
	v_pk_fma_f32 v[46:47], v[80:81], v[114:115], v[0:1]
	v_cmp_ne_u32_e64 s[6:7], 1, v95
	s_cbranch_vccnz .LBB0_214
	v_med3_f32 v95, v46, s55, v228
	v_med3_f32 v113, v47, s55, v228
	v_mov_b32_e32 v116, v65
	v_cvt_pk_fp8_f32 v116, v95, v113
	v_med3_f32 v95, v44, s55, v228
	v_med3_f32 v113, v45, s55, v228
	v_add_co_u32_e32 v114, vcc, 0x6800000, v92
	v_cvt_pk_fp8_f32 v116, v95, v113 op_sel:[0,0,1]
	s_nop 0
	v_addc_co_u32_e32 v115, vcc, 0, v93, vcc
	s_mov_b64 s[12:13], 0
	global_store_dword v[114:115], v116, off sc1
.LBB0_214:
	s_andn2_b64 vcc, exec, s[12:13]
	s_cbranch_vccnz .LBB0_216
	v_cvt_pk_bf16_f32 v46, v46, v47
	v_cvt_pk_bf16_f32 v47, v44, v45
	v_add_co_u32_e32 v44, vcc, 0x6800000, v90
	s_nop 1
	v_addc_co_u32_e32 v45, vcc, 0, v91, vcc
	global_store_dwordx2 v[44:45], v[46:47], off sc1
.LBB0_216:
	v_mov_b32_e32 v95, v94
	v_mov_b32_e32 v44, v94
	v_mov_b32_e32 v45, v94
	v_pk_mul_f32 v[42:43], v[42:43], v[44:45]
	v_pk_mul_f32 v[44:45], v[40:41], v[94:95]
	v_pk_fma_f32 v[40:41], v[74:75], v[42:43], v[6:7]
	v_pk_fma_f32 v[42:43], v[76:77], v[44:45], v[4:5]
	s_and_b64 vcc, exec, s[6:7]
	s_mov_b64 s[12:13], -1
	s_cbranch_vccnz .LBB0_218
	v_med3_f32 v44, v42, s55, v228
	v_med3_f32 v45, v43, s55, v228
	v_mov_b32_e32 v46, v65
	v_cvt_pk_fp8_f32 v46, v44, v45
	v_med3_f32 v44, v40, s55, v228
	v_med3_f32 v45, v41, s55, v228
	s_mov_b64 s[12:13], 0
	v_cvt_pk_fp8_f32 v46, v44, v45 op_sel:[0,0,1]
	v_add_co_u32_e32 v44, vcc, 0x6800000, v92
	s_nop 1
	v_addc_co_u32_e32 v45, vcc, 0, v93, vcc
	global_store_dword v[44:45], v46, off offset:256 sc1
.LBB0_218:
	s_andn2_b64 vcc, exec, s[12:13]
	s_cbranch_vccnz .LBB0_220
	v_cvt_pk_bf16_f32 v42, v42, v43
	v_cvt_pk_bf16_f32 v43, v40, v41
	v_add_co_u32_e32 v40, vcc, 0x6800000, v90
	s_nop 1
	v_addc_co_u32_e32 v41, vcc, 0, v91, vcc
	global_store_dwordx2 v[40:41], v[42:43], off offset:512 sc1
.LBB0_220:
	v_mov_b32_e32 v40, v94
	v_mov_b32_e32 v41, v94
	v_pk_mul_f32 v[38:39], v[38:39], v[40:41]
	v_pk_mul_f32 v[40:41], v[36:37], v[94:95]
	v_pk_fma_f32 v[36:37], v[70:71], v[38:39], v[10:11]
	v_pk_fma_f32 v[38:39], v[72:73], v[40:41], v[8:9]
	s_and_b64 vcc, exec, s[6:7]
	s_mov_b64 s[12:13], -1
	s_cbranch_vccnz .LBB0_222
	v_med3_f32 v40, v38, s55, v228
	v_med3_f32 v41, v39, s55, v228
	v_mov_b32_e32 v42, v65
	v_cvt_pk_fp8_f32 v42, v40, v41
	v_med3_f32 v40, v36, s55, v228
	v_med3_f32 v41, v37, s55, v228
	s_mov_b64 s[12:13], 0
	v_cvt_pk_fp8_f32 v42, v40, v41 op_sel:[0,0,1]
	v_add_co_u32_e32 v40, vcc, 0x6800000, v92
	s_nop 1
	v_addc_co_u32_e32 v41, vcc, 0, v93, vcc
	global_store_dword v[40:41], v42, off offset:512 sc1
.LBB0_222:
	s_andn2_b64 vcc, exec, s[12:13]
	s_cbranch_vccnz .LBB0_224
	v_cvt_pk_bf16_f32 v38, v38, v39
	v_cvt_pk_bf16_f32 v39, v36, v37
	v_add_co_u32_e32 v36, vcc, 0x6800000, v90
	s_nop 1
	v_addc_co_u32_e32 v37, vcc, 0, v91, vcc
	global_store_dwordx2 v[36:37], v[38:39], off offset:1024 sc1

.LBB0_227:
	v_cvt_pk_f32_fp8_e32 v[34:35], v105
	v_cvt_pk_f32_fp8_sdwa v[32:33], v105 src0_sel:WORD_1
	v_cvt_pk_f32_fp8_e32 v[36:37], v108
	v_cvt_pk_f32_fp8_sdwa v[38:39], v108 src0_sel:WORD_1
	v_pk_mul_f32 v[34:35], s[10:11], v[34:35] op_sel:[1,0]
	v_pk_mul_f32 v[32:33], s[10:11], v[32:33] op_sel:[1,0]
	v_pk_fma_f32 v[34:35], s[8:9], v[36:37], v[34:35] op_sel:[1,0,0]
	v_pk_fma_f32 v[32:33], s[8:9], v[38:39], v[32:33] op_sel:[1,0,0]
	v_pk_fma_f32 v[28:29], v[50:51], v[34:35], v[28:29]
	v_cvt_pk_f32_fp8_e32 v[34:35], v106
	v_pk_fma_f32 v[30:31], v[52:53], v[32:33], v[30:31]
	v_cvt_pk_f32_fp8_sdwa v[32:33], v106 src0_sel:WORD_1
	v_cvt_pk_f32_fp8_e32 v[36:37], v109
	v_cvt_pk_f32_fp8_sdwa v[38:39], v109 src0_sel:WORD_1
	v_pk_mul_f32 v[34:35], s[10:11], v[34:35] op_sel:[1,0]
	v_pk_mul_f32 v[32:33], s[10:11], v[32:33] op_sel:[1,0]
	v_pk_fma_f32 v[34:35], s[8:9], v[36:37], v[34:35] op_sel:[1,0,0]
	v_pk_fma_f32 v[32:33], s[8:9], v[38:39], v[32:33] op_sel:[1,0,0]
	v_pk_fma_f32 v[24:25], v[48:49], v[34:35], v[24:25]
	v_cvt_pk_f32_fp8_e32 v[34:35], v107
	v_pk_fma_f32 v[26:27], v[54:55], v[32:33], v[26:27]
	v_cvt_pk_f32_fp8_sdwa v[32:33], v107 src0_sel:WORD_1
	v_cvt_pk_f32_fp8_e32 v[36:37], v110
	v_cvt_pk_f32_fp8_sdwa v[38:39], v110 src0_sel:WORD_1
	v_pk_mul_f32 v[34:35], s[10:11], v[34:35] op_sel:[1,0]
	v_pk_mul_f32 v[32:33], s[10:11], v[32:33] op_sel:[1,0]
	v_pk_fma_f32 v[34:35], s[8:9], v[36:37], v[34:35] op_sel:[1,0,0]
	v_pk_fma_f32 v[32:33], s[8:9], v[38:39], v[32:33] op_sel:[1,0,0]
	v_pk_fma_f32 v[20:21], v[58:59], v[34:35], v[20:21]
	v_cvt_pk_f32_fp8_e32 v[34:35], v111
	v_pk_fma_f32 v[22:23], v[60:61], v[32:33], v[22:23]
	v_cvt_pk_f32_fp8_sdwa v[32:33], v111 src0_sel:WORD_1
	v_cvt_pk_f32_fp8_e32 v[36:37], v112
	v_cvt_pk_f32_fp8_sdwa v[38:39], v112 src0_sel:WORD_1
	v_pk_mul_f32 v[34:35], s[10:11], v[34:35] op_sel:[1,0]
	v_pk_mul_f32 v[32:33], s[10:11], v[32:33] op_sel:[1,0]
	v_pk_fma_f32 v[34:35], s[8:9], v[36:37], v[34:35] op_sel:[1,0,0]
	v_pk_fma_f32 v[32:33], s[8:9], v[38:39], v[32:33] op_sel:[1,0,0]
	v_pk_fma_f32 v[16:17], v[56:57], v[34:35], v[16:17]
	v_add_co_u32_e32 v34, vcc, s74, v90
	v_pk_fma_f32 v[18:19], v[62:63], v[32:33], v[18:19]
	v_cvt_pk_f16_f32 v33, v30, v31
	v_cvt_pk_f16_f32 v32, v28, v29
	v_addc_co_u32_e32 v35, vcc, 0, v91, vcc
	global_store_dwordx2 v[34:35], v[32:33], off offset:2048 nt sc1
	v_cvt_pk_f16_f32 v33, v26, v27
	v_cvt_pk_f16_f32 v32, v24, v25
	global_store_dwordx2 v[34:35], v[32:33], off offset:2560 nt sc1
	v_cvt_pk_f16_f32 v33, v22, v23
	v_cvt_pk_f16_f32 v32, v20, v21
	global_store_dwordx2 v[34:35], v[32:33], off offset:3072 nt sc1
	v_cvt_pk_f16_f32 v33, v18, v19
	v_cvt_pk_f16_f32 v32, v16, v17
	global_store_dwordx2 v[34:35], v[32:33], off offset:3584 nt sc1
.LBB0_228:
	v_pk_mul_f32 v[32:33], v[30:31], v[30:31]
	v_pk_mul_f32 v[34:35], v[28:29], v[28:29]
	s_and_b64 vcc, exec, s[6:7]
	v_pk_mov_b32 v[36:37], v[34:35], v[32:33] op_sel:[1,0]
	v_mov_b32_e32 v35, v33
	v_pk_add_f32 v[32:33], v[36:37], v[34:35]
	v_pk_mul_f32 v[34:35], v[26:27], v[26:27]
	v_pk_add_f32 v[32:33], v[32:33], v[32:33] op_sel_hi:[0,1]
	v_pk_mul_f32 v[36:37], v[24:25], v[24:25]
	v_mul_f32_e32 v32, v20, v20
	v_pk_mov_b32 v[38:39], v[36:37], v[34:35] op_sel:[1,0]
	v_mov_b32_e32 v37, v35
	v_pk_add_f32 v[34:35], v[38:39], v[36:37]
	v_pk_fma_f32 v[36:37], v[20:21], v[20:21], v[32:33] op_sel_hi:[1,1,0]
	v_mul_f32_e32 v32, v22, v22
	v_pk_add_f32 v[34:35], v[34:35], v[34:35] op_sel_hi:[0,1]
	v_pk_fma_f32 v[38:39], v[22:23], v[22:23], v[32:33] op_sel_hi:[1,1,0]
	v_mul_f32_e32 v36, v16, v16
	v_mul_f32_e32 v38, v17, v17
	v_mul_f32_e32 v34, v18, v18
	v_mul_f32_e32 v32, v19, v19
	v_pk_add_f32 v[36:37], v[36:37], v[38:39]
	v_pk_add_f32 v[32:33], v[34:35], v[32:33]
	s_nop 0
	v_pk_add_f32 v[32:33], v[36:37], v[32:33]
	s_nop 0
	v_add_f32_e32 v32, v32, v33
	s_nop 1
	v_add_f32_dpp v32, v32, v32 quad_perm:[1,0,3,2] row_mask:0xf bank_mask:0xf bound_ctrl:1
	s_nop 1
	v_add_f32_dpp v32, v32, v32 quad_perm:[2,3,0,1] row_mask:0xf bank_mask:0xf bound_ctrl:1
	s_nop 1
	v_add_f32_dpp v32, v32, v32 row_half_mirror row_mask:0xf bank_mask:0xf bound_ctrl:1
	s_nop 1
	v_add_f32_dpp v32, v32, v32 row_mirror row_mask:0xf bank_mask:0xf bound_ctrl:1
	s_nop 0
	v_readlane_b32 s14, v32, 16
	v_readlane_b32 s15, v32, 48
	v_readlane_b32 s12, v32, 0
	v_readlane_b32 s13, v32, 32
	v_mov_b32_e32 v32, s14
	v_mov_b32_e32 v33, s15
	v_pk_add_f32 v[32:33], s[12:13], v[32:33]
	s_mov_b64 s[12:13], -1
	v_add_f32_e32 v32, v32, v33
	v_fmamk_f32 v32, v32, 0x3a800000, v229
	v_rsq_f32_e32 v32, v32
	s_nop 0
	v_pk_mul_f32 v[34:35], v[28:29], v[32:33] op_sel_hi:[1,0]
	v_pk_mul_f32 v[28:29], v[30:31], v[32:33] op_sel_hi:[1,0]
	v_pk_fma_f32 v[30:31], v[80:81], v[34:35], v[0:1]
	v_pk_fma_f32 v[28:29], v[78:79], v[28:29], v[2:3]
	s_cbranch_vccnz .LBB0_230
	v_med3_f32 v33, v30, s55, v228
	v_med3_f32 v34, v31, s55, v228
	v_mov_b32_e32 v36, v65
	v_cvt_pk_fp8_f32 v36, v33, v34
	v_med3_f32 v33, v28, s55, v228
	v_med3_f32 v34, v29, s55, v228
	s_mov_b64 s[12:13], 0
	v_cvt_pk_fp8_f32 v36, v33, v34 op_sel:[0,0,1]
	v_add_co_u32_e32 v34, vcc, 0x6800000, v92
	s_nop 1
	v_addc_co_u32_e32 v35, vcc, 0, v93, vcc
	global_store_dword v[34:35], v36, off offset:1024 sc1
.LBB0_230:
	s_andn2_b64 vcc, exec, s[12:13]
	s_cbranch_vccnz .LBB0_232
	v_cvt_pk_bf16_f32 v30, v30, v31
	v_cvt_pk_bf16_f32 v31, v28, v29
	v_add_co_u32_e32 v28, vcc, 0x6800000, v90
	s_nop 1
	v_addc_co_u32_e32 v29, vcc, 0, v91, vcc
	global_store_dwordx2 v[28:29], v[30:31], off offset:2048 sc1
.LBB0_232:
	v_mov_b32_e32 v33, v32
	v_mov_b32_e32 v28, v32
	v_mov_b32_e32 v29, v32
	v_pk_mul_f32 v[26:27], v[26:27], v[28:29]
	v_pk_mul_f32 v[28:29], v[24:25], v[32:33]
	v_pk_fma_f32 v[24:25], v[74:75], v[26:27], v[6:7]
	v_pk_fma_f32 v[26:27], v[76:77], v[28:29], v[4:5]
	s_and_b64 vcc, exec, s[6:7]
	s_mov_b64 s[12:13], -1
	s_cbranch_vccnz .LBB0_234
	v_med3_f32 v28, v26, s55, v228
	v_med3_f32 v29, v27, s55, v228
	v_mov_b32_e32 v30, v65
	v_cvt_pk_fp8_f32 v30, v28, v29
	v_med3_f32 v28, v24, s55, v228
	v_med3_f32 v29, v25, s55, v228
	s_mov_b64 s[12:13], 0
	v_cvt_pk_fp8_f32 v30, v28, v29 op_sel:[0,0,1]
	v_add_co_u32_e32 v28, vcc, 0x6800000, v92
	s_nop 1
	v_addc_co_u32_e32 v29, vcc, 0, v93, vcc
	global_store_dword v[28:29], v30, off offset:1280 sc1
.LBB0_234:
	s_andn2_b64 vcc, exec, s[12:13]
	s_cbranch_vccnz .LBB0_236
	v_cvt_pk_bf16_f32 v26, v26, v27
	v_cvt_pk_bf16_f32 v27, v24, v25
	v_add_co_u32_e32 v24, vcc, 0x6800000, v90
	s_nop 1
	v_addc_co_u32_e32 v25, vcc, 0, v91, vcc
	global_store_dwordx2 v[24:25], v[26:27], off offset:2560 sc1
.LBB0_236:
	v_mov_b32_e32 v24, v32
	v_mov_b32_e32 v25, v32
	v_pk_mul_f32 v[22:23], v[22:23], v[24:25]
	v_pk_mul_f32 v[24:25], v[20:21], v[32:33]
	v_pk_fma_f32 v[20:21], v[70:71], v[22:23], v[10:11]
	v_pk_fma_f32 v[22:23], v[72:73], v[24:25], v[8:9]
	s_and_b64 vcc, exec, s[6:7]
	s_mov_b64 s[12:13], -1
	s_cbranch_vccnz .LBB0_238
	v_med3_f32 v24, v22, s55, v228
	v_med3_f32 v25, v23, s55, v228
	v_mov_b32_e32 v26, v65
	v_cvt_pk_fp8_f32 v26, v24, v25
	v_med3_f32 v24, v20, s55, v228
	v_med3_f32 v25, v21, s55, v228
	s_mov_b64 s[12:13], 0
	v_cvt_pk_fp8_f32 v26, v24, v25 op_sel:[0,0,1]
	v_add_co_u32_e32 v24, vcc, 0x6800000, v92
	s_nop 1
	v_addc_co_u32_e32 v25, vcc, 0, v93, vcc
	global_store_dword v[24:25], v26, off offset:1536 sc1
.LBB0_238:
	s_andn2_b64 vcc, exec, s[12:13]
	s_cbranch_vccnz .LBB0_240
	v_cvt_pk_bf16_f32 v22, v22, v23
	v_cvt_pk_bf16_f32 v23, v20, v21
	v_add_co_u32_e32 v20, vcc, 0x6800000, v90
	s_nop 1
	v_addc_co_u32_e32 v21, vcc, 0, v91, vcc
	global_store_dwordx2 v[20:21], v[22:23], off offset:3072 sc1
.LBB0_240:
	v_mov_b32_e32 v20, v32
	v_mov_b32_e32 v21, v32
	v_pk_mul_f32 v[18:19], v[18:19], v[20:21]
	v_pk_mul_f32 v[20:21], v[16:17], v[32:33]
	v_pk_fma_f32 v[16:17], v[66:67], v[18:19], v[14:15]
	v_pk_fma_f32 v[18:19], v[68:69], v[20:21], v[12:13]
	s_and_b64 vcc, exec, s[6:7]
	s_mov_b64 s[6:7], -1
	s_cbranch_vccnz .LBB0_242
	v_med3_f32 v20, v18, s55, v228
	v_med3_f32 v21, v19, s55, v228
	v_mov_b32_e32 v22, v65
	v_cvt_pk_fp8_f32 v22, v20, v21
	v_med3_f32 v20, v16, s55, v228
	v_med3_f32 v21, v17, s55, v228
	s_mov_b64 s[6:7], 0
	v_cvt_pk_fp8_f32 v22, v20, v21 op_sel:[0,0,1]
	v_add_co_u32_e32 v20, vcc, 0x6800000, v92
	s_nop 1
	v_addc_co_u32_e32 v21, vcc, 0, v93, vcc
	global_store_dword v[20:21], v22, off offset:1792 sc1
.LBB0_242:
	s_andn2_b64 vcc, exec, s[6:7]
	s_cbranch_vccnz .LBB0_203
	v_cvt_pk_bf16_f32 v18, v18, v19
	v_cvt_pk_bf16_f32 v19, v16, v17
	v_add_co_u32_e32 v16, vcc, 0x6800000, v90
	s_nop 1
	v_addc_co_u32_e32 v17, vcc, 0, v91, vcc
	global_store_dwordx2 v[16:17], v[18:19], off offset:3584 sc1
	s_branch .LBB0_203
.LBB0_244:
	v_med3_f32 v36, v34, s55, v228
	v_med3_f32 v37, v35, s55, v228
	v_mov_b32_e32 v38, v65
	v_cvt_pk_fp8_f32 v38, v36, v37
	v_med3_f32 v36, v32, s55, v228
	v_med3_f32 v37, v33, s55, v228
	v_cvt_pk_fp8_f32 v38, v36, v37 op_sel:[0,0,1]
	v_add_co_u32_e32 v36, vcc, 0x6800000, v92
	s_nop 1
	v_addc_co_u32_e32 v37, vcc, 0, v93, vcc
	global_store_dword v[36:37], v38, off offset:768 sc1
	s_cbranch_execnz .LBB0_226
.LBB0_245:
	v_cvt_pk_bf16_f32 v34, v34, v35
	v_cvt_pk_bf16_f32 v35, v32, v33
	v_add_co_u32_e32 v32, vcc, 0x6800000, v90
	s_nop 1
	v_addc_co_u32_e32 v33, vcc, 0, v91, vcc
	global_store_dwordx2 v[32:33], v[34:35], off offset:1536 sc1
	s_and_b64 vcc, exec, s[4:5]
	s_cbranch_vccz .LBB0_227
	s_branch .LBB0_228

.LBB0_414:
	v_add3_u32 v64, s23, v173, v171
	ds_read_b64_tr_b16 v[90:91], v64 offset:36864
	s_nop 1
	ds_read_b64_tr_b16 v[86:87], v64 offset:36896
	ds_read_b64_tr_b16 v[100:101], v64 offset:36928
	ds_read_b64_tr_b16 v[108:109], v64 offset:36960
	ds_read_b64_tr_b16 v[92:93], v64 offset:39168
	ds_read_b64_tr_b16 v[88:89], v64 offset:39200
	ds_read_b64_tr_b16 v[102:103], v64 offset:39232
	ds_read_b64_tr_b16 v[110:111], v64 offset:39264
	ds_read_b64_tr_b16 v[104:105], v64 offset:41472
	ds_read_b64_tr_b16 v[112:113], v64 offset:41504
	ds_read_b64_tr_b16 v[118:119], v64 offset:41536
	ds_read_b64_tr_b16 v[126:127], v64 offset:41568
	ds_read_b64_tr_b16 v[106:107], v64 offset:43776
	ds_read_b64_tr_b16 v[114:115], v64 offset:43808
	ds_read_b64_tr_b16 v[120:121], v64 offset:43840
	ds_read_b64_tr_b16 v[128:129], v64 offset:43872
	ds_read_b64_tr_b16 v[122:123], v64 offset:46080
	ds_read_b64_tr_b16 v[130:131], v64 offset:46112
	ds_read_b64_tr_b16 v[138:139], v64 offset:46144
	ds_read_b64_tr_b16 v[146:147], v64 offset:46176
	ds_read_b64_tr_b16 v[124:125], v64 offset:48384
	ds_read_b64_tr_b16 v[132:133], v64 offset:48416
	ds_read_b64_tr_b16 v[140:141], v64 offset:48448
	ds_read_b64_tr_b16 v[148:149], v64 offset:48480
	ds_read_b64_tr_b16 v[142:143], v64 offset:50688
	ds_read_b64_tr_b16 v[152:153], v64 offset:50720
	ds_read_b64_tr_b16 v[156:157], v64 offset:50752
	ds_read_b64_tr_b16 v[134:135], v64 offset:50784
	ds_read_b64_tr_b16 v[144:145], v64 offset:52992
	ds_read_b64_tr_b16 v[154:155], v64 offset:53024
	ds_read_b64_tr_b16 v[158:159], v64 offset:53056
	ds_read_b64_tr_b16 v[136:137], v64 offset:53088
	ds_read_b64_tr_b16 v[150:151], v64 offset:55296
	ds_read_b64_tr_b16 v[116:117], v64 offset:55328
	ds_read_b64_tr_b16 v[98:99], v64 offset:55360
	ds_read_b64_tr_b16 v[94:95], v64 offset:55392
	v_max3_f32 v64, v82, s84, v83
	v_max3_f32 v64, v64, v84, v85
	v_max3_f32 v64, v64, v78, v79
	v_max3_f32 v64, v64, v80, v81
	v_max3_f32 v64, v64, v74, v75
	v_max3_f32 v64, v64, v76, v77
	v_max3_f32 v64, v64, v70, v71
	v_max3_f32 v64, v64, v72, v73
	v_max3_f32 v64, v64, v66, v67
	v_max3_f32 v64, v64, v68, v69
	v_max3_f32 v64, v64, v60, v61
	v_max3_f32 v64, v64, v62, v63
	v_max3_f32 v64, v64, v56, v57
	v_max3_f32 v64, v64, v58, v59
	v_max3_f32 v64, v64, v52, v53
	v_max3_f32 v64, v64, v54, v55
	v_max3_f32 v64, v64, v48, v49
	v_max3_f32 v64, v64, v50, v51
	v_mov_b32_e32 v96, v64
	s_nop 1
	v_permlane16_swap_b32_e32 v64, v96
	v_max_f32_e32 v96, v96, v96
	v_max_f32_e32 v64, v64, v64
	v_max_f32_e32 v64, v64, v96
	v_mov_b32_e32 v96, v64
	s_nop 1
	v_permlane32_swap_b32_e32 v64, v96
	v_max_f32_e32 v96, v96, v96
	v_max_f32_e32 v64, v64, v64
	v_max_f32_e32 v170, v64, v96
	v_pk_add_f32 v[82:83], v[82:83], v[170:171] op_sel_hi:[1,0] neg_lo:[0,1] neg_hi:[0,1]
	v_pk_add_f32 v[84:85], v[84:85], v[170:171] op_sel_hi:[1,0] neg_lo:[0,1] neg_hi:[0,1]
	v_exp_f32_e32 v82, v82
	v_exp_f32_e32 v83, v83
	v_exp_f32_e32 v84, v84
	v_exp_f32_e32 v85, v85
	v_pk_add_f32 v[78:79], v[78:79], v[170:171] op_sel_hi:[1,0] neg_lo:[0,1] neg_hi:[0,1]
	v_pk_add_f32 v[80:81], v[80:81], v[170:171] op_sel_hi:[1,0] neg_lo:[0,1] neg_hi:[0,1]
	v_exp_f32_e32 v78, v78
	v_exp_f32_e32 v79, v79
	v_exp_f32_e32 v80, v80
	v_exp_f32_e32 v81, v81
	v_pk_add_f32 v[74:75], v[74:75], v[170:171] op_sel_hi:[1,0] neg_lo:[0,1] neg_hi:[0,1]
	v_pk_add_f32 v[96:97], v[82:83], 0 op_sel_hi:[1,0]
	v_pk_add_f32 v[76:77], v[76:77], v[170:171] op_sel_hi:[1,0] neg_lo:[0,1] neg_hi:[0,1]
	v_exp_f32_e32 v192, v74
	v_exp_f32_e32 v193, v75
	v_pk_add_f32 v[96:97], v[84:85], v[96:97]
	v_exp_f32_e32 v194, v76
	v_exp_f32_e32 v195, v77
	v_pk_add_f32 v[70:71], v[70:71], v[170:171] op_sel_hi:[1,0] neg_lo:[0,1] neg_hi:[0,1]
	v_pk_add_f32 v[74:75], v[78:79], v[96:97]
	v_pk_add_f32 v[72:73], v[72:73], v[170:171] op_sel_hi:[1,0] neg_lo:[0,1] neg_hi:[0,1]
	v_exp_f32_e32 v96, v70
	v_exp_f32_e32 v97, v71
	v_pk_add_f32 v[74:75], v[80:81], v[74:75]
	v_exp_f32_e32 v196, v72
	v_exp_f32_e32 v197, v73
	v_pk_add_f32 v[66:67], v[66:67], v[170:171] op_sel_hi:[1,0] neg_lo:[0,1] neg_hi:[0,1]
	v_pk_add_f32 v[74:75], v[192:193], v[74:75]
	v_pk_add_f32 v[68:69], v[68:69], v[170:171] op_sel_hi:[1,0] neg_lo:[0,1] neg_hi:[0,1]
	v_exp_f32_e32 v198, v66
	v_exp_f32_e32 v199, v67
	v_pk_add_f32 v[74:75], v[194:195], v[74:75]
	v_exp_f32_e32 v200, v68
	v_exp_f32_e32 v201, v69
	v_pk_add_f32 v[66:67], v[96:97], v[74:75]
	v_cvt_pk_bf16_f32 v68, v78, v79
	v_pk_add_f32 v[66:67], v[196:197], v[66:67]
	v_cvt_pk_bf16_f32 v69, v80, v81
	v_pk_add_f32 v[66:67], v[198:199], v[66:67]
	v_pk_add_f32 v[74:75], v[60:61], v[170:171] op_sel_hi:[1,0] neg_lo:[0,1] neg_hi:[0,1]
	v_pk_add_f32 v[202:203], v[200:201], v[66:67]
	v_cvt_pk_bf16_f32 v66, v82, v83
	v_cvt_pk_bf16_f32 v67, v84, v85
	v_pk_add_f32 v[76:77], v[62:63], v[170:171] op_sel_hi:[1,0] neg_lo:[0,1] neg_hi:[0,1]
	v_exp_f32_e32 v78, v74
	s_waitcnt lgkmcnt(14)
	v_mfma_f32_16x16x32_bf16 v[70:73], v[90:93], v[66:69], 0
	v_exp_f32_e32 v79, v75
	v_exp_f32_e32 v80, v76
	v_exp_f32_e32 v81, v77
	v_mfma_f32_16x16x32_bf16 v[60:63], v[86:89], v[66:69], 0
	v_add_f32_e64 v84, v56, -v170
	v_add_f32_e64 v85, v57, -v170
	v_pk_add_f32 v[86:87], v[58:59], v[170:171] op_sel_hi:[1,0] neg_lo:[0,1] neg_hi:[0,1]
	v_exp_f32_e32 v84, v84
	v_mfma_f32_16x16x32_bf16 v[74:77], v[100:103], v[66:69], 0
	v_exp_f32_e32 v85, v85
	v_exp_f32_e32 v86, v86
	v_exp_f32_e32 v87, v87
	v_mfma_f32_16x16x32_bf16 v[56:59], v[108:111], v[66:69], 0
	v_cvt_pk_bf16_f32 v66, v192, v193
	v_cvt_pk_bf16_f32 v67, v194, v195
	v_cvt_pk_bf16_f32 v68, v96, v97
	v_cvt_pk_bf16_f32 v69, v196, v197
	v_pk_add_f32 v[88:89], v[52:53], v[170:171] op_sel_hi:[1,0] neg_lo:[0,1] neg_hi:[0,1]
	v_pk_add_f32 v[82:83], v[78:79], v[202:203]
	v_mfma_f32_16x16x32_bf16 v[70:73], v[104:107], v[66:69], v[70:73]
	v_add_f32_e64 v90, v54, -v170
	v_add_f32_e64 v91, v55, -v170
	v_pk_add_f32 v[82:83], v[80:81], v[82:83]
	v_pk_add_f32 v[48:49], v[48:49], v[170:171] op_sel_hi:[1,0] neg_lo:[0,1] neg_hi:[0,1]
	v_mfma_f32_16x16x32_bf16 v[60:63], v[112:115], v[66:69], v[60:63]
	v_add_f32_e64 v82, v84, v82
	v_add_f32_e64 v83, v85, v83
	s_waitcnt lgkmcnt(1)
	v_mov_b32_e32 v100, v98
	v_pk_add_f32 v[82:83], v[86:87], v[82:83]
	v_mfma_f32_16x16x32_bf16 v[74:77], v[118:121], v[66:69], v[74:77]
	v_mov_b32_e32 v118, v116
	v_mov_b32_e32 v119, v117
	v_mov_b32_e32 v101, v99
	v_mfma_f32_16x16x32_bf16 v[52:55], v[126:129], v[66:69], v[56:59]
	s_waitcnt lgkmcnt(0)
	v_mov_b32_e32 v96, v94
	v_mov_b32_e32 v97, v95
	v_mov_b32_e32 v64, v65
	v_cvt_pk_bf16_f32 v58, v78, v79
	v_exp_f32_e32 v78, v88
	v_exp_f32_e32 v79, v89
	v_cvt_pk_bf16_f32 v56, v198, v199
	v_cvt_pk_bf16_f32 v57, v200, v201
	v_cvt_pk_bf16_f32 v59, v80, v81
	v_exp_f32_e32 v80, v90
	v_exp_f32_e32 v81, v91
	v_mfma_f32_16x16x32_bf16 v[66:69], v[122:125], v[56:59], v[70:73]
	v_add_f32_e64 v82, v78, v82
	v_add_f32_e64 v83, v79, v83
	s_cmp_eq_u32 s30, 1
	s_mov_b32 s23, 0xe800000
	v_mfma_f32_16x16x32_bf16 v[60:63], v[130:133], v[56:59], v[60:63]
	s_cselect_b32 s23, s23, 0x2e800000
	s_cmp_lg_u32 s30, 0
	s_cselect_b32 s23, s23, 0x12800000
	v_mfma_f32_16x16x32_bf16 v[70:73], v[138:141], v[56:59], v[74:77]
	s_add_u32 s36, s42, s23
	s_addc_u32 s37, s43, 0
	s_lshl_b32 s66, s22, 6
	v_pk_add_f32 v[74:75], v[50:51], v[170:171] op_sel_hi:[1,0] neg_lo:[0,1] neg_hi:[0,1]
	v_exp_f32_e32 v76, v48
	v_exp_f32_e32 v77, v49
	v_exp_f32_e32 v74, v74
	v_exp_f32_e32 v75, v75
	v_mfma_f32_16x16x32_bf16 v[48:51], v[146:149], v[56:59], v[52:55]
	s_nop 2
	v_cvt_pk_bf16_f32 v52, v84, v85
	v_cvt_pk_bf16_f32 v53, v86, v87
	v_cvt_pk_bf16_f32 v54, v78, v79
	v_cvt_pk_bf16_f32 v55, v80, v81
	v_pk_add_f32 v[78:79], v[80:81], v[82:83]
	s_nop 0
	v_mfma_f32_16x16x32_bf16 v[56:59], v[142:145], v[52:55], v[66:69]
	v_mfma_f32_16x16x32_bf16 v[66:69], v[152:155], v[52:55], v[60:63]
	v_mov_b32_e32 v152, v150
	v_mov_b32_e32 v153, v151
	s_nop 0
	v_pk_add_f32 v[60:61], v[76:77], v[78:79]
	v_mfma_f32_16x16x32_bf16 v[70:73], v[156:159], v[52:55], v[70:73]
	v_add_f32_e64 v60, v74, v60
	v_add_f32_e64 v61, v75, v61
	v_cvt_pk_bf16_f32 v62, v76, v77
	v_pk_add_f32 v[60:61], v[60:61], v[60:61] op_sel:[0,1] op_sel_hi:[1,0]
	v_mfma_f32_16x16x32_bf16 v[48:51], v[134:137], v[52:55], v[48:51]
	v_mov_b32_e32 v61, v60
	s_nop 1
	v_permlane16_swap_b32_e32 v60, v61
	v_cvt_pk_bf16_f32 v63, v74, v75
	v_add_f32_e32 v74, v60, v61
	s_nop 0
	v_mfma_f32_16x16x32_bf16 v[52:55], v[150:153], v[62:65], v[56:59]
	v_mfma_f32_16x16x32_bf16 v[56:59], v[116:119], v[62:65], v[66:69]
	v_mfma_f32_16x16x32_bf16 v[66:69], v[98:101], v[62:65], v[70:73]
	s_nop 2
	v_mov_b32_e32 v70, v74
	s_nop 1
	v_permlane32_swap_b32_e32 v74, v70
	v_mfma_f32_16x16x32_bf16 v[60:63], v[94:97], v[62:65], v[48:51]
	s_nop 2
	v_add_f32_e32 v48, v74, v70
	v_rcp_f32_e32 v49, v48
	s_nop 0
	v_mul_f32_e32 v49, 0x42800000, v49
	v_mul_f32_e32 v50, v49, v52
	v_mul_f32_e32 v51, v49, v53
	v_med3_f32 v53, v50, s55, v228
	v_med3_f32 v51, v51, s55, v228
	v_mov_b32_e32 v50, v65
	v_cvt_pk_fp8_f32 v50, v53, v51
	v_mul_f32_e32 v52, v49, v54
	v_mul_f32_e32 v51, v49, v55
	v_med3_f32 v52, v52, s55, v228
	v_med3_f32 v51, v51, s55, v228
	v_cvt_pk_fp8_f32 v50, v52, v51 op_sel:[0,0,1]
	v_mul_f32_e32 v51, v49, v56
	v_mul_f32_e32 v52, v49, v57
	v_med3_f32 v54, v51, s55, v228
	v_med3_f32 v52, v52, s55, v228
	v_mov_b32_e32 v51, v65
	v_cvt_pk_fp8_f32 v51, v54, v52
	v_mul_f32_e32 v53, v49, v58
	v_mul_f32_e32 v52, v49, v59
	v_med3_f32 v53, v53, s55, v228
	v_med3_f32 v52, v52, s55, v228
	v_cvt_pk_fp8_f32 v51, v53, v52 op_sel:[0,0,1]
	v_mul_f32_e32 v52, v49, v66
	v_mul_f32_e32 v53, v49, v67
	v_med3_f32 v55, v52, s55, v228
	v_med3_f32 v53, v53, s55, v228
	v_mov_b32_e32 v52, v65
	v_cvt_pk_fp8_f32 v52, v55, v53
	v_mul_f32_e32 v54, v49, v68
	v_mul_f32_e32 v53, v49, v69
	v_med3_f32 v54, v54, s55, v228
	v_med3_f32 v53, v53, s55, v228
	v_cvt_pk_fp8_f32 v52, v54, v53 op_sel:[0,0,1]
	v_mul_f32_e32 v53, v49, v60
	v_mul_f32_e32 v54, v49, v61
	v_med3_f32 v56, v53, s55, v228
	v_med3_f32 v54, v54, s55, v228
	v_mov_b32_e32 v53, v65
	v_cvt_pk_fp8_f32 v53, v56, v54
	v_mul_f32_e32 v55, v49, v62
	v_mul_f32_e32 v49, v49, v63
	v_med3_f32 v54, v55, s55, v228
	v_med3_f32 v49, v49, s55, v228
	v_cvt_pk_fp8_f32 v53, v54, v49 op_sel:[0,0,1]
	v_lshlrev_b64 v[54:55], 10, v[166:167]
	v_lshl_add_u64 v[54:55], s[36:37], 0, v[54:55]
	v_lshl_add_u64 v[54:55], v[54:55], 0, s[66:67]
	v_lshl_add_u64 v[54:55], v[54:55], 0, v[160:161]
	global_store_dwordx4 v[54:55], v[50:53], off sc1
	s_and_saveexec_b64 s[36:37], vcc
	s_cbranch_execz .LBB0_416
	v_log_f32_e32 v48, v48
	s_ashr_i32 s31, s30, 31
	s_lshl_b64 s[30:31], s[30:31], 22
	v_readlane_b32 s23, v254, 30
	s_add_u32 s30, s23, s30
	v_readlane_b32 s23, v254, 31
	v_add_f32_e32 v48, v170, v48
	s_addc_u32 s31, s23, s31
	v_mul_f32_e32 v50, 0x3f317218, v48
	v_lshlrev_b64 v[48:49], 6, v[166:167]
	v_lshl_add_u64 v[48:49], s[30:31], 0, v[48:49]
	s_mov_b32 s23, s67
	v_lshl_add_u64 v[48:49], s[22:23], 2, v[48:49]
	global_store_dword v[48:49], v50, off sc1

.LBB0_420:
	v_readlane_b32 s6, v255, 3
	s_mov_b32 s63, s71
	s_nop 0
	v_add3_u32 v10, s6, v173, v171
	v_add3_u32 v12, s6, v171, v173
	ds_read_b64_tr_b16 v[44:45], v10
	ds_read_b64_tr_b16 v[8:9], v10 offset:32
	ds_read_b64_tr_b16 v[50:51], v10 offset:64
	ds_read_b64_tr_b16 v[58:59], v10 offset:96
	ds_read_b64_tr_b16 v[46:47], v12 offset:2304
	ds_read_b64_tr_b16 v[10:11], v12 offset:2336
	ds_read_b64_tr_b16 v[52:53], v12 offset:2368
	ds_read_b64_tr_b16 v[60:61], v12 offset:2400
	ds_read_b64_tr_b16 v[54:55], v12 offset:4608
	ds_read_b64_tr_b16 v[66:67], v12 offset:4640
	ds_read_b64_tr_b16 v[70:71], v12 offset:4672
	ds_read_b64_tr_b16 v[78:79], v12 offset:4704
	ds_read_b64_tr_b16 v[56:57], v12 offset:6912
	ds_read_b64_tr_b16 v[68:69], v12 offset:6944
	ds_read_b64_tr_b16 v[72:73], v12 offset:6976
	ds_read_b64_tr_b16 v[80:81], v12 offset:7008
	ds_read_b64_tr_b16 v[74:75], v12 offset:9216
	ds_read_b64_tr_b16 v[82:83], v12 offset:9248
	ds_read_b64_tr_b16 v[90:91], v12 offset:9280
	ds_read_b64_tr_b16 v[98:99], v12 offset:9312
	ds_read_b64_tr_b16 v[76:77], v12 offset:11520
	ds_read_b64_tr_b16 v[84:85], v12 offset:11552
	ds_read_b64_tr_b16 v[92:93], v12 offset:11584
	ds_read_b64_tr_b16 v[100:101], v12 offset:11616
	ds_read_b64_tr_b16 v[94:95], v12 offset:13824
	ds_read_b64_tr_b16 v[104:105], v12 offset:13856
	ds_read_b64_tr_b16 v[108:109], v12 offset:13888
	ds_read_b64_tr_b16 v[86:87], v12 offset:13920
	ds_read_b64_tr_b16 v[96:97], v12 offset:16128
	ds_read_b64_tr_b16 v[106:107], v12 offset:16160
	ds_read_b64_tr_b16 v[110:111], v12 offset:16192
	ds_read_b64_tr_b16 v[88:89], v12 offset:16224
	ds_read_b64_tr_b16 v[102:103], v12 offset:18432
	ds_read_b64_tr_b16 v[14:15], v12 offset:18464
	ds_read_b64_tr_b16 v[48:49], v12 offset:18496
	ds_read_b64_tr_b16 v[12:13], v12 offset:18528
	v_max3_f32 v62, v40, s84, v41
	v_max3_f32 v62, v62, v42, v43
	v_max3_f32 v62, v62, v36, v37
	v_max3_f32 v62, v62, v38, v39
	v_max3_f32 v62, v62, v32, v33
	v_max3_f32 v62, v62, v34, v35
	v_max3_f32 v62, v62, v28, v29
	v_max3_f32 v62, v62, v30, v31
	v_max3_f32 v62, v62, v24, v25
	v_max3_f32 v62, v62, v26, v27
	v_max3_f32 v62, v62, v20, v21
	v_max3_f32 v62, v62, v22, v23
	v_max3_f32 v62, v62, v16, v17
	v_max3_f32 v62, v62, v18, v19
	v_max3_f32 v62, v62, v4, v5
	v_max3_f32 v62, v62, v6, v7
	v_max3_f32 v62, v62, v0, v1
	v_max3_f32 v62, v62, v2, v3
	v_mov_b32_e32 v63, v62
	s_nop 1
	v_permlane16_swap_b32_e32 v62, v63
	v_max_f32_e32 v63, v63, v63
	v_max_f32_e32 v62, v62, v62
	v_max_f32_e32 v62, v62, v63
	v_mov_b32_e32 v63, v62
	s_nop 1
	v_permlane32_swap_b32_e32 v62, v63
	v_max_f32_e32 v63, v63, v63
	v_max_f32_e32 v62, v62, v62
	v_max_f32_e32 v112, v62, v63
	v_pk_add_f32 v[40:41], v[40:41], v[112:113] op_sel_hi:[1,0] neg_lo:[0,1] neg_hi:[0,1]
	v_pk_add_f32 v[42:43], v[42:43], v[112:113] op_sel_hi:[1,0] neg_lo:[0,1] neg_hi:[0,1]
	v_exp_f32_e32 v40, v40
	v_exp_f32_e32 v41, v41
	v_exp_f32_e32 v42, v42
	v_exp_f32_e32 v43, v43
	v_pk_add_f32 v[36:37], v[36:37], v[112:113] op_sel_hi:[1,0] neg_lo:[0,1] neg_hi:[0,1]
	v_pk_add_f32 v[38:39], v[38:39], v[112:113] op_sel_hi:[1,0] neg_lo:[0,1] neg_hi:[0,1]
	v_exp_f32_e32 v36, v36
	v_exp_f32_e32 v37, v37
	v_exp_f32_e32 v38, v38
	v_exp_f32_e32 v39, v39
	v_pk_add_f32 v[32:33], v[32:33], v[112:113] op_sel_hi:[1,0] neg_lo:[0,1] neg_hi:[0,1]
	v_pk_add_f32 v[62:63], v[40:41], 0 op_sel_hi:[1,0]
	v_pk_add_f32 v[34:35], v[34:35], v[112:113] op_sel_hi:[1,0] neg_lo:[0,1] neg_hi:[0,1]
	v_exp_f32_e32 v32, v32
	v_exp_f32_e32 v33, v33
	v_pk_add_f32 v[62:63], v[42:43], v[62:63]
	v_exp_f32_e32 v34, v34
	v_exp_f32_e32 v35, v35
	v_pk_add_f32 v[28:29], v[28:29], v[112:113] op_sel_hi:[1,0] neg_lo:[0,1] neg_hi:[0,1]
	v_pk_add_f32 v[62:63], v[36:37], v[62:63]
	v_pk_add_f32 v[30:31], v[30:31], v[112:113] op_sel_hi:[1,0] neg_lo:[0,1] neg_hi:[0,1]
	v_exp_f32_e32 v114, v28
	v_exp_f32_e32 v115, v29
	v_pk_add_f32 v[62:63], v[38:39], v[62:63]
	v_exp_f32_e32 v116, v30
	v_exp_f32_e32 v117, v31
	v_pk_add_f32 v[24:25], v[24:25], v[112:113] op_sel_hi:[1,0] neg_lo:[0,1] neg_hi:[0,1]
	v_pk_add_f32 v[62:63], v[32:33], v[62:63]
	v_pk_add_f32 v[26:27], v[26:27], v[112:113] op_sel_hi:[1,0] neg_lo:[0,1] neg_hi:[0,1]
	v_exp_f32_e32 v118, v24
	v_exp_f32_e32 v119, v25
	v_pk_add_f32 v[62:63], v[34:35], v[62:63]
	v_exp_f32_e32 v120, v26
	v_exp_f32_e32 v121, v27
	v_pk_add_f32 v[24:25], v[114:115], v[62:63]
	v_cvt_pk_bf16_f32 v26, v36, v37
	v_pk_add_f32 v[24:25], v[116:117], v[24:25]
	v_cvt_pk_bf16_f32 v27, v38, v39
	v_pk_add_f32 v[24:25], v[118:119], v[24:25]
	v_pk_add_f32 v[20:21], v[20:21], v[112:113] op_sel_hi:[1,0] neg_lo:[0,1] neg_hi:[0,1]
	v_pk_add_f32 v[62:63], v[120:121], v[24:25]
	v_cvt_pk_bf16_f32 v24, v40, v41
	v_cvt_pk_bf16_f32 v25, v42, v43
	v_pk_add_f32 v[22:23], v[22:23], v[112:113] op_sel_hi:[1,0] neg_lo:[0,1] neg_hi:[0,1]
	v_exp_f32_e32 v36, v20
	s_waitcnt lgkmcnt(14)
	v_mfma_f32_16x16x32_bf16 v[28:31], v[44:47], v[24:27], 0
	v_exp_f32_e32 v37, v21
	v_exp_f32_e32 v38, v22
	v_exp_f32_e32 v39, v23
	v_mfma_f32_16x16x32_bf16 v[8:11], v[8:11], v[24:27], 0
	v_add_f32_e64 v42, v16, -v112
	v_add_f32_e64 v43, v17, -v112
	v_pk_add_f32 v[44:45], v[18:19], v[112:113] op_sel_hi:[1,0] neg_lo:[0,1] neg_hi:[0,1]
	v_pk_add_f32 v[40:41], v[36:37], v[62:63]
	v_mfma_f32_16x16x32_bf16 v[20:23], v[50:53], v[24:27], 0
	v_add_f32_e64 v40, v38, v40
	v_add_f32_e64 v41, v39, v41
	v_pk_add_f32 v[0:1], v[0:1], v[112:113] op_sel_hi:[1,0] neg_lo:[0,1] neg_hi:[0,1]
	v_mov_b32_e32 v64, v65
	v_mfma_f32_16x16x32_bf16 v[16:19], v[58:61], v[24:27], 0
	v_cvt_pk_bf16_f32 v24, v32, v33
	v_cvt_pk_bf16_f32 v25, v34, v35
	v_cvt_pk_bf16_f32 v26, v114, v115
	v_cvt_pk_bf16_f32 v27, v116, v117
	v_exp_f32_e32 v32, v42
	v_exp_f32_e32 v33, v43
	v_mfma_f32_16x16x32_bf16 v[28:31], v[54:57], v[24:27], v[28:31]
	v_exp_f32_e32 v34, v44
	v_exp_f32_e32 v35, v45
	v_pk_add_f32 v[42:43], v[4:5], v[112:113] op_sel_hi:[1,0] neg_lo:[0,1] neg_hi:[0,1]
	v_mfma_f32_16x16x32_bf16 v[8:11], v[66:69], v[24:27], v[8:11]
	v_add_f32_e64 v44, v6, -v112
	v_add_f32_e64 v45, v7, -v112
	v_pk_add_f32 v[40:41], v[32:33], v[40:41]
	s_waitcnt lgkmcnt(1)
	v_mov_b32_e32 v50, v48
	v_mfma_f32_16x16x32_bf16 v[4:7], v[78:81], v[24:27], v[16:19]
	v_add_f32_e64 v40, v34, v40
	v_add_f32_e64 v41, v35, v41
	v_mov_b32_e32 v51, v49
	s_and_b64 s[6:7], s[26:27], exec
	v_cvt_pk_bf16_f32 v16, v118, v119
	v_cvt_pk_bf16_f32 v17, v120, v121
	v_cvt_pk_bf16_f32 v18, v36, v37
	v_cvt_pk_bf16_f32 v19, v38, v39
	v_mfma_f32_16x16x32_bf16 v[20:23], v[70:73], v[24:27], v[20:23]
	v_add_f32_e64 v38, v2, -v112
	v_add_f32_e64 v39, v3, -v112
	s_mov_b32 s6, 0xe800000
	s_cselect_b32 s8, s6, 0x2e800000
	v_mfma_f32_16x16x32_bf16 v[24:27], v[74:77], v[16:19], v[28:31]
	s_and_b64 s[6:7], s[28:29], exec
	s_cselect_b32 s6, 0x12800000, s8
	s_add_u32 s6, s42, s6
	v_exp_f32_e32 v28, v42
	v_exp_f32_e32 v29, v43
	v_exp_f32_e32 v30, v44
	v_exp_f32_e32 v31, v45
	v_mfma_f32_16x16x32_bf16 v[8:11], v[82:85], v[16:19], v[8:11]
	v_add_f32_e64 v36, v28, v40
	v_add_f32_e64 v37, v29, v41
	v_exp_f32_e32 v40, v0
	v_exp_f32_e32 v41, v1
	v_mfma_f32_16x16x32_bf16 v[0:3], v[98:101], v[16:19], v[4:7]
	s_addc_u32 s7, s43, 0
	s_lshl_b32 s66, s22, 6
	v_cvt_pk_bf16_f32 v62, v40, v41
	v_cvt_pk_bf16_f32 v4, v32, v33
	v_cvt_pk_bf16_f32 v5, v34, v35
	v_cvt_pk_bf16_f32 v6, v28, v29
	v_cvt_pk_bf16_f32 v7, v30, v31
	v_mfma_f32_16x16x32_bf16 v[20:23], v[90:93], v[16:19], v[20:23]
	s_nop 0
	v_mfma_f32_16x16x32_bf16 v[16:19], v[94:97], v[4:7], v[24:27]
	s_nop 2
	v_exp_f32_e32 v24, v38
	v_exp_f32_e32 v25, v39
	v_mfma_f32_16x16x32_bf16 v[8:11], v[104:107], v[4:7], v[8:11]
	v_mov_b32_e32 v104, v102
	v_mov_b32_e32 v105, v103
	v_cvt_pk_bf16_f32 v63, v24, v25
	v_mfma_f32_16x16x32_bf16 v[20:23], v[108:111], v[4:7], v[20:23]
	v_add_f32_e64 v26, v30, v36
	v_add_f32_e64 v27, v31, v37
	v_pk_add_f32 v[26:27], v[40:41], v[26:27]
	v_mfma_f32_16x16x32_bf16 v[0:3], v[86:89], v[4:7], v[0:3]
	v_add_f32_e64 v26, v24, v26
	v_add_f32_e64 v27, v25, v27
	v_pk_add_f32 v[26:27], v[26:27], v[26:27] op_sel:[0,1] op_sel_hi:[1,0]
	v_mfma_f32_16x16x32_bf16 v[4:7], v[102:105], v[62:65], v[16:19]
	v_mov_b32_e32 v27, v26
	s_nop 1
	v_permlane16_swap_b32_e32 v26, v27
	v_mov_b32_e32 v16, v14
	v_mov_b32_e32 v17, v15
	v_add_f32_e32 v24, v26, v27
	s_nop 0
	v_mfma_f32_16x16x32_bf16 v[8:11], v[14:17], v[62:65], v[8:11]
	s_waitcnt lgkmcnt(0)
	v_mov_b32_e32 v14, v12
	v_mov_b32_e32 v15, v13
	v_mfma_f32_16x16x32_bf16 v[16:19], v[48:51], v[62:65], v[20:23]
	s_nop 2
	v_mov_b32_e32 v20, v24
	s_nop 1
	v_permlane32_swap_b32_e32 v24, v20
	v_mfma_f32_16x16x32_bf16 v[12:15], v[12:15], v[62:65], v[0:3]
	s_nop 2
	v_add_f32_e32 v0, v24, v20
	v_rcp_f32_e32 v1, v0
	s_nop 0
	v_mul_f32_e32 v1, 0x42800000, v1
	v_mul_f32_e32 v2, v1, v4
	v_mul_f32_e32 v3, v1, v5
	v_med3_f32 v5, v2, s55, v228
	v_med3_f32 v3, v3, s55, v228
	v_mov_b32_e32 v2, v65
	v_cvt_pk_fp8_f32 v2, v5, v3
	v_mul_f32_e32 v4, v1, v6
	v_mul_f32_e32 v3, v1, v7
	v_med3_f32 v4, v4, s55, v228
	v_med3_f32 v3, v3, s55, v228
	v_cvt_pk_fp8_f32 v2, v4, v3 op_sel:[0,0,1]
	v_mul_f32_e32 v3, v1, v8
	v_mul_f32_e32 v4, v1, v9
	v_med3_f32 v6, v3, s55, v228
	v_med3_f32 v4, v4, s55, v228
	v_mov_b32_e32 v3, v65
	v_cvt_pk_fp8_f32 v3, v6, v4
	v_mul_f32_e32 v5, v1, v10
	v_mul_f32_e32 v4, v1, v11
	v_med3_f32 v5, v5, s55, v228
	v_med3_f32 v4, v4, s55, v228
	v_cvt_pk_fp8_f32 v3, v5, v4 op_sel:[0,0,1]
	v_mul_f32_e32 v4, v1, v16
	v_mul_f32_e32 v5, v1, v17
	v_med3_f32 v7, v4, s55, v228
	v_med3_f32 v5, v5, s55, v228
	v_mov_b32_e32 v4, v65
	v_cvt_pk_fp8_f32 v4, v7, v5
	v_mul_f32_e32 v6, v1, v18
	v_mul_f32_e32 v5, v1, v19
	v_med3_f32 v6, v6, s55, v228
	v_med3_f32 v5, v5, s55, v228
	v_cvt_pk_fp8_f32 v4, v6, v5 op_sel:[0,0,1]
	v_mul_f32_e32 v5, v1, v12
	v_mul_f32_e32 v6, v1, v13
	v_med3_f32 v8, v5, s55, v228
	v_med3_f32 v6, v6, s55, v228
	v_mov_b32_e32 v5, v65
	v_cvt_pk_fp8_f32 v5, v8, v6
	v_mul_f32_e32 v7, v1, v14
	v_mul_f32_e32 v1, v1, v15
	v_med3_f32 v6, v7, s55, v228
	v_med3_f32 v1, v1, s55, v228
	v_cvt_pk_fp8_f32 v5, v6, v1 op_sel:[0,0,1]
	v_lshlrev_b64 v[6:7], 10, v[164:165]
	v_lshl_add_u64 v[6:7], s[6:7], 0, v[6:7]
	v_lshl_add_u64 v[6:7], v[6:7], 0, s[66:67]
	v_lshl_add_u64 v[6:7], v[6:7], 0, v[160:161]
	global_store_dwordx4 v[6:7], v[2:5], off sc1
	s_and_saveexec_b64 s[6:7], vcc
	s_cbranch_execz .LBB0_422
	v_log_f32_e32 v0, v0
	s_ashr_i32 s25, s24, 31
	s_lshl_b64 s[8:9], s[24:25], 22
	v_readlane_b32 s10, v254, 30
	s_add_u32 s8, s10, s8
	v_readlane_b32 s10, v254, 31
	s_addc_u32 s9, s10, s9
	v_add_f32_e32 v0, v112, v0
	v_mul_f32_e32 v2, 0x3f317218, v0
	v_lshl_add_u64 v[0:1], s[8:9], 0, v[162:163]
	s_lshl_b32 s66, s22, 2
	v_lshl_add_u64 v[0:1], v[0:1], 0, s[66:67]
	global_store_dword v[0:1], v2, off sc1

.LBB0_468:
	v_lshl_add_u64 v[10:11], s[42:43], 0, v[8:9]
	v_add_co_u32_e32 v12, vcc, 0x12800000, v10
	v_lshl_add_u64 v[18:19], s[42:43], 0, v[0:1]
	s_nop 0
	v_addc_co_u32_e32 v13, vcc, 0, v11, vcc
	v_add_co_u32_e32 v14, vcc, 0xe800000, v10
	global_load_dword v55, v[12:13], off nt
	s_nop 0
	v_addc_co_u32_e32 v15, vcc, 0, v11, vcc
	v_add_co_u32_e32 v16, vcc, s8, v10
	global_load_dword v64, v[14:15], off nt
	s_nop 0
	v_addc_co_u32_e32 v17, vcc, 0, v11, vcc
	v_add_co_u32_e32 v20, vcc, 0x700000, v18
	global_load_dword v74, v[16:17], off
	s_nop 0
	v_addc_co_u32_e32 v21, vcc, 0, v19, vcc
	v_add_co_u32_e32 v22, vcc, 0xb00000, v18
	global_load_dword v75, v[20:21], off
	s_nop 0
	v_addc_co_u32_e32 v23, vcc, 0, v19, vcc
	global_load_dword v76, v[22:23], off
	v_add_co_u32_e32 v18, vcc, 0xf00000, v18
	v_lshl_add_u64 v[24:25], s[42:43], 0, v[2:3]
	s_nop 0
	v_addc_co_u32_e32 v19, vcc, 0, v19, vcc
	global_load_dword v77, v[18:19], off
	global_load_dword v51, v[12:13], off offset:256 nt
	global_load_dword v50, v[14:15], off offset:256 nt
	global_load_dword v49, v[16:17], off offset:256
	v_add_co_u32_e32 v28, vcc, s9, v24
	s_mov_b32 s7, 0x16800000
	s_nop 0
	v_addc_co_u32_e32 v29, vcc, 0, v25, vcc
	v_add_co_u32_e32 v56, vcc, s10, v24
	global_load_dword v52, v[28:29], off
	s_nop 0
	v_addc_co_u32_e32 v57, vcc, 0, v25, vcc
	global_load_dword v53, v[56:57], off
	v_add_co_u32_e32 v58, vcc, s11, v24
	s_add_i32 s6, s6, 2
	s_nop 0
	v_addc_co_u32_e32 v59, vcc, 0, v25, vcc
	global_load_dword v54, v[58:59], off
	global_load_dword v45, v[12:13], off offset:512 nt
	global_load_dword v44, v[14:15], off offset:512 nt
	global_load_dword v43, v[16:17], off offset:512
	v_lshl_add_u64 v[24:25], s[42:43], 0, v[4:5]
	v_add_co_u32_e32 v60, vcc, s9, v24
	v_lshl_add_u64 v[0:1], v[0:1], 0, s[80:81]
	s_nop 0
	v_addc_co_u32_e32 v61, vcc, 0, v25, vcc
	v_add_co_u32_e32 v62, vcc, s10, v24
	global_load_dword v46, v[60:61], off
	s_nop 0
	v_addc_co_u32_e32 v63, vcc, 0, v25, vcc
	global_load_dword v47, v[62:63], off
	v_add_co_u32_e32 v66, vcc, s11, v24
	v_lshl_add_u64 v[2:3], v[2:3], 0, s[80:81]
	s_nop 0
	v_addc_co_u32_e32 v67, vcc, 0, v25, vcc
	global_load_dword v48, v[66:67], off
	global_load_dword v39, v[12:13], off offset:768 nt
	global_load_dword v38, v[14:15], off offset:768 nt
	global_load_dword v37, v[16:17], off offset:768
	v_lshl_add_u64 v[24:25], s[42:43], 0, v[6:7]
	v_add_co_u32_e32 v68, vcc, s9, v24
	v_lshl_add_u64 v[4:5], v[4:5], 0, s[80:81]
	s_nop 0
	v_addc_co_u32_e32 v69, vcc, 0, v25, vcc
	v_add_co_u32_e32 v70, vcc, s10, v24
	global_load_dword v40, v[68:69], off
	s_nop 0
	v_addc_co_u32_e32 v71, vcc, 0, v25, vcc
	global_load_dword v41, v[70:71], off
	v_add_co_u32_e32 v72, vcc, s11, v24
	v_lshl_add_u64 v[6:7], v[6:7], 0, s[80:81]
	s_nop 0
	v_addc_co_u32_e32 v73, vcc, 0, v25, vcc
	global_load_dword v42, v[72:73], off
	global_load_dword v33, v[12:13], off offset:1024 nt
	global_load_dword v32, v[14:15], off offset:1024 nt
	global_load_dword v31, v[16:17], off offset:1024
	global_load_dword v36, v[20:21], off offset:64
	global_load_dword v35, v[22:23], off offset:64
	global_load_dword v34, v[18:19], off offset:64
	global_load_dword v27, v[12:13], off offset:1280 nt
	global_load_dword v26, v[14:15], off offset:1280 nt
	global_load_dword v25, v[16:17], off offset:1280
	global_load_dword v30, v[28:29], off offset:64
	s_nop 0
	global_load_dword v29, v[56:57], off offset:64
	global_load_dword v28, v[58:59], off offset:64
	global_load_dword v21, v[12:13], off offset:1536 nt
	global_load_dword v20, v[14:15], off offset:1536 nt
	global_load_dword v19, v[16:17], off offset:1536
	global_load_dword v24, v[60:61], off offset:64
	global_load_dword v23, v[62:63], off offset:64
	global_load_dword v22, v[66:67], off offset:64
	global_load_dword v18, v[12:13], off offset:1792 nt
	s_nop 0
	global_load_dword v13, v[14:15], off offset:1792 nt
	global_load_dword v12, v[16:17], off offset:1792
	s_nop 0
	global_load_dword v16, v[68:69], off offset:64
	global_load_dword v15, v[70:71], off offset:64
	global_load_dword v14, v[72:73], off offset:64
	v_add_co_u32_e32 v10, vcc, s7, v10
	v_lshl_add_u64 v[8:9], v[8:9], 0, s[12:13]
	s_nop 0
	v_addc_co_u32_e32 v11, vcc, 0, v11, vcc
	s_cmp_lt_u32 s6, 30
	s_waitcnt vmcnt(0)
	v_cvt_pk_f32_fp8_e32 v[60:61], v64
	v_cvt_pk_f32_fp8_sdwa v[62:63], v64 src0_sel:WORD_1
	v_cvt_pk_f32_fp8_e32 v[66:67], v74
	v_cvt_pk_f32_fp8_sdwa v[68:69], v74 src0_sel:WORD_1
	v_max3_f32 v17, v75, v76, v77
	v_sub_f32_e32 v56, v75, v17
	v_sub_f32_e32 v57, v76, v17
	v_mul_f32_e32 v56, 0x3fb8aa3b, v56
	v_mul_f32_e32 v57, 0x3fb8aa3b, v57
	v_sub_f32_e32 v17, v77, v17
	v_exp_f32_e32 v56, v56
	v_exp_f32_e32 v57, v57
	v_mul_f32_e32 v17, 0x3fb8aa3b, v17
	v_exp_f32_e32 v17, v17
	v_add_f32_e32 v58, v56, v57
	v_add_f32_e32 v58, v17, v58
	v_rcp_f32_e32 v58, v58
	s_nop 0
	v_mul_f32_e32 v58, 0.5, v58
	v_mul_f32_e32 v70, v56, v58
	v_mul_f32_e32 v71, v57, v58
	v_cvt_pk_f32_fp8_e32 v[56:57], v55
	v_mul_f32_e32 v17, v17, v58
	v_cvt_pk_f32_fp8_sdwa v[58:59], v55 src0_sel:WORD_1
	v_mul_f32_e32 v55, v71, v60
	v_fmac_f32_e32 v55, v70, v56
	v_mul_f32_e32 v56, v71, v61
	v_fmac_f32_e32 v56, v70, v57
	v_mul_f32_e32 v57, v71, v62
	v_fmac_f32_e32 v57, v70, v58
	v_mul_f32_e32 v58, v71, v63
	v_fmac_f32_e32 v58, v70, v59
	v_fmac_f32_e32 v55, v17, v66
	v_fmac_f32_e32 v56, v17, v67
	v_fmac_f32_e32 v57, v17, v68
	v_fmac_f32_e32 v58, v17, v69
	v_med3_f32 v17, v55, s55, v228
	v_med3_f32 v55, v56, s55, v228
	v_med3_f32 v56, v57, s55, v228
	v_med3_f32 v57, v58, s55, v228
	v_mov_b32_e32 v58, v65
	v_cvt_pk_fp8_f32 v58, v17, v55
	v_max3_f32 v17, v52, v53, v54
	v_sub_f32_e32 v52, v52, v17
	v_sub_f32_e32 v53, v53, v17
	v_mul_f32_e32 v52, 0x3fb8aa3b, v52
	v_mul_f32_e32 v53, 0x3fb8aa3b, v53
	v_sub_f32_e32 v17, v54, v17
	v_exp_f32_e32 v52, v52
	v_exp_f32_e32 v53, v53
	v_mul_f32_e32 v17, 0x3fb8aa3b, v17
	v_exp_f32_e32 v17, v17
	v_cvt_pk_fp8_f32 v58, v56, v57 op_sel:[0,0,1]
	v_add_f32_e32 v54, v52, v53
	v_cvt_pk_f32_fp8_e32 v[56:57], v50
	v_add_f32_e32 v54, v17, v54
	v_rcp_f32_e32 v54, v54
	global_store_dword v[10:11], v58, off sc1
	v_cvt_pk_f32_fp8_e32 v[58:59], v49
	v_cvt_pk_f32_fp8_sdwa v[60:61], v49 src0_sel:WORD_1
	v_mul_f32_e32 v54, 0.5, v54
	v_mul_f32_e32 v62, v52, v54
	v_mul_f32_e32 v63, v53, v54
	v_cvt_pk_f32_fp8_e32 v[52:53], v51
	v_mul_f32_e32 v17, v17, v54
	v_cvt_pk_f32_fp8_sdwa v[54:55], v51 src0_sel:WORD_1
	v_cvt_pk_f32_fp8_sdwa v[50:51], v50 src0_sel:WORD_1
	v_mul_f32_e32 v49, v63, v56
	v_fmac_f32_e32 v49, v62, v52
	v_mul_f32_e32 v52, v63, v57
	v_fmac_f32_e32 v52, v62, v53
	v_mul_f32_e32 v50, v63, v50
	v_mul_f32_e32 v51, v63, v51
	v_fmac_f32_e32 v49, v17, v58
	v_fmac_f32_e32 v52, v17, v59
	v_fmac_f32_e32 v50, v62, v54
	v_fmac_f32_e32 v51, v62, v55
	v_fmac_f32_e32 v50, v17, v60
	v_fmac_f32_e32 v51, v17, v61
	v_med3_f32 v17, v49, s55, v228
	v_med3_f32 v49, v52, s55, v228
	v_mov_b32_e32 v52, v65
	v_cvt_pk_fp8_f32 v52, v17, v49
	v_max3_f32 v17, v46, v47, v48
	v_sub_f32_e32 v46, v46, v17
	v_sub_f32_e32 v47, v47, v17
	v_mul_f32_e32 v46, 0x3fb8aa3b, v46
	v_mul_f32_e32 v47, 0x3fb8aa3b, v47
	v_sub_f32_e32 v17, v48, v17
	v_exp_f32_e32 v46, v46
	v_exp_f32_e32 v47, v47
	v_mul_f32_e32 v17, 0x3fb8aa3b, v17
	v_exp_f32_e32 v17, v17
	v_med3_f32 v50, v50, s55, v228
	v_add_f32_e32 v48, v46, v47
	v_med3_f32 v51, v51, s55, v228
	v_add_f32_e32 v48, v17, v48
	v_rcp_f32_e32 v48, v48
	v_cvt_pk_fp8_f32 v52, v50, v51 op_sel:[0,0,1]
	v_cvt_pk_f32_fp8_e32 v[50:51], v44
	v_cvt_pk_f32_fp8_sdwa v[54:55], v43 src0_sel:WORD_1
	v_mul_f32_e32 v48, 0.5, v48
	v_mul_f32_e32 v56, v46, v48
	v_mul_f32_e32 v57, v47, v48
	v_cvt_pk_f32_fp8_e32 v[46:47], v45
	v_mul_f32_e32 v17, v17, v48
	v_cvt_pk_f32_fp8_sdwa v[48:49], v45 src0_sel:WORD_1
	v_cvt_pk_f32_fp8_sdwa v[44:45], v44 src0_sel:WORD_1
	global_store_dword v[10:11], v52, off offset:256 sc1
	v_cvt_pk_f32_fp8_e32 v[52:53], v43
	v_mul_f32_e32 v43, v57, v50
	v_fmac_f32_e32 v43, v56, v46
	v_mul_f32_e32 v46, v57, v51
	v_fmac_f32_e32 v46, v56, v47
	v_mul_f32_e32 v44, v57, v44
	v_mul_f32_e32 v45, v57, v45
	v_fmac_f32_e32 v43, v17, v52
	v_fmac_f32_e32 v46, v17, v53
	v_fmac_f32_e32 v44, v56, v48
	v_fmac_f32_e32 v45, v56, v49
	v_fmac_f32_e32 v44, v17, v54
	v_fmac_f32_e32 v45, v17, v55
	v_med3_f32 v17, v43, s55, v228
	v_med3_f32 v43, v46, s55, v228
	v_mov_b32_e32 v46, v65
	v_cvt_pk_fp8_f32 v46, v17, v43
	v_max3_f32 v17, v40, v41, v42
	v_sub_f32_e32 v40, v40, v17
	v_sub_f32_e32 v41, v41, v17
	v_mul_f32_e32 v40, 0x3fb8aa3b, v40
	v_mul_f32_e32 v41, 0x3fb8aa3b, v41
	v_sub_f32_e32 v17, v42, v17
	v_exp_f32_e32 v40, v40
	v_exp_f32_e32 v41, v41
	v_mul_f32_e32 v17, 0x3fb8aa3b, v17
	v_exp_f32_e32 v17, v17
	v_med3_f32 v44, v44, s55, v228
	v_add_f32_e32 v42, v40, v41
	v_med3_f32 v45, v45, s55, v228
	v_add_f32_e32 v42, v17, v42
	v_rcp_f32_e32 v42, v42
	v_cvt_pk_fp8_f32 v46, v44, v45 op_sel:[0,0,1]
	v_cvt_pk_f32_fp8_e32 v[44:45], v38
	v_cvt_pk_f32_fp8_sdwa v[48:49], v37 src0_sel:WORD_1
	v_mul_f32_e32 v42, 0.5, v42
	v_mul_f32_e32 v50, v40, v42
	v_mul_f32_e32 v51, v41, v42
	v_cvt_pk_f32_fp8_e32 v[40:41], v39
	v_mul_f32_e32 v17, v17, v42
	v_cvt_pk_f32_fp8_sdwa v[42:43], v39 src0_sel:WORD_1
	v_cvt_pk_f32_fp8_sdwa v[38:39], v38 src0_sel:WORD_1
	global_store_dword v[10:11], v46, off offset:512 sc1
	v_cvt_pk_f32_fp8_e32 v[46:47], v37
	v_mul_f32_e32 v37, v51, v44
	v_fmac_f32_e32 v37, v50, v40
	v_mul_f32_e32 v40, v51, v45
	v_fmac_f32_e32 v40, v50, v41
	v_mul_f32_e32 v38, v51, v38
	v_mul_f32_e32 v39, v51, v39
	v_fmac_f32_e32 v37, v17, v46
	v_fmac_f32_e32 v40, v17, v47
	v_fmac_f32_e32 v38, v50, v42
	v_fmac_f32_e32 v39, v50, v43
	v_fmac_f32_e32 v38, v17, v48
	v_fmac_f32_e32 v39, v17, v49
	v_med3_f32 v17, v37, s55, v228
	v_med3_f32 v37, v40, s55, v228
	v_mov_b32_e32 v40, v65
	v_cvt_pk_fp8_f32 v40, v17, v37
	v_max3_f32 v17, v36, v35, v34
	v_sub_f32_e32 v36, v36, v17
	v_sub_f32_e32 v35, v35, v17
	v_mul_f32_e32 v36, 0x3fb8aa3b, v36
	v_mul_f32_e32 v35, 0x3fb8aa3b, v35
	v_sub_f32_e32 v17, v34, v17
	v_exp_f32_e32 v36, v36
	v_exp_f32_e32 v35, v35
	v_mul_f32_e32 v17, 0x3fb8aa3b, v17
	v_exp_f32_e32 v17, v17
	v_med3_f32 v38, v38, s55, v228
	v_add_f32_e32 v34, v36, v35
	v_med3_f32 v39, v39, s55, v228
	v_add_f32_e32 v34, v17, v34
	v_rcp_f32_e32 v34, v34
	v_cvt_pk_fp8_f32 v40, v38, v39 op_sel:[0,0,1]
	v_cvt_pk_f32_fp8_e32 v[38:39], v32
	v_cvt_pk_f32_fp8_sdwa v[42:43], v31 src0_sel:WORD_1
	v_mul_f32_e32 v34, 0.5, v34
	v_mul_f32_e32 v44, v36, v34
	v_mul_f32_e32 v45, v35, v34
	v_mul_f32_e32 v17, v17, v34
	v_cvt_pk_f32_fp8_e32 v[34:35], v33
	v_cvt_pk_f32_fp8_sdwa v[36:37], v33 src0_sel:WORD_1
	v_cvt_pk_f32_fp8_sdwa v[32:33], v32 src0_sel:WORD_1
	global_store_dword v[10:11], v40, off offset:768 sc1
	v_cvt_pk_f32_fp8_e32 v[40:41], v31
	v_mul_f32_e32 v31, v45, v38
	v_fmac_f32_e32 v31, v44, v34
	v_mul_f32_e32 v34, v45, v39
	v_fmac_f32_e32 v34, v44, v35
	v_mul_f32_e32 v32, v45, v32
	v_mul_f32_e32 v33, v45, v33
	v_fmac_f32_e32 v31, v17, v40
	v_fmac_f32_e32 v34, v17, v41
	v_fmac_f32_e32 v32, v44, v36
	v_fmac_f32_e32 v33, v44, v37
	v_fmac_f32_e32 v32, v17, v42
	v_fmac_f32_e32 v33, v17, v43
	v_med3_f32 v17, v31, s55, v228
	v_med3_f32 v31, v34, s55, v228
	v_mov_b32_e32 v34, v65
	v_cvt_pk_fp8_f32 v34, v17, v31
	v_max3_f32 v17, v30, v29, v28
	v_sub_f32_e32 v30, v30, v17
	v_sub_f32_e32 v29, v29, v17
	v_mul_f32_e32 v30, 0x3fb8aa3b, v30
	v_mul_f32_e32 v29, 0x3fb8aa3b, v29
	v_sub_f32_e32 v17, v28, v17
	v_exp_f32_e32 v30, v30
	v_exp_f32_e32 v29, v29
	v_mul_f32_e32 v17, 0x3fb8aa3b, v17
	v_exp_f32_e32 v17, v17
	v_med3_f32 v32, v32, s55, v228
	v_add_f32_e32 v28, v30, v29
	v_med3_f32 v33, v33, s55, v228
	v_add_f32_e32 v28, v17, v28
	v_rcp_f32_e32 v28, v28
	v_cvt_pk_fp8_f32 v34, v32, v33 op_sel:[0,0,1]
	v_cvt_pk_f32_fp8_e32 v[32:33], v26
	v_cvt_pk_f32_fp8_sdwa v[36:37], v25 src0_sel:WORD_1
	v_mul_f32_e32 v28, 0.5, v28
	v_mul_f32_e32 v38, v30, v28
	v_mul_f32_e32 v39, v29, v28
	v_mul_f32_e32 v17, v17, v28
	v_cvt_pk_f32_fp8_e32 v[28:29], v27
	v_cvt_pk_f32_fp8_sdwa v[30:31], v27 src0_sel:WORD_1
	v_cvt_pk_f32_fp8_sdwa v[26:27], v26 src0_sel:WORD_1
	global_store_dword v[10:11], v34, off offset:1024 sc1
	v_cvt_pk_f32_fp8_e32 v[34:35], v25
	v_mul_f32_e32 v25, v39, v32
	v_fmac_f32_e32 v25, v38, v28
	v_mul_f32_e32 v28, v39, v33
	v_fmac_f32_e32 v28, v38, v29
	v_mul_f32_e32 v26, v39, v26
	v_mul_f32_e32 v27, v39, v27
	v_fmac_f32_e32 v25, v17, v34
	v_fmac_f32_e32 v28, v17, v35
	v_fmac_f32_e32 v26, v38, v30
	v_fmac_f32_e32 v27, v38, v31
	v_fmac_f32_e32 v26, v17, v36
	v_fmac_f32_e32 v27, v17, v37
	v_med3_f32 v17, v25, s55, v228
	v_med3_f32 v25, v28, s55, v228
	v_mov_b32_e32 v28, v65
	v_cvt_pk_fp8_f32 v28, v17, v25
	v_max3_f32 v17, v24, v23, v22
	v_sub_f32_e32 v24, v24, v17
	v_sub_f32_e32 v23, v23, v17
	v_mul_f32_e32 v24, 0x3fb8aa3b, v24
	v_mul_f32_e32 v23, 0x3fb8aa3b, v23
	v_sub_f32_e32 v17, v22, v17
	v_exp_f32_e32 v24, v24
	v_exp_f32_e32 v23, v23
	v_mul_f32_e32 v17, 0x3fb8aa3b, v17
	v_exp_f32_e32 v17, v17
	v_med3_f32 v26, v26, s55, v228
	v_add_f32_e32 v22, v24, v23
	v_med3_f32 v27, v27, s55, v228
	v_add_f32_e32 v22, v17, v22
	v_rcp_f32_e32 v22, v22
	v_cvt_pk_fp8_f32 v28, v26, v27 op_sel:[0,0,1]
	v_cvt_pk_f32_fp8_e32 v[26:27], v20
	v_cvt_pk_f32_fp8_sdwa v[30:31], v19 src0_sel:WORD_1
	v_mul_f32_e32 v22, 0.5, v22
	v_mul_f32_e32 v32, v24, v22
	v_mul_f32_e32 v33, v23, v22
	v_mul_f32_e32 v17, v17, v22
	v_cvt_pk_f32_fp8_e32 v[22:23], v21
	v_cvt_pk_f32_fp8_sdwa v[24:25], v21 src0_sel:WORD_1
	v_cvt_pk_f32_fp8_sdwa v[20:21], v20 src0_sel:WORD_1
	global_store_dword v[10:11], v28, off offset:1280 sc1
	v_cvt_pk_f32_fp8_e32 v[28:29], v19
	v_mul_f32_e32 v19, v33, v26
	v_fmac_f32_e32 v19, v32, v22
	v_mul_f32_e32 v22, v33, v27
	v_fmac_f32_e32 v22, v32, v23
	v_mul_f32_e32 v20, v33, v20
	v_mul_f32_e32 v21, v33, v21
	v_fmac_f32_e32 v19, v17, v28
	v_fmac_f32_e32 v22, v17, v29
	v_fmac_f32_e32 v20, v32, v24
	v_fmac_f32_e32 v21, v32, v25
	v_fmac_f32_e32 v20, v17, v30
	v_fmac_f32_e32 v21, v17, v31
	v_med3_f32 v17, v19, s55, v228
	v_med3_f32 v19, v22, s55, v228
	v_mov_b32_e32 v22, v65
	v_cvt_pk_fp8_f32 v22, v17, v19
	v_max3_f32 v17, v16, v15, v14
	v_sub_f32_e32 v16, v16, v17
	v_sub_f32_e32 v15, v15, v17
	v_mul_f32_e32 v16, 0x3fb8aa3b, v16
	v_mul_f32_e32 v15, 0x3fb8aa3b, v15
	v_sub_f32_e32 v14, v14, v17
	v_exp_f32_e32 v16, v16
	v_exp_f32_e32 v15, v15
	v_mul_f32_e32 v14, 0x3fb8aa3b, v14
	v_exp_f32_e32 v14, v14
	v_med3_f32 v20, v20, s55, v228
	v_add_f32_e32 v17, v16, v15
	v_med3_f32 v21, v21, s55, v228
	v_add_f32_e32 v17, v14, v17
	v_rcp_f32_e32 v17, v17
	v_cvt_pk_fp8_f32 v22, v20, v21 op_sel:[0,0,1]
	v_cvt_pk_f32_fp8_sdwa v[20:21], v13 src0_sel:WORD_1
	v_mul_f32_e32 v17, 0.5, v17
	v_mul_f32_e32 v24, v16, v17
	v_mul_f32_e32 v25, v15, v17
	v_mul_f32_e32 v26, v14, v17
	v_cvt_pk_f32_fp8_e32 v[14:15], v18
	v_cvt_pk_f32_fp8_sdwa v[16:17], v18 src0_sel:WORD_1
	v_cvt_pk_f32_fp8_e32 v[18:19], v13
	global_store_dword v[10:11], v22, off offset:1536 sc1
	v_cvt_pk_f32_fp8_e32 v[22:23], v12
	v_cvt_pk_f32_fp8_sdwa v[12:13], v12 src0_sel:WORD_1
	v_mul_f32_e32 v18, v25, v18
	v_fmac_f32_e32 v18, v24, v14
	v_mul_f32_e32 v14, v25, v19
	v_fmac_f32_e32 v14, v24, v15
	v_mul_f32_e32 v15, v25, v20
	v_fmac_f32_e32 v15, v24, v16
	v_fmac_f32_e32 v15, v26, v12
	v_mul_f32_e32 v12, v25, v21
	v_fmac_f32_e32 v18, v26, v22
	v_fmac_f32_e32 v14, v26, v23
	v_fmac_f32_e32 v12, v24, v17
	v_fmac_f32_e32 v12, v26, v13
	v_med3_f32 v13, v18, s55, v228
	v_med3_f32 v14, v14, s55, v228
	v_mov_b32_e32 v16, v65
	v_cvt_pk_fp8_f32 v16, v13, v14
	v_med3_f32 v15, v15, s55, v228
	v_med3_f32 v12, v12, s55, v228
	v_cvt_pk_fp8_f32 v16, v15, v12 op_sel:[0,0,1]
	global_store_dword v[10:11], v16, off offset:1792 sc1
	s_cbranch_scc1 .LBB0_468
	s_barrier
	s_branch .LBB0_665

.LBB0_471:
	v_add_u32_e32 v20, v38, v25
	v_add_u32_e32 v22, v39, v25
	v_add_u32_e32 v34, v38, v31
	s_waitcnt lgkmcnt(0)
	s_barrier
	ds_read_b64_tr_b16 v[16:17], v45 offset:28928
	ds_read_b64_tr_b16 v[18:19], v45 offset:29568
	ds_read_b64_tr_b16 v[20:21], v20 offset:39168
	ds_read_b64_tr_b16 v[22:23], v22 offset:39168
	ds_read_b64_tr_b16 v[46:47], v34 offset:39168
	v_add_u32_e32 v34, v39, v31
	ds_read_b64_tr_b16 v[48:49], v34 offset:39168
	v_add_u32_e32 v34, v38, v36
	ds_read_b64_tr_b16 v[50:51], v34 offset:39168
	v_add_u32_e32 v34, v39, v36
	ds_read_b64_tr_b16 v[52:53], v34 offset:39168
	v_add_u32_e32 v34, v38, v37
	ds_read_b64_tr_b16 v[54:55], v34 offset:39168
	v_add_u32_e32 v34, v39, v37
	ds_read_b64_tr_b16 v[56:57], v34 offset:39168
	v_add_u32_e32 v34, v40, v25
	s_waitcnt lgkmcnt(6)
	v_mfma_f32_16x16x32_bf16 v[20:23], v[20:23], v[16:19], 0
	v_mov_b32_e32 v35, s25
	s_cmp_lg_u32 s26, 16
	s_mov_b32 s30, s26
	s_waitcnt lgkmcnt(4)
	v_mfma_f32_16x16x32_bf16 v[46:49], v[46:49], v[16:19], 0
	s_waitcnt lgkmcnt(2)
	v_mfma_f32_16x16x32_bf16 v[50:53], v[50:53], v[16:19], 0
	s_waitcnt lgkmcnt(0)
	v_mfma_f32_16x16x32_bf16 v[16:19], v[54:57], v[16:19], 0
	ds_read_b64_tr_b16 v[54:55], v45 offset:34048
	ds_read_b64_tr_b16 v[56:57], v45 offset:34688
	ds_read_b64_tr_b16 v[58:59], v34 offset:39168
	v_add_u32_e32 v34, v41, v25
	ds_read_b64_tr_b16 v[60:61], v34 offset:39168
	v_add_u32_e32 v34, v40, v31
	s_waitcnt lgkmcnt(0)
	v_mfma_f32_16x16x32_bf16 v[20:23], v[58:61], v[54:57], v[20:23]
	ds_read_b64_tr_b16 v[58:59], v34 offset:39168
	v_add_u32_e32 v34, v41, v31
	ds_read_b64_tr_b16 v[60:61], v34 offset:39168
	v_add_u32_e32 v34, v40, v36
	s_waitcnt lgkmcnt(0)
	v_mfma_f32_16x16x32_bf16 v[46:49], v[58:61], v[54:57], v[46:49]
	ds_read_b64_tr_b16 v[58:59], v34 offset:39168
	v_add_u32_e32 v34, v41, v36
	ds_read_b64_tr_b16 v[60:61], v34 offset:39168
	v_add_u32_e32 v34, v40, v37
	s_waitcnt lgkmcnt(0)
	v_mfma_f32_16x16x32_bf16 v[50:53], v[58:61], v[54:57], v[50:53]
	ds_read_b64_tr_b16 v[58:59], v34 offset:39168
	v_add_u32_e32 v34, v41, v37
	ds_read_b64_tr_b16 v[60:61], v34 offset:39168
	v_or_b32_e32 v34, s24, v30
	s_waitcnt lgkmcnt(0)
	v_mfma_f32_16x16x32_bf16 v[16:19], v[58:61], v[54:57], v[16:19]
	v_lshlrev_b64 v[34:35], 8, v[34:35]
	v_lshl_add_u64 v[34:35], v[32:33], 0, v[34:35]
	v_cvt_pk_bf16_f32 v20, v20, v21
	v_cvt_pk_bf16_f32 v21, v22, v23
	v_lshl_add_u64 v[22:23], s[14:15], 1, v[34:35]
	global_store_dwordx2 v[22:23], v[20:21], off sc1
	v_cvt_pk_bf16_f32 v20, v46, v47
	v_cvt_pk_bf16_f32 v21, v48, v49
	v_lshl_add_u64 v[22:23], s[16:17], 1, v[34:35]
	global_store_dwordx2 v[22:23], v[20:21], off sc1
	v_cvt_pk_bf16_f32 v20, v50, v51
	v_cvt_pk_bf16_f32 v21, v52, v53
	v_lshl_add_u64 v[22:23], s[18:19], 1, v[34:35]
	v_cvt_pk_bf16_f32 v16, v16, v17
	v_cvt_pk_bf16_f32 v17, v18, v19
	v_lshl_add_u64 v[18:19], s[20:21], 1, v[34:35]
	global_store_dwordx2 v[22:23], v[20:21], off sc1
	global_store_dwordx2 v[18:19], v[16:17], off sc1
	s_cbranch_scc0 .LBB0_476

.Lscan_loop:
	v_add_u32_e32 v0, 0x40000, v0
	v_add_u32_e32 v2, 0x1000, v2
	v_mov_b32_e32 v102, v0
	global_load_dword v118, v102, s[98:99]
	global_load_dword v134, v2, s[100:101]
	v_add_u32_e32 v103, 0x4000, v0
	global_load_dword v119, v103, s[98:99]
	global_load_dword v136, v2, s[100:101] offset:256
	v_add_u32_e32 v104, 0x8000, v0
	global_load_dword v120, v104, s[98:99]
	global_load_dword v138, v2, s[100:101] offset:512
	v_add_u32_e32 v105, 0xc000, v0
	global_load_dword v121, v105, s[98:99]
	global_load_dword v140, v2, s[100:101] offset:768
	v_add_u32_e32 v106, 0x10000, v0
	global_load_dword v122, v106, s[98:99]
	global_load_dword v142, v2, s[100:101] offset:1024
	v_add_u32_e32 v107, 0x14000, v0
	global_load_dword v123, v107, s[98:99]
	global_load_dword v144, v2, s[100:101] offset:1280
	v_add_u32_e32 v108, 0x18000, v0
	global_load_dword v124, v108, s[98:99]
	global_load_dword v146, v2, s[100:101] offset:1536
	v_add_u32_e32 v109, 0x1c000, v0
	global_load_dword v125, v109, s[98:99]
	global_load_dword v148, v2, s[100:101] offset:1792
	v_add_u32_e32 v110, 0x20000, v0
	global_load_dword v126, v110, s[98:99]
	global_load_dword v150, v2, s[100:101] offset:2048
	v_add_u32_e32 v111, 0x24000, v0
	global_load_dword v127, v111, s[98:99]
	global_load_dword v152, v2, s[100:101] offset:2304
	v_add_u32_e32 v112, 0x28000, v0
	global_load_dword v128, v112, s[98:99]
	global_load_dword v154, v2, s[100:101] offset:2560
	v_add_u32_e32 v113, 0x2c000, v0
	global_load_dword v129, v113, s[98:99]
	global_load_dword v156, v2, s[100:101] offset:2816
	v_add_u32_e32 v114, 0x30000, v0
	global_load_dword v130, v114, s[98:99]
	global_load_dword v158, v2, s[100:101] offset:3072
	v_add_u32_e32 v115, 0x34000, v0
	global_load_dword v131, v115, s[98:99]
	global_load_dword v160, v2, s[100:101] offset:3328
	v_add_u32_e32 v116, 0x38000, v0
	global_load_dword v132, v116, s[98:99]
	global_load_dword v162, v2, s[100:101] offset:3584
	v_add_u32_e32 v117, 0x3c000, v0
	global_load_dword v133, v117, s[98:99]
	global_load_dword v164, v2, s[100:101] offset:3840
	s_waitcnt vmcnt(32)
	v_lshlrev_b32_e32 v11, 16, v36
	v_and_b32_e32 v10, 0xffff0000, v36
	v_cvt_pk_bf16_f32 v16, v5, v4
	global_store_dword v20, v16, s[98:99] sc1
	v_pk_fma_f32 v[4:5], v[4:5], v[70:71], v[10:11] op_sel_hi:[1,0,1]
	v_lshlrev_b32_e32 v11, 16, v37
	v_and_b32_e32 v10, 0xffff0000, v37
	v_cvt_pk_bf16_f32 v16, v5, v4
	global_store_dword v21, v16, s[98:99] sc1
	v_pk_fma_f32 v[4:5], v[4:5], v[72:73], v[10:11] op_sel_hi:[1,0,1]
	v_lshlrev_b32_e32 v11, 16, v38
	v_and_b32_e32 v10, 0xffff0000, v38
	v_cvt_pk_bf16_f32 v16, v5, v4
	global_store_dword v22, v16, s[98:99] sc1
	v_pk_fma_f32 v[4:5], v[4:5], v[74:75], v[10:11] op_sel_hi:[1,0,1]
	v_lshlrev_b32_e32 v11, 16, v39
	v_and_b32_e32 v10, 0xffff0000, v39
	v_cvt_pk_bf16_f32 v16, v5, v4
	global_store_dword v23, v16, s[98:99] sc1
	v_pk_fma_f32 v[4:5], v[4:5], v[76:77], v[10:11] op_sel_hi:[1,0,1]
	v_lshlrev_b32_e32 v11, 16, v40
	v_and_b32_e32 v10, 0xffff0000, v40
	v_cvt_pk_bf16_f32 v16, v5, v4
	global_store_dword v24, v16, s[98:99] sc1
	v_pk_fma_f32 v[4:5], v[4:5], v[78:79], v[10:11] op_sel_hi:[1,0,1]
	v_lshlrev_b32_e32 v11, 16, v41
	v_and_b32_e32 v10, 0xffff0000, v41
	v_cvt_pk_bf16_f32 v16, v5, v4
	global_store_dword v25, v16, s[98:99] sc1
	v_pk_fma_f32 v[4:5], v[4:5], v[80:81], v[10:11] op_sel_hi:[1,0,1]
	v_lshlrev_b32_e32 v11, 16, v42
	v_and_b32_e32 v10, 0xffff0000, v42
	v_cvt_pk_bf16_f32 v16, v5, v4
	global_store_dword v26, v16, s[98:99] sc1
	v_pk_fma_f32 v[4:5], v[4:5], v[82:83], v[10:11] op_sel_hi:[1,0,1]
	v_lshlrev_b32_e32 v11, 16, v43
	v_and_b32_e32 v10, 0xffff0000, v43
	v_cvt_pk_bf16_f32 v16, v5, v4
	global_store_dword v27, v16, s[98:99] sc1
	v_pk_fma_f32 v[4:5], v[4:5], v[84:85], v[10:11] op_sel_hi:[1,0,1]
	v_lshlrev_b32_e32 v11, 16, v44
	v_and_b32_e32 v10, 0xffff0000, v44
	v_cvt_pk_bf16_f32 v16, v5, v4
	global_store_dword v28, v16, s[98:99] sc1
	v_pk_fma_f32 v[4:5], v[4:5], v[86:87], v[10:11] op_sel_hi:[1,0,1]
	v_lshlrev_b32_e32 v11, 16, v45
	v_and_b32_e32 v10, 0xffff0000, v45
	v_cvt_pk_bf16_f32 v16, v5, v4
	global_store_dword v29, v16, s[98:99] sc1
	v_pk_fma_f32 v[4:5], v[4:5], v[88:89], v[10:11] op_sel_hi:[1,0,1]
	v_lshlrev_b32_e32 v11, 16, v46
	v_and_b32_e32 v10, 0xffff0000, v46
	v_cvt_pk_bf16_f32 v16, v5, v4
	global_store_dword v30, v16, s[98:99] sc1
	v_pk_fma_f32 v[4:5], v[4:5], v[90:91], v[10:11] op_sel_hi:[1,0,1]
	v_lshlrev_b32_e32 v11, 16, v47
	v_and_b32_e32 v10, 0xffff0000, v47
	v_cvt_pk_bf16_f32 v16, v5, v4
	global_store_dword v31, v16, s[98:99] sc1
	v_pk_fma_f32 v[4:5], v[4:5], v[92:93], v[10:11] op_sel_hi:[1,0,1]
	v_lshlrev_b32_e32 v11, 16, v48
	v_and_b32_e32 v10, 0xffff0000, v48
	v_cvt_pk_bf16_f32 v16, v5, v4
	global_store_dword v32, v16, s[98:99] sc1
	v_pk_fma_f32 v[4:5], v[4:5], v[94:95], v[10:11] op_sel_hi:[1,0,1]
	v_lshlrev_b32_e32 v11, 16, v49
	v_and_b32_e32 v10, 0xffff0000, v49
	v_cvt_pk_bf16_f32 v16, v5, v4
	global_store_dword v33, v16, s[98:99] sc1
	v_pk_fma_f32 v[4:5], v[4:5], v[96:97], v[10:11] op_sel_hi:[1,0,1]
	v_lshlrev_b32_e32 v11, 16, v50
	v_and_b32_e32 v10, 0xffff0000, v50
	v_cvt_pk_bf16_f32 v16, v5, v4
	global_store_dword v34, v16, s[98:99] sc1
	v_pk_fma_f32 v[4:5], v[4:5], v[98:99], v[10:11] op_sel_hi:[1,0,1]
	v_lshlrev_b32_e32 v11, 16, v51
	v_and_b32_e32 v10, 0xffff0000, v51
	v_cvt_pk_bf16_f32 v16, v5, v4
	global_store_dword v35, v16, s[98:99] sc1
	v_pk_fma_f32 v[4:5], v[4:5], v[100:101], v[10:11] op_sel_hi:[1,0,1]
	s_add_i32 s10, s10, -1
	s_cmp_eq_u32 s10, 0
	s_cbranch_scc1 .Lscan_last
	v_add_u32_e32 v0, 0x40000, v0
	v_add_u32_e32 v2, 0x1000, v2
	v_mov_b32_e32 v20, v0
	global_load_dword v36, v20, s[98:99]
	global_load_dword v70, v2, s[100:101]
	v_add_u32_e32 v21, 0x4000, v0
	global_load_dword v37, v21, s[98:99]
	global_load_dword v72, v2, s[100:101] offset:256
	v_add_u32_e32 v22, 0x8000, v0
	global_load_dword v38, v22, s[98:99]
	global_load_dword v74, v2, s[100:101] offset:512
	v_add_u32_e32 v23, 0xc000, v0
	global_load_dword v39, v23, s[98:99]
	global_load_dword v76, v2, s[100:101] offset:768
	v_add_u32_e32 v24, 0x10000, v0
	global_load_dword v40, v24, s[98:99]
	global_load_dword v78, v2, s[100:101] offset:1024
	v_add_u32_e32 v25, 0x14000, v0
	global_load_dword v41, v25, s[98:99]
	global_load_dword v80, v2, s[100:101] offset:1280
	v_add_u32_e32 v26, 0x18000, v0
	global_load_dword v42, v26, s[98:99]
	global_load_dword v82, v2, s[100:101] offset:1536
	v_add_u32_e32 v27, 0x1c000, v0
	global_load_dword v43, v27, s[98:99]
	global_load_dword v84, v2, s[100:101] offset:1792
	v_add_u32_e32 v28, 0x20000, v0
	global_load_dword v44, v28, s[98:99]
	global_load_dword v86, v2, s[100:101] offset:2048
	v_add_u32_e32 v29, 0x24000, v0
	global_load_dword v45, v29, s[98:99]
	global_load_dword v88, v2, s[100:101] offset:2304
	v_add_u32_e32 v30, 0x28000, v0
	global_load_dword v46, v30, s[98:99]
	global_load_dword v90, v2, s[100:101] offset:2560
	v_add_u32_e32 v31, 0x2c000, v0
	global_load_dword v47, v31, s[98:99]
	global_load_dword v92, v2, s[100:101] offset:2816
	v_add_u32_e32 v32, 0x30000, v0
	global_load_dword v48, v32, s[98:99]
	global_load_dword v94, v2, s[100:101] offset:3072
	v_add_u32_e32 v33, 0x34000, v0
	global_load_dword v49, v33, s[98:99]
	global_load_dword v96, v2, s[100:101] offset:3328
	v_add_u32_e32 v34, 0x38000, v0
	global_load_dword v50, v34, s[98:99]
	global_load_dword v98, v2, s[100:101] offset:3584
	v_add_u32_e32 v35, 0x3c000, v0
	global_load_dword v51, v35, s[98:99]
	global_load_dword v100, v2, s[100:101] offset:3840
	s_waitcnt vmcnt(32)
	v_lshlrev_b32_e32 v11, 16, v118
	v_and_b32_e32 v10, 0xffff0000, v118
	v_cvt_pk_bf16_f32 v16, v5, v4
	global_store_dword v102, v16, s[98:99] sc1
	v_pk_fma_f32 v[4:5], v[4:5], v[134:135], v[10:11] op_sel_hi:[1,0,1]
	v_lshlrev_b32_e32 v11, 16, v119
	v_and_b32_e32 v10, 0xffff0000, v119
	v_cvt_pk_bf16_f32 v16, v5, v4
	global_store_dword v103, v16, s[98:99] sc1
	v_pk_fma_f32 v[4:5], v[4:5], v[136:137], v[10:11] op_sel_hi:[1,0,1]
	v_lshlrev_b32_e32 v11, 16, v120
	v_and_b32_e32 v10, 0xffff0000, v120
	v_cvt_pk_bf16_f32 v16, v5, v4
	global_store_dword v104, v16, s[98:99] sc1
	v_pk_fma_f32 v[4:5], v[4:5], v[138:139], v[10:11] op_sel_hi:[1,0,1]
	v_lshlrev_b32_e32 v11, 16, v121
	v_and_b32_e32 v10, 0xffff0000, v121
	v_cvt_pk_bf16_f32 v16, v5, v4
	global_store_dword v105, v16, s[98:99] sc1
	v_pk_fma_f32 v[4:5], v[4:5], v[140:141], v[10:11] op_sel_hi:[1,0,1]
	v_lshlrev_b32_e32 v11, 16, v122
	v_and_b32_e32 v10, 0xffff0000, v122
	v_cvt_pk_bf16_f32 v16, v5, v4
	global_store_dword v106, v16, s[98:99] sc1
	v_pk_fma_f32 v[4:5], v[4:5], v[142:143], v[10:11] op_sel_hi:[1,0,1]
	v_lshlrev_b32_e32 v11, 16, v123
	v_and_b32_e32 v10, 0xffff0000, v123
	v_cvt_pk_bf16_f32 v16, v5, v4
	global_store_dword v107, v16, s[98:99] sc1
	v_pk_fma_f32 v[4:5], v[4:5], v[144:145], v[10:11] op_sel_hi:[1,0,1]
	v_lshlrev_b32_e32 v11, 16, v124
	v_and_b32_e32 v10, 0xffff0000, v124
	v_cvt_pk_bf16_f32 v16, v5, v4
	global_store_dword v108, v16, s[98:99] sc1
	v_pk_fma_f32 v[4:5], v[4:5], v[146:147], v[10:11] op_sel_hi:[1,0,1]
	v_lshlrev_b32_e32 v11, 16, v125
	v_and_b32_e32 v10, 0xffff0000, v125
	v_cvt_pk_bf16_f32 v16, v5, v4
	global_store_dword v109, v16, s[98:99] sc1
	v_pk_fma_f32 v[4:5], v[4:5], v[148:149], v[10:11] op_sel_hi:[1,0,1]
	v_lshlrev_b32_e32 v11, 16, v126
	v_and_b32_e32 v10, 0xffff0000, v126
	v_cvt_pk_bf16_f32 v16, v5, v4
	global_store_dword v110, v16, s[98:99] sc1
	v_pk_fma_f32 v[4:5], v[4:5], v[150:151], v[10:11] op_sel_hi:[1,0,1]
	v_lshlrev_b32_e32 v11, 16, v127
	v_and_b32_e32 v10, 0xffff0000, v127
	v_cvt_pk_bf16_f32 v16, v5, v4
	global_store_dword v111, v16, s[98:99] sc1
	v_pk_fma_f32 v[4:5], v[4:5], v[152:153], v[10:11] op_sel_hi:[1,0,1]
	v_lshlrev_b32_e32 v11, 16, v128
	v_and_b32_e32 v10, 0xffff0000, v128
	v_cvt_pk_bf16_f32 v16, v5, v4
	global_store_dword v112, v16, s[98:99] sc1
	v_pk_fma_f32 v[4:5], v[4:5], v[154:155], v[10:11] op_sel_hi:[1,0,1]
	v_lshlrev_b32_e32 v11, 16, v129
	v_and_b32_e32 v10, 0xffff0000, v129
	v_cvt_pk_bf16_f32 v16, v5, v4
	global_store_dword v113, v16, s[98:99] sc1
	v_pk_fma_f32 v[4:5], v[4:5], v[156:157], v[10:11] op_sel_hi:[1,0,1]
	v_lshlrev_b32_e32 v11, 16, v130
	v_and_b32_e32 v10, 0xffff0000, v130
	v_cvt_pk_bf16_f32 v16, v5, v4
	global_store_dword v114, v16, s[98:99] sc1
	v_pk_fma_f32 v[4:5], v[4:5], v[158:159], v[10:11] op_sel_hi:[1,0,1]
	v_lshlrev_b32_e32 v11, 16, v131
	v_and_b32_e32 v10, 0xffff0000, v131
	v_cvt_pk_bf16_f32 v16, v5, v4
	global_store_dword v115, v16, s[98:99] sc1
	v_pk_fma_f32 v[4:5], v[4:5], v[160:161], v[10:11] op_sel_hi:[1,0,1]
	v_lshlrev_b32_e32 v11, 16, v132
	v_and_b32_e32 v10, 0xffff0000, v132
	v_cvt_pk_bf16_f32 v16, v5, v4
	global_store_dword v116, v16, s[98:99] sc1
	v_pk_fma_f32 v[4:5], v[4:5], v[162:163], v[10:11] op_sel_hi:[1,0,1]
	v_lshlrev_b32_e32 v11, 16, v133
	v_and_b32_e32 v10, 0xffff0000, v133
	v_cvt_pk_bf16_f32 v16, v5, v4
	global_store_dword v117, v16, s[98:99] sc1
	v_pk_fma_f32 v[4:5], v[4:5], v[164:165], v[10:11] op_sel_hi:[1,0,1]
	s_branch .Lscan_loop
.Lscan_last:
	s_waitcnt vmcnt(0)
	v_lshlrev_b32_e32 v11, 16, v118
	v_and_b32_e32 v10, 0xffff0000, v118
	v_cvt_pk_bf16_f32 v16, v5, v4
	global_store_dword v102, v16, s[98:99] sc1
	v_pk_fma_f32 v[4:5], v[4:5], v[134:135], v[10:11] op_sel_hi:[1,0,1]
	v_lshlrev_b32_e32 v11, 16, v119
	v_and_b32_e32 v10, 0xffff0000, v119
	v_cvt_pk_bf16_f32 v16, v5, v4
	global_store_dword v103, v16, s[98:99] sc1
	v_pk_fma_f32 v[4:5], v[4:5], v[136:137], v[10:11] op_sel_hi:[1,0,1]
	v_lshlrev_b32_e32 v11, 16, v120
	v_and_b32_e32 v10, 0xffff0000, v120
	v_cvt_pk_bf16_f32 v16, v5, v4
	global_store_dword v104, v16, s[98:99] sc1
	v_pk_fma_f32 v[4:5], v[4:5], v[138:139], v[10:11] op_sel_hi:[1,0,1]
	v_lshlrev_b32_e32 v11, 16, v121
	v_and_b32_e32 v10, 0xffff0000, v121
	v_cvt_pk_bf16_f32 v16, v5, v4
	global_store_dword v105, v16, s[98:99] sc1
	v_pk_fma_f32 v[4:5], v[4:5], v[140:141], v[10:11] op_sel_hi:[1,0,1]
	v_lshlrev_b32_e32 v11, 16, v122
	v_and_b32_e32 v10, 0xffff0000, v122
	v_cvt_pk_bf16_f32 v16, v5, v4
	global_store_dword v106, v16, s[98:99] sc1
	v_pk_fma_f32 v[4:5], v[4:5], v[142:143], v[10:11] op_sel_hi:[1,0,1]
	v_lshlrev_b32_e32 v11, 16, v123
	v_and_b32_e32 v10, 0xffff0000, v123
	v_cvt_pk_bf16_f32 v16, v5, v4
	global_store_dword v107, v16, s[98:99] sc1
	v_pk_fma_f32 v[4:5], v[4:5], v[144:145], v[10:11] op_sel_hi:[1,0,1]
	v_lshlrev_b32_e32 v11, 16, v124
	v_and_b32_e32 v10, 0xffff0000, v124
	v_cvt_pk_bf16_f32 v16, v5, v4
	global_store_dword v108, v16, s[98:99] sc1
	v_pk_fma_f32 v[4:5], v[4:5], v[146:147], v[10:11] op_sel_hi:[1,0,1]
	v_lshlrev_b32_e32 v11, 16, v125
	v_and_b32_e32 v10, 0xffff0000, v125
	v_cvt_pk_bf16_f32 v16, v5, v4
	global_store_dword v109, v16, s[98:99] sc1
	v_pk_fma_f32 v[4:5], v[4:5], v[148:149], v[10:11] op_sel_hi:[1,0,1]
	v_lshlrev_b32_e32 v11, 16, v126
	v_and_b32_e32 v10, 0xffff0000, v126
	v_cvt_pk_bf16_f32 v16, v5, v4
	global_store_dword v110, v16, s[98:99] sc1
	v_pk_fma_f32 v[4:5], v[4:5], v[150:151], v[10:11] op_sel_hi:[1,0,1]
	v_lshlrev_b32_e32 v11, 16, v127
	v_and_b32_e32 v10, 0xffff0000, v127
	v_cvt_pk_bf16_f32 v16, v5, v4
	global_store_dword v111, v16, s[98:99] sc1
	v_pk_fma_f32 v[4:5], v[4:5], v[152:153], v[10:11] op_sel_hi:[1,0,1]
	v_lshlrev_b32_e32 v11, 16, v128
	v_and_b32_e32 v10, 0xffff0000, v128
	v_cvt_pk_bf16_f32 v16, v5, v4
	global_store_dword v112, v16, s[98:99] sc1
	v_pk_fma_f32 v[4:5], v[4:5], v[154:155], v[10:11] op_sel_hi:[1,0,1]
	v_lshlrev_b32_e32 v11, 16, v129
	v_and_b32_e32 v10, 0xffff0000, v129
	v_cvt_pk_bf16_f32 v16, v5, v4
	global_store_dword v113, v16, s[98:99] sc1
	v_pk_fma_f32 v[4:5], v[4:5], v[156:157], v[10:11] op_sel_hi:[1,0,1]
	v_lshlrev_b32_e32 v11, 16, v130
	v_and_b32_e32 v10, 0xffff0000, v130
	v_cvt_pk_bf16_f32 v16, v5, v4
	global_store_dword v114, v16, s[98:99] sc1
	v_pk_fma_f32 v[4:5], v[4:5], v[158:159], v[10:11] op_sel_hi:[1,0,1]
	v_lshlrev_b32_e32 v11, 16, v131
	v_and_b32_e32 v10, 0xffff0000, v131
	v_cvt_pk_bf16_f32 v16, v5, v4
	global_store_dword v115, v16, s[98:99] sc1
	v_pk_fma_f32 v[4:5], v[4:5], v[160:161], v[10:11] op_sel_hi:[1,0,1]
	v_lshlrev_b32_e32 v11, 16, v132
	v_and_b32_e32 v10, 0xffff0000, v132
	v_cvt_pk_bf16_f32 v16, v5, v4
	global_store_dword v116, v16, s[98:99] sc1
	v_pk_fma_f32 v[4:5], v[4:5], v[162:163], v[10:11] op_sel_hi:[1,0,1]
	v_lshlrev_b32_e32 v11, 16, v133
	v_and_b32_e32 v10, 0xffff0000, v133
	v_cvt_pk_bf16_f32 v16, v5, v4
	global_store_dword v117, v16, s[98:99] sc1
	v_pk_fma_f32 v[4:5], v[4:5], v[164:165], v[10:11] op_sel_hi:[1,0,1]
	v_add_u32_e32 v6, s62, v6
	s_mov_b32 s10, 0x1ffff
	v_cmp_lt_i32_e32 vcc, s10, v6
	s_or_b64 s[8:9], vcc, s[8:9]
	v_add_u16_e32 v7, s62, v7
	s_andn2_b64 exec, exec, s[8:9]
	s_cbranch_execnz .LBB0_523

.LBB0_597:
	s_or_b64 exec, exec, s[28:29]
	s_waitcnt lgkmcnt(0)
	s_barrier
	ds_read_b128 v[10:13], v200
	ds_read_b128 v[14:17], v200 offset:16
	ds_read_b128 v[4:7], v200 offset:32
	ds_read_b128 v[0:3], v200 offset:48
	s_mov_b32 s28, 0x2e800000
	s_waitcnt lgkmcnt(3)
	v_pk_add_f32 v[18:19], v[60:61], v[10:11] op_sel_hi:[1,0] neg_lo:[0,1] neg_hi:[0,1]
	v_add_u32_e32 v67, 32, v67
	v_pk_mul_f32 v[10:11], v[18:19], v[10:11] op_sel:[0,1]
	v_add_u32_e32 v184, 32, v184
	s_waitcnt vmcnt(0)
	v_pk_fma_f32 v[10:11], v[136:137], v[10:11], v[138:139]
	v_add_u32_e32 v185, 32, v185
	v_mul_f32_e32 v18, 0xbfb8aa3b, v10
	v_mul_f32_e32 v19, 0xbfb8aa3b, v11
	v_exp_f32_e32 v18, v18
	v_exp_f32_e32 v19, v19
	v_add_u32_e32 v186, 32, v186
	v_add_u32_e32 v187, 32, v187
	v_add_f32_e32 v18, 1.0, v18
	v_add_f32_e32 v19, 1.0, v19
	v_rcp_f32_e32 v18, v18
	v_rcp_f32_e32 v19, v19
	v_add_u32_e32 v188, 32, v188
	v_add_u32_e32 v189, 32, v189
	v_add_u32_e32 v190, 32, v190
	v_pk_mul_f32 v[10:11], v[10:11], v[18:19]
	s_nop 0
	v_cvt_pk_bf16_f32 v20, v10, v11
	v_lshl_add_u64 v[10:11], v[68:69], 0, s[26:27]
	v_add_co_u32_e32 v18, vcc, s28, v10
	s_mov_b32 s28, 0x2e801000
	s_nop 0
	v_addc_co_u32_e32 v19, vcc, 0, v11, vcc
	global_store_dword v[18:19], v20, off offset:1024 sc1
	v_pk_add_f32 v[20:21], v[62:63], v[12:13] op_sel_hi:[1,0] neg_lo:[0,1] neg_hi:[0,1]
	v_mov_b32_e32 v12, v13
	v_pk_mul_f32 v[12:13], v[20:21], v[12:13] op_sel_hi:[1,0]
	s_add_u32 s26, s26, 0x10000
	v_pk_fma_f32 v[12:13], v[136:137], v[12:13], v[138:139]
	s_addc_u32 s27, s27, 0
	v_mul_f32_e32 v20, 0xbfb8aa3b, v12
	v_mul_f32_e32 v21, 0xbfb8aa3b, v13
	v_exp_f32_e32 v20, v20
	v_exp_f32_e32 v21, v21
	s_cmp_lg_u32 s26, 0x80000
	v_add_f32_e32 v20, 1.0, v20
	v_add_f32_e32 v21, 1.0, v21
	v_rcp_f32_e32 v20, v20
	v_rcp_f32_e32 v21, v21
	s_nop 0
	v_pk_mul_f32 v[12:13], v[12:13], v[20:21]
	s_nop 0
	v_cvt_pk_bf16_f32 v12, v12, v13
	global_store_dword v[18:19], v12, off offset:3072 sc1
	s_waitcnt lgkmcnt(2)
	v_pk_add_f32 v[12:13], v[56:57], v[14:15] op_sel_hi:[1,0] neg_lo:[0,1] neg_hi:[0,1]
	s_nop 0
	v_pk_mul_f32 v[12:13], v[12:13], v[14:15] op_sel:[0,1]
	s_nop 0
	v_pk_fma_f32 v[12:13], v[136:137], v[12:13], v[138:139]
	s_nop 0
	v_mul_f32_e32 v14, 0xbfb8aa3b, v12
	v_mul_f32_e32 v15, 0xbfb8aa3b, v13
	v_exp_f32_e32 v14, v14
	v_exp_f32_e32 v15, v15
	v_add_f32_e32 v14, 1.0, v14
	v_add_f32_e32 v15, 1.0, v15
	v_rcp_f32_e32 v14, v14
	v_rcp_f32_e32 v15, v15
	s_nop 0
	v_pk_mul_f32 v[12:13], v[12:13], v[14:15]
	s_nop 0
	v_cvt_pk_bf16_f32 v14, v12, v13
	v_add_co_u32_e32 v12, vcc, s28, v10
	s_mov_b32 s28, 0x2e802000
	s_nop 0
	v_addc_co_u32_e32 v13, vcc, 0, v11, vcc
	global_store_dword v[12:13], v14, off offset:1024 sc1
	v_pk_add_f32 v[14:15], v[58:59], v[16:17] op_sel_hi:[1,0] neg_lo:[0,1] neg_hi:[0,1]
	v_mov_b32_e32 v16, v17
	v_pk_mul_f32 v[14:15], v[14:15], v[16:17] op_sel_hi:[1,0]
	s_nop 0
	v_pk_fma_f32 v[14:15], v[136:137], v[14:15], v[138:139]
	s_nop 0
	v_mul_f32_e32 v16, 0xbfb8aa3b, v14
	v_mul_f32_e32 v17, 0xbfb8aa3b, v15
	v_exp_f32_e32 v16, v16
	v_exp_f32_e32 v17, v17
	v_add_f32_e32 v16, 1.0, v16
	v_add_f32_e32 v17, 1.0, v17
	v_rcp_f32_e32 v16, v16
	v_rcp_f32_e32 v17, v17
	s_nop 0
	v_pk_mul_f32 v[14:15], v[14:15], v[16:17]
	s_nop 0
	v_cvt_pk_bf16_f32 v14, v14, v15
	global_store_dword v[12:13], v14, off offset:3072 sc1
	s_waitcnt lgkmcnt(1)
	v_pk_add_f32 v[12:13], v[52:53], v[4:5] op_sel_hi:[1,0] neg_lo:[0,1] neg_hi:[0,1]
	s_nop 0
	v_pk_mul_f32 v[4:5], v[12:13], v[4:5] op_sel:[0,1]
	s_nop 0
	v_pk_fma_f32 v[4:5], v[136:137], v[4:5], v[138:139]
	s_nop 0
	v_mul_f32_e32 v12, 0xbfb8aa3b, v4
	v_mul_f32_e32 v13, 0xbfb8aa3b, v5
	v_exp_f32_e32 v12, v12
	v_exp_f32_e32 v13, v13
	v_add_f32_e32 v12, 1.0, v12
	v_add_f32_e32 v13, 1.0, v13
	v_rcp_f32_e32 v12, v12
	v_rcp_f32_e32 v13, v13
	s_nop 0
	v_pk_mul_f32 v[4:5], v[4:5], v[12:13]
	s_nop 0
	v_cvt_pk_bf16_f32 v12, v4, v5
	v_add_co_u32_e32 v4, vcc, s28, v10
	s_mov_b32 s28, 0x2e803000
	s_nop 0
	v_addc_co_u32_e32 v5, vcc, 0, v11, vcc
	global_store_dword v[4:5], v12, off offset:1024 sc1
	v_pk_add_f32 v[12:13], v[54:55], v[6:7] op_sel_hi:[1,0] neg_lo:[0,1] neg_hi:[0,1]
	v_mov_b32_e32 v6, v7
	v_pk_mul_f32 v[6:7], v[12:13], v[6:7] op_sel_hi:[1,0]
	s_nop 0
	v_pk_fma_f32 v[6:7], v[136:137], v[6:7], v[138:139]
	s_nop 0
	v_mul_f32_e32 v12, 0xbfb8aa3b, v6
	v_mul_f32_e32 v13, 0xbfb8aa3b, v7
	v_exp_f32_e32 v12, v12
	v_exp_f32_e32 v13, v13
	v_add_f32_e32 v12, 1.0, v12
	v_add_f32_e32 v13, 1.0, v13
	v_rcp_f32_e32 v12, v12
	v_rcp_f32_e32 v13, v13
	s_nop 0
	v_pk_mul_f32 v[6:7], v[6:7], v[12:13]
	s_nop 0
	v_cvt_pk_bf16_f32 v6, v6, v7
	global_store_dword v[4:5], v6, off offset:3072 sc1
	s_waitcnt lgkmcnt(0)
	v_pk_add_f32 v[4:5], v[48:49], v[0:1] op_sel_hi:[1,0] neg_lo:[0,1] neg_hi:[0,1]
	s_nop 0
	v_pk_mul_f32 v[0:1], v[4:5], v[0:1] op_sel:[0,1]
	s_nop 0
	v_pk_fma_f32 v[0:1], v[136:137], v[0:1], v[138:139]
	s_nop 0
	v_mul_f32_e32 v4, 0xbfb8aa3b, v0
	v_mul_f32_e32 v5, 0xbfb8aa3b, v1
	v_exp_f32_e32 v4, v4
	v_exp_f32_e32 v5, v5
	v_add_f32_e32 v4, 1.0, v4
	v_add_f32_e32 v5, 1.0, v5
	v_rcp_f32_e32 v4, v4
	v_rcp_f32_e32 v5, v5
	s_nop 0
	v_pk_mul_f32 v[0:1], v[0:1], v[4:5]
	s_nop 0
	v_cvt_pk_bf16_f32 v4, v0, v1
	v_add_co_u32_e32 v0, vcc, s28, v10
	s_mov_b32 s28, 0x2e804000
	s_nop 0
	v_addc_co_u32_e32 v1, vcc, 0, v11, vcc
	global_store_dword v[0:1], v4, off offset:1024 sc1
	v_pk_add_f32 v[4:5], v[50:51], v[2:3] op_sel_hi:[1,0] neg_lo:[0,1] neg_hi:[0,1]
	v_mov_b32_e32 v2, v3
	v_pk_mul_f32 v[2:3], v[4:5], v[2:3] op_sel_hi:[1,0]
	s_nop 0
	v_pk_fma_f32 v[2:3], v[136:137], v[2:3], v[138:139]
	s_nop 0
	v_mul_f32_e32 v4, 0xbfb8aa3b, v2
	v_mul_f32_e32 v5, 0xbfb8aa3b, v3
	v_exp_f32_e32 v4, v4
	v_exp_f32_e32 v5, v5
	v_add_f32_e32 v4, 1.0, v4
	v_add_f32_e32 v5, 1.0, v5
	v_rcp_f32_e32 v4, v4
	v_rcp_f32_e32 v5, v5
	s_nop 0
	v_pk_mul_f32 v[2:3], v[2:3], v[4:5]
	s_nop 0
	v_cvt_pk_bf16_f32 v2, v2, v3
	global_store_dword v[0:1], v2, off offset:3072 sc1
	ds_read_b128 v[0:3], v200 offset:64
	s_waitcnt lgkmcnt(0)
	v_pk_add_f32 v[4:5], v[166:167], v[0:1] op_sel_hi:[1,0] neg_lo:[0,1] neg_hi:[0,1]
	s_nop 0
	v_pk_mul_f32 v[0:1], v[4:5], v[0:1] op_sel:[0,1]
	s_nop 0
	v_pk_fma_f32 v[0:1], v[136:137], v[0:1], v[138:139]
	s_nop 0
	v_mul_f32_e32 v4, 0xbfb8aa3b, v0
	v_mul_f32_e32 v5, 0xbfb8aa3b, v1
	v_exp_f32_e32 v4, v4
	v_exp_f32_e32 v5, v5
	v_add_f32_e32 v4, 1.0, v4
	v_add_f32_e32 v5, 1.0, v5
	v_rcp_f32_e32 v4, v4
	v_rcp_f32_e32 v5, v5
	s_nop 0
	v_pk_mul_f32 v[0:1], v[0:1], v[4:5]
	s_nop 0
	v_cvt_pk_bf16_f32 v4, v0, v1
	v_add_co_u32_e32 v0, vcc, s28, v10
	s_mov_b32 s28, 0x2e805000
	s_nop 0
	v_addc_co_u32_e32 v1, vcc, 0, v11, vcc
	global_store_dword v[0:1], v4, off offset:1024 sc1
	v_pk_add_f32 v[4:5], v[46:47], v[2:3] op_sel_hi:[1,0] neg_lo:[0,1] neg_hi:[0,1]
	v_mov_b32_e32 v2, v3
	v_pk_mul_f32 v[2:3], v[4:5], v[2:3] op_sel_hi:[1,0]
	s_nop 0
	v_pk_fma_f32 v[2:3], v[136:137], v[2:3], v[138:139]
	s_nop 0
	v_mul_f32_e32 v4, 0xbfb8aa3b, v2
	v_mul_f32_e32 v5, 0xbfb8aa3b, v3
	v_exp_f32_e32 v4, v4
	v_exp_f32_e32 v5, v5
	v_add_f32_e32 v4, 1.0, v4
	v_add_f32_e32 v5, 1.0, v5
	v_rcp_f32_e32 v4, v4
	v_rcp_f32_e32 v5, v5
	s_nop 0
	v_pk_mul_f32 v[2:3], v[2:3], v[4:5]
	s_nop 0
	v_cvt_pk_bf16_f32 v2, v2, v3
	global_store_dword v[0:1], v2, off offset:3072 sc1
	ds_read_b128 v[0:3], v200 offset:80
	s_waitcnt lgkmcnt(0)
	v_pk_add_f32 v[4:5], v[40:41], v[0:1] op_sel_hi:[1,0] neg_lo:[0,1] neg_hi:[0,1]
	s_nop 0
	v_pk_mul_f32 v[0:1], v[4:5], v[0:1] op_sel:[0,1]
	s_nop 0
	v_pk_fma_f32 v[0:1], v[136:137], v[0:1], v[138:139]
	s_nop 0
	v_mul_f32_e32 v4, 0xbfb8aa3b, v0
	v_mul_f32_e32 v5, 0xbfb8aa3b, v1
	v_exp_f32_e32 v4, v4
	v_exp_f32_e32 v5, v5
	v_add_f32_e32 v4, 1.0, v4
	v_add_f32_e32 v5, 1.0, v5
	v_rcp_f32_e32 v4, v4
	v_rcp_f32_e32 v5, v5
	s_nop 0
	v_pk_mul_f32 v[0:1], v[0:1], v[4:5]
	s_nop 0
	v_cvt_pk_bf16_f32 v4, v0, v1
	v_add_co_u32_e32 v0, vcc, s28, v10
	s_mov_b32 s28, 0x2e806000
	s_nop 0
	v_addc_co_u32_e32 v1, vcc, 0, v11, vcc
	global_store_dword v[0:1], v4, off offset:1024 sc1
	v_pk_add_f32 v[4:5], v[42:43], v[2:3] op_sel_hi:[1,0] neg_lo:[0,1] neg_hi:[0,1]
	v_mov_b32_e32 v2, v3
	v_pk_mul_f32 v[2:3], v[4:5], v[2:3] op_sel_hi:[1,0]
	s_nop 0
	v_pk_fma_f32 v[2:3], v[136:137], v[2:3], v[138:139]
	s_nop 0
	v_mul_f32_e32 v4, 0xbfb8aa3b, v2
	v_mul_f32_e32 v5, 0xbfb8aa3b, v3
	v_exp_f32_e32 v4, v4
	v_exp_f32_e32 v5, v5
	v_add_f32_e32 v4, 1.0, v4
	v_add_f32_e32 v5, 1.0, v5
	v_rcp_f32_e32 v4, v4
	v_rcp_f32_e32 v5, v5
	s_nop 0
	v_pk_mul_f32 v[2:3], v[2:3], v[4:5]
	s_nop 0
	v_cvt_pk_bf16_f32 v2, v2, v3
	global_store_dword v[0:1], v2, off offset:3072 sc1
	ds_read_b128 v[0:3], v200 offset:96
	ds_read_b128 v[4:7], v200 offset:112
	s_waitcnt lgkmcnt(1)
	v_pk_add_f32 v[12:13], v[36:37], v[0:1] op_sel_hi:[1,0] neg_lo:[0,1] neg_hi:[0,1]
	s_nop 0
	v_pk_mul_f32 v[0:1], v[12:13], v[0:1] op_sel:[0,1]
	s_nop 0
	v_pk_fma_f32 v[0:1], v[136:137], v[0:1], v[138:139]
	s_nop 0
	v_mul_f32_e32 v12, 0xbfb8aa3b, v0
	v_mul_f32_e32 v13, 0xbfb8aa3b, v1
	v_exp_f32_e32 v12, v12
	v_exp_f32_e32 v13, v13
	v_add_f32_e32 v12, 1.0, v12
	v_add_f32_e32 v13, 1.0, v13
	v_rcp_f32_e32 v12, v12
	v_rcp_f32_e32 v13, v13
	s_nop 0
	v_pk_mul_f32 v[0:1], v[0:1], v[12:13]
	s_nop 0
	v_cvt_pk_bf16_f32 v12, v0, v1
	v_add_co_u32_e32 v0, vcc, s28, v10
	s_mov_b32 s28, 0x2e807000
	s_nop 0
	v_addc_co_u32_e32 v1, vcc, 0, v11, vcc
	global_store_dword v[0:1], v12, off offset:1024 sc1
	v_pk_add_f32 v[12:13], v[38:39], v[2:3] op_sel_hi:[1,0] neg_lo:[0,1] neg_hi:[0,1]
	v_mov_b32_e32 v2, v3
	v_pk_mul_f32 v[2:3], v[12:13], v[2:3] op_sel_hi:[1,0]
	s_nop 0
	v_pk_fma_f32 v[2:3], v[136:137], v[2:3], v[138:139]
	s_nop 0
	v_mul_f32_e32 v12, 0xbfb8aa3b, v2
	v_mul_f32_e32 v13, 0xbfb8aa3b, v3
	v_exp_f32_e32 v12, v12
	v_exp_f32_e32 v13, v13
	v_add_f32_e32 v12, 1.0, v12
	v_add_f32_e32 v13, 1.0, v13
	v_rcp_f32_e32 v12, v12
	v_rcp_f32_e32 v13, v13
	s_nop 0
	v_pk_mul_f32 v[2:3], v[2:3], v[12:13]
	s_nop 0
	v_cvt_pk_bf16_f32 v2, v2, v3
	global_store_dword v[0:1], v2, off offset:3072 sc1
	s_waitcnt lgkmcnt(0)
	v_pk_add_f32 v[0:1], v[44:45], v[4:5] op_sel_hi:[1,0] neg_lo:[0,1] neg_hi:[0,1]
	s_nop 0
	v_pk_mul_f32 v[0:1], v[0:1], v[4:5] op_sel:[0,1]
	v_mov_b32_e32 v4, v7
	v_pk_fma_f32 v[0:1], v[136:137], v[0:1], v[138:139]
	s_nop 0
	v_mul_f32_e32 v2, 0xbfb8aa3b, v0
	v_mul_f32_e32 v3, 0xbfb8aa3b, v1
	v_exp_f32_e32 v2, v2
	v_exp_f32_e32 v3, v3
	v_add_f32_e32 v2, 1.0, v2
	v_add_f32_e32 v3, 1.0, v3
	v_rcp_f32_e32 v2, v2
	v_rcp_f32_e32 v3, v3
	s_nop 0
	v_pk_mul_f32 v[0:1], v[0:1], v[2:3]
	s_nop 0
	v_cvt_pk_bf16_f32 v2, v0, v1
	v_add_co_u32_e32 v0, vcc, s28, v10
	s_nop 1
	v_addc_co_u32_e32 v1, vcc, 0, v11, vcc
	global_store_dword v[0:1], v2, off offset:1024 sc1
	v_pk_add_f32 v[2:3], v[8:9], v[6:7] op_sel_hi:[1,0] neg_lo:[0,1] neg_hi:[0,1]
	s_nop 0
	v_pk_mul_f32 v[2:3], v[2:3], v[4:5] op_sel_hi:[1,0]
	s_nop 0
	v_pk_fma_f32 v[2:3], v[136:137], v[2:3], v[138:139]
	s_nop 0
	v_mul_f32_e32 v4, 0xbfb8aa3b, v2
	v_mul_f32_e32 v5, 0xbfb8aa3b, v3
	v_exp_f32_e32 v4, v4
	v_exp_f32_e32 v5, v5
	v_add_f32_e32 v4, 1.0, v4
	v_add_f32_e32 v5, 1.0, v5
	v_rcp_f32_e32 v4, v4
	v_rcp_f32_e32 v5, v5
	s_nop 0
	v_pk_mul_f32 v[2:3], v[2:3], v[4:5]
	s_nop 0
	v_cvt_pk_bf16_f32 v2, v2, v3
	global_store_dword v[0:1], v2, off offset:3072 sc1
	s_cbranch_scc0 .LBB0_664

.LBB0_745:
	v_add_co_u32_e32 v172, vcc, 0x6801000, v164
	s_waitcnt vmcnt(15)
	v_cvt_f32_f16_sdwa v227, v175 dst_sel:DWORD dst_unused:UNUSED_PAD src0_sel:WORD_1
	v_cvt_f32_f16_sdwa v247, v174 dst_sel:DWORD dst_unused:UNUSED_PAD src0_sel:WORD_1
	v_cvt_f32_f16_e32 v246, v174
	v_cvt_f32_f16_e32 v226, v175
	v_addc_co_u32_e32 v173, vcc, 0, v165, vcc
	s_waitcnt vmcnt(14)
	v_lshlrev_b32_e32 v224, 16, v212
	v_and_b32_e32 v225, 0xffff0000, v212
	v_add_co_u32_e32 v212, vcc, s74, v164
	v_lshlrev_b32_e32 v174, 16, v213
	v_and_b32_e32 v175, 0xffff0000, v213
	v_addc_co_u32_e32 v213, vcc, 0, v165, vcc
	s_mov_b32 s8, 0x40101000
	v_pk_fma_f32 v[224:225], v[16:17], v[224:225], v[246:247]
	v_pk_fma_f32 v[174:175], v[18:19], v[174:175], v[226:227]
	v_add_co_u32_e32 v164, vcc, s8, v164
	v_cvt_pk_f16_f32 v227, v174, v175
	v_cvt_pk_f16_f32 v226, v224, v225
	v_addc_co_u32_e32 v165, vcc, 0, v165, vcc
	global_store_dwordx2 v[164:165], v[226:227], off offset:-4096 nt sc1
	v_pk_mul_f32 v[226:227], v[174:175], v[174:175]
	v_pk_mul_f32 v[246:247], v[224:225], v[224:225]
	v_cvt_f32_f16_sdwa v251, v208 dst_sel:DWORD dst_unused:UNUSED_PAD src0_sel:WORD_1
	v_pk_mov_b32 v[248:249], v[246:247], v[226:227] op_sel:[1,0]
	v_mov_b32_e32 v247, v227
	v_pk_add_f32 v[226:227], v[248:249], v[246:247]
	v_cvt_f32_f16_sdwa v249, v209 dst_sel:DWORD dst_unused:UNUSED_PAD src0_sel:WORD_1
	v_cvt_f32_f16_e32 v250, v208
	v_cvt_f32_f16_e32 v248, v209
	s_waitcnt vmcnt(14)
	v_lshlrev_b32_e32 v246, 16, v214
	v_and_b32_e32 v247, 0xffff0000, v214
	v_lshlrev_b32_e32 v208, 16, v215
	v_and_b32_e32 v209, 0xffff0000, v215
	v_pk_fma_f32 v[214:215], v[0:1], v[246:247], v[250:251]
	v_pk_fma_f32 v[208:209], v[2:3], v[208:209], v[248:249]
	v_cvt_pk_f16_f32 v246, v214, v215
	v_cvt_pk_f16_f32 v247, v208, v209
	global_store_dwordx2 v[212:213], v[246:247], off offset:512 nt sc1
	v_pk_mul_f32 v[246:247], v[208:209], v[208:209]
	v_pk_mul_f32 v[248:249], v[214:215], v[214:215]
	v_cvt_f32_f16_sdwa v253, v210 dst_sel:DWORD dst_unused:UNUSED_PAD src0_sel:WORD_1
	v_pk_mov_b32 v[250:251], v[248:249], v[246:247] op_sel:[1,0]
	v_mov_b32_e32 v249, v247
	v_pk_add_f32 v[246:247], v[250:251], v[248:249]
	v_cvt_f32_f16_sdwa v251, v211 dst_sel:DWORD dst_unused:UNUSED_PAD src0_sel:WORD_1
	v_cvt_f32_f16_e32 v250, v211
	v_cvt_f32_f16_e32 v252, v210
	s_waitcnt vmcnt(14)
	v_lshlrev_b32_e32 v210, 16, v219
	v_and_b32_e32 v211, 0xffff0000, v219
	v_lshlrev_b32_e32 v248, 16, v218
	v_and_b32_e32 v249, 0xffff0000, v218
	v_pk_fma_f32 v[210:211], v[26:27], v[210:211], v[250:251]
	v_cvt_f32_f16_sdwa v251, v216 dst_sel:DWORD dst_unused:UNUSED_PAD src0_sel:WORD_1
	v_cvt_f32_f16_e32 v250, v216
	v_pk_fma_f32 v[218:219], v[24:25], v[248:249], v[252:253]
	v_cvt_pk_f16_f32 v249, v210, v211
	v_cvt_pk_f16_f32 v248, v218, v219
	global_store_dwordx2 v[212:213], v[248:249], off offset:1024 nt sc1
	s_waitcnt vmcnt(14)
	v_lshlrev_b32_e32 v248, 16, v220
	v_and_b32_e32 v249, 0xffff0000, v220
	v_cvt_f32_f16_sdwa v253, v217 dst_sel:DWORD dst_unused:UNUSED_PAD src0_sel:WORD_1
	v_cvt_f32_f16_e32 v252, v217
	v_lshlrev_b32_e32 v216, 16, v221
	v_and_b32_e32 v217, 0xffff0000, v221
	v_pk_fma_f32 v[220:221], v[28:29], v[248:249], v[250:251]
	v_pk_add_f32 v[226:227], v[226:227], v[226:227] op_sel:[0,1] op_sel_hi:[1,0]
	v_mul_f32_e32 v64, v220, v220
	v_mul_f32_e32 v223, v221, v221
	v_pk_add_f32 v[246:247], v[246:247], v[246:247] op_sel:[0,1] op_sel_hi:[1,0]
	v_mov_b32_e32 v227, v64
	v_mov_b32_e32 v247, v223
	v_mul_f32_e32 v64, v219, v219
	v_pk_fma_f32 v[216:217], v[30:31], v[216:217], v[252:253]
	v_pk_add_f32 v[226:227], v[226:227], v[246:247]
	v_pk_fma_f32 v[246:247], v[218:219], v[218:219], v[64:65] op_sel_hi:[1,1,0]
	v_mul_f32_e32 v64, v211, v211
	v_mul_f32_e32 v245, v216, v216
	v_mul_f32_e32 v248, v217, v217
	v_pk_fma_f32 v[250:251], v[210:211], v[210:211], v[64:65] op_sel_hi:[1,1,0]
	v_mov_b32_e32 v247, v245
	v_mov_b32_e32 v251, v248
	v_pk_add_f32 v[246:247], v[246:247], v[250:251]
	v_cvt_pk_f16_f32 v249, v216, v217
	v_pk_add_f32 v[226:227], v[226:227], v[246:247]
	v_cvt_pk_f16_f32 v248, v220, v221
	v_add_f32_e32 v64, v226, v227
	global_store_dwordx2 v[212:213], v[248:249], off offset:1536 nt sc1
	v_mov_b32_e32 v223, v65
	v_add_f32_dpp v64, v64, v64 quad_perm:[1,0,3,2] row_mask:0xf bank_mask:0xf bound_ctrl:1
	v_lshl_add_u64 v[246:247], s[42:43], 0, v[150:151]
	global_load_dwordx2 v[172:173], v[172:173], off offset:3584
	v_add_f32_dpp v64, v64, v64 quad_perm:[2,3,0,1] row_mask:0xf bank_mask:0xf bound_ctrl:1
	v_mov_b32_e32 v245, v65
	s_nop 0
	v_add_f32_dpp v64, v64, v64 row_half_mirror row_mask:0xf bank_mask:0xf bound_ctrl:1
	s_nop 1
	v_add_f32_dpp v64, v64, v64 row_mirror row_mask:0xf bank_mask:0xf bound_ctrl:1
	s_nop 0
	v_readlane_b32 s10, v64, 16
	v_readlane_b32 s11, v64, 48
	v_readlane_b32 s8, v64, 0
	v_readlane_b32 s9, v64, 32
	v_mov_b32_e32 v226, s10
	v_mov_b32_e32 v227, s11
	v_pk_add_f32 v[226:227], s[8:9], v[226:227]
	s_mov_b32 s8, 0x36800000
	v_add_f32_e32 v64, v226, v227
	v_fmamk_f32 v64, v64, 0x3a800000, v229
	v_rsq_f32_e32 v226, v64
	s_nop 0
	v_pk_mul_f32 v[224:225], v[224:225], v[226:227] op_sel_hi:[1,0]
	v_pk_mul_f32 v[174:175], v[174:175], v[226:227] op_sel_hi:[1,0]
	v_pk_fma_f32 v[224:225], v[134:135], v[224:225], v[4:5]
	v_pk_fma_f32 v[248:249], v[132:133], v[174:175], v[6:7]
	v_med3_f32 v64, v224, s55, v228
	v_med3_f32 v174, v225, s55, v228
	v_cvt_pk_fp8_f32 v223, v64, v174
	v_med3_f32 v64, v248, s55, v228
	v_med3_f32 v174, v249, s55, v228
	v_cvt_pk_bf16_f32 v250, v224, v225
	v_cvt_pk_fp8_f32 v223, v64, v174 op_sel:[0,0,1]
	v_add_co_u32_e32 v174, vcc, s8, v246
	v_cvt_pk_bf16_f32 v251, v248, v249
	s_nop 0
	v_addc_co_u32_e32 v175, vcc, 0, v247, vcc
	v_lshlrev_b32_e32 v246, 16, v250
	v_and_b32_e32 v247, 0xffff0000, v250
	v_pk_add_f32 v[224:225], v[224:225], v[246:247] neg_lo:[0,1] neg_hi:[0,1]
	v_lshlrev_b32_e32 v246, 16, v251
	v_and_b32_e32 v247, 0xffff0000, v251
	v_pk_mul_f32 v[214:215], v[214:215], v[226:227] op_sel_hi:[1,0]
	v_pk_add_f32 v[246:247], v[248:249], v[246:247] neg_lo:[0,1] neg_hi:[0,1]
	v_pk_mul_f32 v[208:209], v[208:209], v[226:227] op_sel_hi:[1,0]
	v_pk_fma_f32 v[214:215], v[138:139], v[214:215], v[8:9]
	v_cvt_pk_bf16_f32 v224, v224, v225
	v_cvt_pk_bf16_f32 v225, v246, v247
	v_pk_fma_f32 v[208:209], v[136:137], v[208:209], v[10:11]
	v_cvt_pk_bf16_f32 v246, v214, v215
	global_store_dword v[174:175], v223, off sc1
	v_med3_f32 v223, v214, s55, v228
	v_med3_f32 v227, v215, s55, v228
	v_cvt_pk_bf16_f32 v247, v208, v209
	v_lshlrev_b32_e32 v248, 16, v246
	v_and_b32_e32 v249, 0xffff0000, v246
	v_cvt_pk_fp8_f32 v245, v223, v227
	v_pk_add_f32 v[214:215], v[214:215], v[248:249] neg_lo:[0,1] neg_hi:[0,1]
	v_lshlrev_b32_e32 v248, 16, v247
	v_and_b32_e32 v249, 0xffff0000, v247
	v_med3_f32 v223, v208, s55, v228
	v_med3_f32 v227, v209, s55, v228
	v_pk_add_f32 v[208:209], v[208:209], v[248:249] neg_lo:[0,1] neg_hi:[0,1]
	v_cvt_pk_bf16_f32 v214, v214, v215
	v_cvt_pk_bf16_f32 v215, v208, v209
	v_pk_mul_f32 v[208:209], v[218:219], v[226:227] op_sel_hi:[1,0]
	v_cvt_pk_fp8_f32 v245, v223, v227 op_sel:[0,0,1]
	v_pk_fma_f32 v[208:209], v[142:143], v[208:209], v[20:21]
	v_pk_mul_f32 v[210:211], v[210:211], v[226:227] op_sel_hi:[1,0]
	v_med3_f32 v218, v208, s55, v228
	v_med3_f32 v219, v209, s55, v228
	v_mov_b32_e32 v227, v65
	v_cvt_pk_fp8_f32 v227, v218, v219
	v_pk_fma_f32 v[210:211], v[140:141], v[210:211], v[22:23]
	v_add_u32_e32 v223, s28, v131
	v_med3_f32 v218, v210, s55, v228
	v_med3_f32 v219, v211, s55, v228
	v_cvt_pk_fp8_f32 v227, v218, v219 op_sel:[0,0,1]
	ds_write2st64_b64 v223, v[224:225], v[214:215] offset1:1
	v_cvt_pk_bf16_f32 v214, v208, v209
	v_cvt_pk_bf16_f32 v215, v210, v211
	v_lshlrev_b32_e32 v218, 16, v214
	v_and_b32_e32 v219, 0xffff0000, v214
	v_pk_add_f32 v[208:209], v[208:209], v[218:219] neg_lo:[0,1] neg_hi:[0,1]
	v_lshlrev_b32_e32 v218, 16, v215
	v_and_b32_e32 v219, 0xffff0000, v215
	v_pk_add_f32 v[210:211], v[210:211], v[218:219] neg_lo:[0,1] neg_hi:[0,1]
	v_pk_mul_f32 v[218:219], v[220:221], v[226:227] op_sel_hi:[1,0]
	v_cvt_pk_bf16_f32 v208, v208, v209
	v_pk_fma_f32 v[218:219], v[146:147], v[218:219], v[12:13]
	v_mov_b32_e32 v221, v65
	v_med3_f32 v209, v218, s55, v228
	v_med3_f32 v220, v219, s55, v228
	v_cvt_pk_fp8_f32 v221, v209, v220
	v_pk_mul_f32 v[216:217], v[216:217], v[226:227] op_sel_hi:[1,0]
	v_add_u32_e32 v64, s27, v131
	v_pk_fma_f32 v[216:217], v[144:145], v[216:217], v[14:15]
	global_store_dword v[174:175], v245, off offset:256 sc1
	v_med3_f32 v209, v216, s55, v228
	v_med3_f32 v220, v217, s55, v228
	v_cvt_pk_fp8_f32 v221, v209, v220 op_sel:[0,0,1]
	v_cvt_pk_bf16_f32 v209, v210, v211
	v_cvt_pk_bf16_f32 v210, v218, v219
	v_cvt_pk_bf16_f32 v211, v216, v217
	global_store_dword v[174:175], v221, off offset:768 sc1
	v_lshlrev_b32_e32 v220, 16, v210
	v_and_b32_e32 v221, 0xffff0000, v210
	v_pk_add_f32 v[218:219], v[218:219], v[220:221] neg_lo:[0,1] neg_hi:[0,1]
	v_lshlrev_b32_e32 v220, 16, v211
	v_and_b32_e32 v221, 0xffff0000, v211
	v_pk_add_f32 v[216:217], v[216:217], v[220:221] neg_lo:[0,1] neg_hi:[0,1]
	ds_write2st64_b64 v64, v[250:251], v[246:247] offset1:1
	global_store_dword v[174:175], v227, off offset:512 sc1
	v_cvt_pk_bf16_f32 v218, v218, v219
	v_cvt_pk_bf16_f32 v219, v216, v217
	ds_write2st64_b64 v64, v[214:215], v[210:211] offset0:2 offset1:3
	ds_write2st64_b64 v223, v[208:209], v[218:219] offset0:2 offset1:3
	v_cvt_f32_f16_sdwa v211, v193 dst_sel:DWORD dst_unused:UNUSED_PAD src0_sel:WORD_1
	v_cvt_f32_f16_sdwa v215, v192 dst_sel:DWORD dst_unused:UNUSED_PAD src0_sel:WORD_1
	v_cvt_f32_f16_e32 v214, v192
	v_cvt_f32_f16_e32 v210, v193
	s_waitcnt vmcnt(19)
	v_lshlrev_b32_e32 v208, 16, v196
	v_and_b32_e32 v209, 0xffff0000, v196
	v_lshlrev_b32_e32 v192, 16, v197
	v_and_b32_e32 v193, 0xffff0000, v197
	v_pk_fma_f32 v[196:197], v[16:17], v[208:209], v[214:215]
	v_pk_fma_f32 v[192:193], v[18:19], v[192:193], v[210:211]
	v_cvt_pk_f16_f32 v208, v196, v197
	v_cvt_pk_f16_f32 v209, v192, v193
	global_store_dwordx2 v[212:213], v[208:209], off offset:2048 nt sc1
	v_pk_mul_f32 v[208:209], v[192:193], v[192:193]
	v_pk_mul_f32 v[210:211], v[196:197], v[196:197]
	v_cvt_f32_f16_sdwa v217, v194 dst_sel:DWORD dst_unused:UNUSED_PAD src0_sel:WORD_1
	v_pk_mov_b32 v[214:215], v[210:211], v[208:209] op_sel:[1,0]
	v_mov_b32_e32 v211, v209
	v_pk_add_f32 v[208:209], v[214:215], v[210:211]
	v_cvt_f32_f16_sdwa v215, v195 dst_sel:DWORD dst_unused:UNUSED_PAD src0_sel:WORD_1
	v_cvt_f32_f16_e32 v216, v194
	v_cvt_f32_f16_e32 v214, v195
	s_waitcnt vmcnt(19)
	v_lshlrev_b32_e32 v210, 16, v200
	v_and_b32_e32 v211, 0xffff0000, v200
	v_lshlrev_b32_e32 v194, 16, v201
	v_and_b32_e32 v195, 0xffff0000, v201
	v_pk_fma_f32 v[200:201], v[0:1], v[210:211], v[216:217]
	v_pk_fma_f32 v[194:195], v[2:3], v[194:195], v[214:215]
	v_cvt_pk_f16_f32 v210, v200, v201
	v_cvt_pk_f16_f32 v211, v194, v195
	v_cvt_f32_f16_sdwa v219, v198 dst_sel:DWORD dst_unused:UNUSED_PAD src0_sel:WORD_1
	v_cvt_f32_f16_e32 v218, v198
	global_store_dwordx2 v[212:213], v[210:211], off offset:2560 nt sc1
	v_pk_mul_f32 v[210:211], v[194:195], v[194:195]
	v_pk_mul_f32 v[214:215], v[200:201], v[200:201]
	s_waitcnt vmcnt(19)
	v_lshlrev_b32_e32 v198, 16, v205
	v_pk_mov_b32 v[216:217], v[214:215], v[210:211] op_sel:[1,0]
	v_mov_b32_e32 v215, v211
	v_pk_add_f32 v[210:211], v[216:217], v[214:215]
	v_lshlrev_b32_e32 v214, 16, v204
	v_and_b32_e32 v215, 0xffff0000, v204
	v_cvt_f32_f16_sdwa v217, v199 dst_sel:DWORD dst_unused:UNUSED_PAD src0_sel:WORD_1
	v_cvt_f32_f16_e32 v216, v199
	v_and_b32_e32 v199, 0xffff0000, v205
	v_pk_fma_f32 v[204:205], v[24:25], v[214:215], v[218:219]
	v_cvt_f32_f16_sdwa v219, v202 dst_sel:DWORD dst_unused:UNUSED_PAD src0_sel:WORD_1
	v_cvt_f32_f16_e32 v218, v202
	v_pk_fma_f32 v[198:199], v[26:27], v[198:199], v[216:217]
	s_waitcnt vmcnt(18)
	v_lshlrev_b32_e32 v216, 16, v206
	v_and_b32_e32 v217, 0xffff0000, v206
	v_cvt_f32_f16_sdwa v221, v203 dst_sel:DWORD dst_unused:UNUSED_PAD src0_sel:WORD_1
	v_cvt_f32_f16_e32 v220, v203
	v_lshlrev_b32_e32 v202, 16, v207
	v_and_b32_e32 v203, 0xffff0000, v207
	v_pk_fma_f32 v[206:207], v[28:29], v[216:217], v[218:219]
	v_pk_add_f32 v[208:209], v[208:209], v[208:209] op_sel:[0,1] op_sel_hi:[1,0]
	v_mul_f32_e32 v216, v206, v206
	v_mul_f32_e32 v217, v207, v207
	v_pk_add_f32 v[210:211], v[210:211], v[210:211] op_sel:[0,1] op_sel_hi:[1,0]
	v_mov_b32_e32 v209, v216
	v_mov_b32_e32 v211, v217
	v_pk_fma_f32 v[202:203], v[30:31], v[202:203], v[220:221]
	v_pk_add_f32 v[208:209], v[208:209], v[210:211]
	v_mul_f32_e32 v210, v205, v205
	v_mul_f32_e32 v216, v199, v199
	v_mul_f32_e32 v218, v202, v202
	v_mul_f32_e32 v219, v203, v203
	v_pk_fma_f32 v[210:211], v[204:205], v[204:205], v[210:211] op_sel_hi:[1,1,0]
	v_pk_fma_f32 v[216:217], v[198:199], v[198:199], v[216:217] op_sel_hi:[1,1,0]
	v_mov_b32_e32 v211, v218
	v_mov_b32_e32 v217, v219
	v_pk_add_f32 v[210:211], v[210:211], v[216:217]
	v_cvt_pk_f16_f32 v215, v198, v199
	v_pk_add_f32 v[208:209], v[208:209], v[210:211]
	v_cvt_pk_f16_f32 v214, v204, v205
	v_add_f32_e32 v208, v208, v209
	global_store_dwordx2 v[212:213], v[214:215], off offset:3072 nt sc1
	v_mov_b32_e32 v215, v65
	v_add_f32_dpp v208, v208, v208 quad_perm:[1,0,3,2] row_mask:0xf bank_mask:0xf bound_ctrl:1
	v_cvt_pk_f16_f32 v211, v202, v203
	v_cvt_pk_f16_f32 v210, v206, v207
	v_add_f32_dpp v208, v208, v208 quad_perm:[2,3,0,1] row_mask:0xf bank_mask:0xf bound_ctrl:1
	global_store_dwordx2 v[212:213], v[210:211], off offset:3584 nt sc1
	s_nop 0
	v_add_f32_dpp v208, v208, v208 row_half_mirror row_mask:0xf bank_mask:0xf bound_ctrl:1
	s_nop 1
	v_add_f32_dpp v208, v208, v208 row_mirror row_mask:0xf bank_mask:0xf bound_ctrl:1
	s_nop 0
	v_readlane_b32 s10, v208, 16
	v_readlane_b32 s11, v208, 48
	v_readlane_b32 s8, v208, 0
	v_readlane_b32 s9, v208, 32
	v_mov_b32_e32 v208, s10
	v_mov_b32_e32 v209, s11
	v_pk_add_f32 v[208:209], s[8:9], v[208:209]
	s_nop 0
	v_add_f32_e32 v208, v208, v209
	v_fmamk_f32 v208, v208, 0x3a800000, v229
	v_rsq_f32_e32 v208, v208
	s_nop 0
	v_pk_mul_f32 v[196:197], v[196:197], v[208:209] op_sel_hi:[1,0]
	s_nop 0
	v_pk_fma_f32 v[196:197], v[134:135], v[196:197], v[4:5]
	v_pk_mul_f32 v[192:193], v[192:193], v[208:209] op_sel_hi:[1,0]
	v_med3_f32 v209, v196, s55, v228
	v_med3_f32 v214, v197, s55, v228
	v_cvt_pk_fp8_f32 v215, v209, v214
	v_pk_fma_f32 v[192:193], v[132:133], v[192:193], v[6:7]
	v_cvt_pk_bf16_f32 v210, v196, v197
	v_cvt_pk_bf16_f32 v211, v192, v193
	v_lshlrev_b32_e32 v212, 16, v210
	v_and_b32_e32 v213, 0xffff0000, v210
	v_med3_f32 v209, v192, s55, v228
	v_med3_f32 v214, v193, s55, v228
	v_pk_add_f32 v[196:197], v[196:197], v[212:213] neg_lo:[0,1] neg_hi:[0,1]
	v_lshlrev_b32_e32 v212, 16, v211
	v_and_b32_e32 v213, 0xffff0000, v211
	v_cvt_pk_fp8_f32 v215, v209, v214 op_sel:[0,0,1]
	v_pk_add_f32 v[192:193], v[192:193], v[212:213] neg_lo:[0,1] neg_hi:[0,1]
	v_add_u32_e32 v209, s24, v236
	v_cvt_pk_bf16_f32 v196, v196, v197
	v_cvt_pk_bf16_f32 v197, v192, v193
	v_pk_mul_f32 v[192:193], v[200:201], v[208:209] op_sel_hi:[1,0]
	v_mov_b32_e32 v212, v65
	v_pk_fma_f32 v[192:193], v[138:139], v[192:193], v[8:9]
	v_pk_mul_f32 v[194:195], v[194:195], v[208:209] op_sel_hi:[1,0]
	v_med3_f32 v200, v192, s55, v228
	v_med3_f32 v201, v193, s55, v228
	v_cvt_pk_fp8_f32 v212, v200, v201
	v_pk_fma_f32 v[194:195], v[136:137], v[194:195], v[10:11]
	ds_write_b64 v209, v[196:197]
	v_med3_f32 v200, v194, s55, v228
	v_med3_f32 v201, v195, s55, v228
	v_cvt_pk_bf16_f32 v196, v192, v193
	v_cvt_pk_fp8_f32 v212, v200, v201 op_sel:[0,0,1]
	v_cvt_pk_bf16_f32 v197, v194, v195
	v_lshlrev_b32_e32 v200, 16, v196
	v_and_b32_e32 v201, 0xffff0000, v196
	v_pk_add_f32 v[192:193], v[192:193], v[200:201] neg_lo:[0,1] neg_hi:[0,1]
	v_lshlrev_b32_e32 v200, 16, v197
	v_and_b32_e32 v201, 0xffff0000, v197
	v_pk_add_f32 v[194:195], v[194:195], v[200:201] neg_lo:[0,1] neg_hi:[0,1]
	v_add_u32_e32 v209, 16, v64
	v_cvt_pk_bf16_f32 v192, v192, v193
	v_cvt_pk_bf16_f32 v193, v194, v195
	v_pk_mul_f32 v[194:195], v[204:205], v[208:209] op_sel_hi:[1,0]
	ds_write2st64_b64 v209, v[210:211], v[196:197] offset0:4 offset1:5
	v_pk_fma_f32 v[194:195], v[142:143], v[194:195], v[20:21]
	v_pk_mul_f32 v[196:197], v[198:199], v[208:209] op_sel_hi:[1,0]
	v_med3_f32 v198, v194, s55, v228
	v_med3_f32 v199, v195, s55, v228
	v_mov_b32_e32 v200, v65
	v_cvt_pk_fp8_f32 v200, v198, v199
	v_pk_fma_f32 v[196:197], v[140:141], v[196:197], v[22:23]
	v_mov_b32_e32 v205, v65
	v_med3_f32 v198, v196, s55, v228
	v_med3_f32 v199, v197, s55, v228
	v_cvt_pk_fp8_f32 v200, v198, v199 op_sel:[0,0,1]
	v_cvt_pk_bf16_f32 v198, v194, v195
	v_cvt_pk_bf16_f32 v199, v196, v197
	v_and_b32_e32 v201, 0xffff0000, v198
	global_store_dword v[174:175], v200, off offset:1536 sc1
	v_lshlrev_b32_e32 v200, 16, v198
	v_pk_add_f32 v[194:195], v[194:195], v[200:201] neg_lo:[0,1] neg_hi:[0,1]
	v_lshlrev_b32_e32 v200, 16, v199
	v_and_b32_e32 v201, 0xffff0000, v199
	v_pk_add_f32 v[196:197], v[196:197], v[200:201] neg_lo:[0,1] neg_hi:[0,1]
	v_cvt_pk_bf16_f32 v194, v194, v195
	v_cvt_pk_bf16_f32 v195, v196, v197
	v_pk_mul_f32 v[196:197], v[206:207], v[208:209] op_sel_hi:[1,0]
	v_pk_mul_f32 v[200:201], v[202:203], v[208:209] op_sel_hi:[1,0]
	v_pk_fma_f32 v[196:197], v[146:147], v[196:197], v[12:13]
	v_add_u32_e32 v204, s29, v131
	v_med3_f32 v202, v196, s55, v228
	v_med3_f32 v203, v197, s55, v228
	v_cvt_pk_fp8_f32 v205, v202, v203
	v_pk_fma_f32 v[200:201], v[144:145], v[200:201], v[14:15]
	ds_write2st64_b64 v204, v[192:193], v[194:195] offset0:1 offset1:2
	v_med3_f32 v202, v200, s55, v228
	v_med3_f32 v203, v201, s55, v228
	v_cvt_pk_bf16_f32 v192, v196, v197
	v_cvt_pk_fp8_f32 v205, v202, v203 op_sel:[0,0,1]
	v_cvt_pk_bf16_f32 v193, v200, v201
	v_lshlrev_b32_e32 v194, 16, v192
	v_and_b32_e32 v195, 0xffff0000, v192
	v_pk_add_f32 v[194:195], v[196:197], v[194:195] neg_lo:[0,1] neg_hi:[0,1]
	v_lshlrev_b32_e32 v196, 16, v193
	v_and_b32_e32 v197, 0xffff0000, v193
	v_pk_add_f32 v[196:197], v[200:201], v[196:197] neg_lo:[0,1] neg_hi:[0,1]
	v_cvt_pk_bf16_f32 v194, v194, v195
	v_cvt_pk_bf16_f32 v195, v196, v197
	global_store_dword v[174:175], v215, off offset:1024 sc1
	global_store_dword v[174:175], v212, off offset:1280 sc1
	global_store_dword v[174:175], v205, off offset:1792 sc1
	ds_write2st64_b64 v209, v[198:199], v[192:193] offset0:6 offset1:7
	ds_write_b64 v204, v[194:195] offset:1536
	v_cvt_f32_f16_sdwa v195, v177 dst_sel:DWORD dst_unused:UNUSED_PAD src0_sel:WORD_1
	v_cvt_f32_f16_sdwa v197, v176 dst_sel:DWORD dst_unused:UNUSED_PAD src0_sel:WORD_1
	v_cvt_f32_f16_e32 v196, v176
	v_cvt_f32_f16_e32 v194, v177
	s_waitcnt vmcnt(23)
	v_lshlrev_b32_e32 v192, 16, v180
	v_and_b32_e32 v193, 0xffff0000, v180
	v_lshlrev_b32_e32 v176, 16, v181
	v_and_b32_e32 v177, 0xffff0000, v181
	v_pk_fma_f32 v[180:181], v[16:17], v[192:193], v[196:197]
	v_pk_fma_f32 v[176:177], v[18:19], v[176:177], v[194:195]
	v_cvt_pk_f16_f32 v192, v180, v181
	v_cvt_pk_f16_f32 v193, v176, v177
	global_store_dwordx2 v[164:165], v[192:193], off nt sc1
	v_pk_mul_f32 v[192:193], v[176:177], v[176:177]
	v_pk_mul_f32 v[194:195], v[180:181], v[180:181]
	v_cvt_f32_f16_sdwa v199, v178 dst_sel:DWORD dst_unused:UNUSED_PAD src0_sel:WORD_1
	v_pk_mov_b32 v[196:197], v[194:195], v[192:193] op_sel:[1,0]
	v_mov_b32_e32 v195, v193
	v_pk_add_f32 v[192:193], v[196:197], v[194:195]
	v_cvt_f32_f16_sdwa v197, v179 dst_sel:DWORD dst_unused:UNUSED_PAD src0_sel:WORD_1
	v_cvt_f32_f16_e32 v198, v178
	v_cvt_f32_f16_e32 v196, v179
	s_waitcnt vmcnt(23)
	v_lshlrev_b32_e32 v194, 16, v184
	v_and_b32_e32 v195, 0xffff0000, v184
	v_lshlrev_b32_e32 v178, 16, v185
	v_and_b32_e32 v179, 0xffff0000, v185
	v_pk_fma_f32 v[184:185], v[0:1], v[194:195], v[198:199]
	v_pk_fma_f32 v[178:179], v[2:3], v[178:179], v[196:197]
	v_cvt_pk_f16_f32 v194, v184, v185
	v_cvt_pk_f16_f32 v195, v178, v179
	v_cvt_f32_f16_sdwa v201, v182 dst_sel:DWORD dst_unused:UNUSED_PAD src0_sel:WORD_1
	v_cvt_f32_f16_e32 v200, v182
	global_store_dwordx2 v[164:165], v[194:195], off offset:512 nt sc1
	v_pk_mul_f32 v[194:195], v[178:179], v[178:179]
	v_pk_mul_f32 v[196:197], v[184:185], v[184:185]
	s_waitcnt vmcnt(23)
	v_lshlrev_b32_e32 v182, 16, v189
	v_pk_mov_b32 v[198:199], v[196:197], v[194:195] op_sel:[1,0]
	v_mov_b32_e32 v197, v195
	v_pk_add_f32 v[194:195], v[198:199], v[196:197]
	v_lshlrev_b32_e32 v196, 16, v188
	v_and_b32_e32 v197, 0xffff0000, v188
	v_cvt_f32_f16_sdwa v199, v183 dst_sel:DWORD dst_unused:UNUSED_PAD src0_sel:WORD_1
	v_cvt_f32_f16_e32 v198, v183
	v_and_b32_e32 v183, 0xffff0000, v189
	v_pk_fma_f32 v[188:189], v[24:25], v[196:197], v[200:201]
	v_cvt_f32_f16_sdwa v201, v186 dst_sel:DWORD dst_unused:UNUSED_PAD src0_sel:WORD_1
	v_cvt_f32_f16_e32 v200, v186
	v_pk_fma_f32 v[182:183], v[26:27], v[182:183], v[198:199]
	s_waitcnt vmcnt(22)
	v_lshlrev_b32_e32 v198, 16, v190
	v_and_b32_e32 v199, 0xffff0000, v190
	v_cvt_f32_f16_sdwa v203, v187 dst_sel:DWORD dst_unused:UNUSED_PAD src0_sel:WORD_1
	v_cvt_f32_f16_e32 v202, v187
	v_lshlrev_b32_e32 v186, 16, v191
	v_and_b32_e32 v187, 0xffff0000, v191
	v_pk_fma_f32 v[190:191], v[28:29], v[198:199], v[200:201]
	v_pk_add_f32 v[192:193], v[192:193], v[192:193] op_sel:[0,1] op_sel_hi:[1,0]
	v_mul_f32_e32 v198, v190, v190
	v_mul_f32_e32 v199, v191, v191
	v_pk_add_f32 v[194:195], v[194:195], v[194:195] op_sel:[0,1] op_sel_hi:[1,0]
	v_mov_b32_e32 v193, v198
	v_mov_b32_e32 v195, v199
	v_pk_fma_f32 v[186:187], v[30:31], v[186:187], v[202:203]
	v_pk_add_f32 v[192:193], v[192:193], v[194:195]
	v_mul_f32_e32 v194, v189, v189
	v_mul_f32_e32 v198, v183, v183
	v_mul_f32_e32 v200, v186, v186
	v_mul_f32_e32 v201, v187, v187
	v_pk_fma_f32 v[194:195], v[188:189], v[188:189], v[194:195] op_sel_hi:[1,1,0]
	v_pk_fma_f32 v[198:199], v[182:183], v[182:183], v[198:199] op_sel_hi:[1,1,0]
	v_mov_b32_e32 v195, v200
	v_mov_b32_e32 v199, v201
	v_pk_add_f32 v[194:195], v[194:195], v[198:199]
	v_cvt_pk_f16_f32 v197, v182, v183
	v_pk_add_f32 v[192:193], v[192:193], v[194:195]
	v_cvt_pk_f16_f32 v196, v188, v189
	v_add_f32_e32 v192, v192, v193
	global_store_dwordx2 v[164:165], v[196:197], off offset:1024 nt sc1
	v_mov_b32_e32 v197, v65
	v_add_f32_dpp v192, v192, v192 quad_perm:[1,0,3,2] row_mask:0xf bank_mask:0xf bound_ctrl:1
	v_cvt_pk_f16_f32 v195, v186, v187
	v_cvt_pk_f16_f32 v194, v190, v191
	v_add_f32_dpp v192, v192, v192 quad_perm:[2,3,0,1] row_mask:0xf bank_mask:0xf bound_ctrl:1
	global_store_dwordx2 v[164:165], v[194:195], off offset:1536 nt sc1
	s_nop 0
	v_add_f32_dpp v192, v192, v192 row_half_mirror row_mask:0xf bank_mask:0xf bound_ctrl:1
	s_nop 1
	v_add_f32_dpp v192, v192, v192 row_mirror row_mask:0xf bank_mask:0xf bound_ctrl:1
	s_nop 0
	v_readlane_b32 s10, v192, 16
	v_readlane_b32 s11, v192, 48
	v_readlane_b32 s8, v192, 0
	v_readlane_b32 s9, v192, 32
	v_mov_b32_e32 v192, s10
	v_mov_b32_e32 v193, s11
	v_pk_add_f32 v[192:193], s[8:9], v[192:193]
	s_nop 0
	v_add_f32_e32 v192, v192, v193
	v_fmamk_f32 v192, v192, 0x3a800000, v229
	v_rsq_f32_e32 v192, v192
	s_nop 0
	v_pk_mul_f32 v[180:181], v[180:181], v[192:193] op_sel_hi:[1,0]
	s_nop 0
	v_pk_fma_f32 v[180:181], v[134:135], v[180:181], v[4:5]
	v_pk_mul_f32 v[176:177], v[176:177], v[192:193] op_sel_hi:[1,0]
	v_med3_f32 v193, v180, s55, v228
	v_med3_f32 v196, v181, s55, v228
	v_cvt_pk_fp8_f32 v197, v193, v196
	v_pk_fma_f32 v[176:177], v[132:133], v[176:177], v[6:7]
	v_cvt_pk_bf16_f32 v194, v180, v181
	v_med3_f32 v193, v176, s55, v228
	v_med3_f32 v196, v177, s55, v228
	v_cvt_pk_fp8_f32 v197, v193, v196 op_sel:[0,0,1]
	v_cvt_pk_bf16_f32 v195, v176, v177
	v_lshlrev_b32_e32 v196, 16, v194
	v_add_u32_e32 v193, s25, v236
	global_store_dword v[174:175], v197, off offset:2048 sc1
	v_and_b32_e32 v197, 0xffff0000, v194
	v_pk_add_f32 v[180:181], v[180:181], v[196:197] neg_lo:[0,1] neg_hi:[0,1]
	v_lshlrev_b32_e32 v196, 16, v195
	v_and_b32_e32 v197, 0xffff0000, v195
	v_pk_add_f32 v[176:177], v[176:177], v[196:197] neg_lo:[0,1] neg_hi:[0,1]
	v_cvt_pk_bf16_f32 v180, v180, v181
	v_cvt_pk_bf16_f32 v181, v176, v177
	v_pk_mul_f32 v[176:177], v[184:185], v[192:193] op_sel_hi:[1,0]
	v_mov_b32_e32 v196, v65
	v_pk_fma_f32 v[176:177], v[138:139], v[176:177], v[8:9]
	v_pk_mul_f32 v[178:179], v[178:179], v[192:193] op_sel_hi:[1,0]
	v_med3_f32 v184, v176, s55, v228
	v_med3_f32 v185, v177, s55, v228
	v_cvt_pk_fp8_f32 v196, v184, v185
	v_pk_fma_f32 v[178:179], v[136:137], v[178:179], v[10:11]
	ds_write_b64 v193, v[180:181]
	v_med3_f32 v184, v178, s55, v228
	v_med3_f32 v185, v179, s55, v228
	v_cvt_pk_bf16_f32 v180, v176, v177
	v_cvt_pk_fp8_f32 v196, v184, v185 op_sel:[0,0,1]
	v_cvt_pk_bf16_f32 v181, v178, v179
	v_lshlrev_b32_e32 v184, 16, v180
	v_and_b32_e32 v185, 0xffff0000, v180
	v_pk_add_f32 v[176:177], v[176:177], v[184:185] neg_lo:[0,1] neg_hi:[0,1]
	v_lshlrev_b32_e32 v184, 16, v181
	v_and_b32_e32 v185, 0xffff0000, v181
	v_pk_add_f32 v[178:179], v[178:179], v[184:185] neg_lo:[0,1] neg_hi:[0,1]
	v_add_u32_e32 v193, 32, v64
	v_cvt_pk_bf16_f32 v176, v176, v177
	v_cvt_pk_bf16_f32 v177, v178, v179
	v_pk_mul_f32 v[178:179], v[188:189], v[192:193] op_sel_hi:[1,0]
	ds_write2st64_b64 v193, v[194:195], v[180:181] offset0:8 offset1:9
	v_pk_fma_f32 v[178:179], v[142:143], v[178:179], v[20:21]
	v_pk_mul_f32 v[180:181], v[182:183], v[192:193] op_sel_hi:[1,0]
	v_med3_f32 v182, v178, s55, v228
	v_med3_f32 v183, v179, s55, v228
	v_mov_b32_e32 v184, v65
	v_cvt_pk_fp8_f32 v184, v182, v183
	v_pk_fma_f32 v[180:181], v[140:141], v[180:181], v[22:23]
	v_mov_b32_e32 v189, v65
	v_med3_f32 v182, v180, s55, v228
	v_med3_f32 v183, v181, s55, v228
	v_cvt_pk_fp8_f32 v184, v182, v183 op_sel:[0,0,1]
	v_cvt_pk_bf16_f32 v182, v178, v179
	v_cvt_pk_bf16_f32 v183, v180, v181
	v_and_b32_e32 v185, 0xffff0000, v182
	global_store_dword v[174:175], v184, off offset:2560 sc1
	v_lshlrev_b32_e32 v184, 16, v182
	v_pk_add_f32 v[178:179], v[178:179], v[184:185] neg_lo:[0,1] neg_hi:[0,1]
	v_lshlrev_b32_e32 v184, 16, v183
	v_and_b32_e32 v185, 0xffff0000, v183
	v_pk_add_f32 v[180:181], v[180:181], v[184:185] neg_lo:[0,1] neg_hi:[0,1]
	v_cvt_pk_bf16_f32 v178, v178, v179
	v_cvt_pk_bf16_f32 v179, v180, v181
	v_pk_mul_f32 v[180:181], v[190:191], v[192:193] op_sel_hi:[1,0]
	v_pk_mul_f32 v[184:185], v[186:187], v[192:193] op_sel_hi:[1,0]
	v_pk_fma_f32 v[180:181], v[146:147], v[180:181], v[12:13]
	v_add_u32_e32 v188, s30, v131
	v_med3_f32 v186, v180, s55, v228
	v_med3_f32 v187, v181, s55, v228
	v_cvt_pk_fp8_f32 v189, v186, v187
	v_pk_fma_f32 v[184:185], v[144:145], v[184:185], v[14:15]
	ds_write2st64_b64 v188, v[176:177], v[178:179] offset0:1 offset1:2
	v_med3_f32 v186, v184, s55, v228
	v_med3_f32 v187, v185, s55, v228
	v_cvt_pk_bf16_f32 v176, v180, v181
	v_cvt_pk_fp8_f32 v189, v186, v187 op_sel:[0,0,1]
	v_cvt_pk_bf16_f32 v177, v184, v185
	v_lshlrev_b32_e32 v178, 16, v176
	v_and_b32_e32 v179, 0xffff0000, v176
	v_pk_add_f32 v[178:179], v[180:181], v[178:179] neg_lo:[0,1] neg_hi:[0,1]
	v_lshlrev_b32_e32 v180, 16, v177
	v_and_b32_e32 v181, 0xffff0000, v177
	v_pk_add_f32 v[180:181], v[184:185], v[180:181] neg_lo:[0,1] neg_hi:[0,1]
	v_cvt_pk_bf16_f32 v178, v178, v179
	v_cvt_pk_bf16_f32 v179, v180, v181
	global_store_dword v[174:175], v196, off offset:2304 sc1
	global_store_dword v[174:175], v189, off offset:2816 sc1
	ds_write2st64_b64 v193, v[182:183], v[176:177] offset0:10 offset1:11
	ds_write_b64 v188, v[178:179] offset:1536
	v_cvt_f32_f16_sdwa v179, v157 dst_sel:DWORD dst_unused:UNUSED_PAD src0_sel:WORD_1
	v_cvt_f32_f16_sdwa v181, v156 dst_sel:DWORD dst_unused:UNUSED_PAD src0_sel:WORD_1
	v_cvt_f32_f16_e32 v180, v156
	v_cvt_f32_f16_e32 v178, v157
	s_waitcnt vmcnt(27)
	v_lshlrev_b32_e32 v176, 16, v160
	v_and_b32_e32 v177, 0xffff0000, v160
	v_lshlrev_b32_e32 v156, 16, v161
	v_and_b32_e32 v157, 0xffff0000, v161
	v_pk_fma_f32 v[160:161], v[16:17], v[176:177], v[180:181]
	v_pk_fma_f32 v[156:157], v[18:19], v[156:157], v[178:179]
	v_cvt_pk_f16_f32 v176, v160, v161
	v_cvt_pk_f16_f32 v177, v156, v157
	global_store_dwordx2 v[164:165], v[176:177], off offset:2048 nt sc1
	v_pk_mul_f32 v[176:177], v[156:157], v[156:157]
	v_pk_mul_f32 v[178:179], v[160:161], v[160:161]
	v_cvt_f32_f16_sdwa v183, v158 dst_sel:DWORD dst_unused:UNUSED_PAD src0_sel:WORD_1
	v_pk_mov_b32 v[180:181], v[178:179], v[176:177] op_sel:[1,0]
	v_mov_b32_e32 v179, v177
	v_pk_add_f32 v[176:177], v[180:181], v[178:179]
	v_cvt_f32_f16_sdwa v181, v159 dst_sel:DWORD dst_unused:UNUSED_PAD src0_sel:WORD_1
	v_cvt_f32_f16_e32 v182, v158
	v_cvt_f32_f16_e32 v180, v159
	s_waitcnt vmcnt(27)
	v_lshlrev_b32_e32 v178, 16, v166
	v_and_b32_e32 v179, 0xffff0000, v166
	v_lshlrev_b32_e32 v158, 16, v167
	v_and_b32_e32 v159, 0xffff0000, v167
	v_pk_fma_f32 v[166:167], v[0:1], v[178:179], v[182:183]
	v_pk_fma_f32 v[158:159], v[2:3], v[158:159], v[180:181]
	v_cvt_pk_f16_f32 v178, v166, v167
	v_cvt_pk_f16_f32 v179, v158, v159
	v_cvt_f32_f16_sdwa v185, v162 dst_sel:DWORD dst_unused:UNUSED_PAD src0_sel:WORD_1
	v_cvt_f32_f16_e32 v184, v162
	global_store_dwordx2 v[164:165], v[178:179], off offset:2560 nt sc1
	v_pk_mul_f32 v[178:179], v[158:159], v[158:159]
	v_pk_mul_f32 v[180:181], v[166:167], v[166:167]
	s_waitcnt vmcnt(27)
	v_lshlrev_b32_e32 v162, 16, v171
	v_pk_mov_b32 v[182:183], v[180:181], v[178:179] op_sel:[1,0]
	v_mov_b32_e32 v181, v179
	v_pk_add_f32 v[178:179], v[182:183], v[180:181]
	v_lshlrev_b32_e32 v180, 16, v170
	v_and_b32_e32 v181, 0xffff0000, v170
	v_cvt_f32_f16_sdwa v183, v163 dst_sel:DWORD dst_unused:UNUSED_PAD src0_sel:WORD_1
	v_cvt_f32_f16_e32 v182, v163
	v_and_b32_e32 v163, 0xffff0000, v171
	v_pk_fma_f32 v[170:171], v[24:25], v[180:181], v[184:185]
	v_cvt_f32_f16_sdwa v185, v168 dst_sel:DWORD dst_unused:UNUSED_PAD src0_sel:WORD_1
	v_cvt_f32_f16_e32 v184, v168
	v_pk_fma_f32 v[162:163], v[26:27], v[162:163], v[182:183]
	s_waitcnt vmcnt(22)
	v_lshlrev_b32_e32 v182, 16, v172
	v_and_b32_e32 v183, 0xffff0000, v172
	v_cvt_f32_f16_sdwa v187, v169 dst_sel:DWORD dst_unused:UNUSED_PAD src0_sel:WORD_1
	v_cvt_f32_f16_e32 v186, v169
	v_lshlrev_b32_e32 v168, 16, v173
	v_and_b32_e32 v169, 0xffff0000, v173
	v_pk_fma_f32 v[172:173], v[28:29], v[182:183], v[184:185]
	v_pk_add_f32 v[176:177], v[176:177], v[176:177] op_sel:[0,1] op_sel_hi:[1,0]
	v_mul_f32_e32 v182, v172, v172
	v_mul_f32_e32 v183, v173, v173
	v_pk_add_f32 v[178:179], v[178:179], v[178:179] op_sel:[0,1] op_sel_hi:[1,0]
	v_mov_b32_e32 v177, v182
	v_mov_b32_e32 v179, v183
	v_pk_fma_f32 v[168:169], v[30:31], v[168:169], v[186:187]
	v_pk_add_f32 v[176:177], v[176:177], v[178:179]
	v_mul_f32_e32 v178, v171, v171
	v_mul_f32_e32 v182, v163, v163
	v_mul_f32_e32 v184, v168, v168
	v_mul_f32_e32 v185, v169, v169
	v_pk_fma_f32 v[178:179], v[170:171], v[170:171], v[178:179] op_sel_hi:[1,1,0]
	v_pk_fma_f32 v[182:183], v[162:163], v[162:163], v[182:183] op_sel_hi:[1,1,0]
	v_mov_b32_e32 v179, v184
	v_mov_b32_e32 v183, v185
	v_pk_add_f32 v[178:179], v[178:179], v[182:183]
	v_cvt_pk_f16_f32 v181, v162, v163
	v_pk_add_f32 v[176:177], v[176:177], v[178:179]
	v_cvt_pk_f16_f32 v180, v170, v171
	v_add_f32_e32 v176, v176, v177
	global_store_dwordx2 v[164:165], v[180:181], off offset:3072 nt sc1
	v_mov_b32_e32 v181, v65
	v_add_f32_dpp v176, v176, v176 quad_perm:[1,0,3,2] row_mask:0xf bank_mask:0xf bound_ctrl:1
	v_cvt_pk_f16_f32 v179, v168, v169
	v_cvt_pk_f16_f32 v178, v172, v173
	v_add_f32_dpp v176, v176, v176 quad_perm:[2,3,0,1] row_mask:0xf bank_mask:0xf bound_ctrl:1
	global_store_dwordx2 v[164:165], v[178:179], off offset:3584 nt sc1
	v_add_u32_e32 v64, 48, v64
	v_add_f32_dpp v176, v176, v176 row_half_mirror row_mask:0xf bank_mask:0xf bound_ctrl:1
	s_nop 1
	v_add_f32_dpp v176, v176, v176 row_mirror row_mask:0xf bank_mask:0xf bound_ctrl:1
	s_nop 0
	v_readlane_b32 s10, v176, 16
	v_readlane_b32 s11, v176, 48
	v_readlane_b32 s8, v176, 0
	v_readlane_b32 s9, v176, 32
	v_mov_b32_e32 v176, s10
	v_mov_b32_e32 v177, s11
	v_pk_add_f32 v[176:177], s[8:9], v[176:177]
	s_nop 0
	v_add_f32_e32 v176, v176, v177
	v_fmamk_f32 v176, v176, 0x3a800000, v229
	v_rsq_f32_e32 v176, v176
	s_nop 0
	v_pk_mul_f32 v[160:161], v[160:161], v[176:177] op_sel_hi:[1,0]
	s_nop 0
	v_pk_fma_f32 v[160:161], v[134:135], v[160:161], v[4:5]
	v_pk_mul_f32 v[156:157], v[156:157], v[176:177] op_sel_hi:[1,0]
	v_med3_f32 v177, v160, s55, v228
	v_med3_f32 v180, v161, s55, v228
	v_cvt_pk_fp8_f32 v181, v177, v180
	v_pk_fma_f32 v[156:157], v[132:133], v[156:157], v[6:7]
	v_cvt_pk_bf16_f32 v164, v160, v161
	v_cvt_pk_bf16_f32 v165, v156, v157
	v_lshlrev_b32_e32 v178, 16, v164
	v_and_b32_e32 v179, 0xffff0000, v164
	v_med3_f32 v177, v156, s55, v228
	v_med3_f32 v180, v157, s55, v228
	v_pk_add_f32 v[160:161], v[160:161], v[178:179] neg_lo:[0,1] neg_hi:[0,1]
	v_lshlrev_b32_e32 v178, 16, v165
	v_and_b32_e32 v179, 0xffff0000, v165
	v_cvt_pk_fp8_f32 v181, v177, v180 op_sel:[0,0,1]
	v_pk_add_f32 v[156:157], v[156:157], v[178:179] neg_lo:[0,1] neg_hi:[0,1]
	v_add_u32_e32 v177, s26, v236
	v_cvt_pk_bf16_f32 v160, v160, v161
	v_cvt_pk_bf16_f32 v161, v156, v157
	v_pk_mul_f32 v[156:157], v[166:167], v[176:177] op_sel_hi:[1,0]
	v_mov_b32_e32 v178, v65
	v_pk_fma_f32 v[156:157], v[138:139], v[156:157], v[8:9]
	v_pk_mul_f32 v[158:159], v[158:159], v[176:177] op_sel_hi:[1,0]
	v_med3_f32 v166, v156, s55, v228
	v_med3_f32 v167, v157, s55, v228
	v_cvt_pk_fp8_f32 v178, v166, v167
	v_pk_fma_f32 v[158:159], v[136:137], v[158:159], v[10:11]
	ds_write_b64 v177, v[160:161]
	v_med3_f32 v166, v158, s55, v228
	v_med3_f32 v167, v159, s55, v228
	v_cvt_pk_bf16_f32 v160, v156, v157
	v_cvt_pk_fp8_f32 v178, v166, v167 op_sel:[0,0,1]
	v_cvt_pk_bf16_f32 v161, v158, v159
	v_lshlrev_b32_e32 v166, 16, v160
	v_and_b32_e32 v167, 0xffff0000, v160
	v_pk_add_f32 v[156:157], v[156:157], v[166:167] neg_lo:[0,1] neg_hi:[0,1]
	v_lshlrev_b32_e32 v166, 16, v161
	v_and_b32_e32 v167, 0xffff0000, v161
	v_pk_add_f32 v[158:159], v[158:159], v[166:167] neg_lo:[0,1] neg_hi:[0,1]
	v_cvt_pk_bf16_f32 v156, v156, v157
	v_cvt_pk_bf16_f32 v157, v158, v159
	v_pk_mul_f32 v[158:159], v[170:171], v[176:177] op_sel_hi:[1,0]
	ds_write2st64_b64 v64, v[164:165], v[160:161] offset0:12 offset1:13
	v_pk_fma_f32 v[158:159], v[142:143], v[158:159], v[20:21]
	v_pk_mul_f32 v[160:161], v[162:163], v[176:177] op_sel_hi:[1,0]
	v_med3_f32 v162, v158, s55, v228
	v_med3_f32 v163, v159, s55, v228
	v_mov_b32_e32 v164, v65
	v_cvt_pk_fp8_f32 v164, v162, v163
	v_pk_fma_f32 v[160:161], v[140:141], v[160:161], v[22:23]
	v_add_u32_e32 v166, s31, v131
	v_med3_f32 v162, v160, s55, v228
	v_med3_f32 v163, v161, s55, v228
	v_cvt_pk_fp8_f32 v164, v162, v163 op_sel:[0,0,1]
	v_cvt_pk_bf16_f32 v162, v158, v159
	v_cvt_pk_bf16_f32 v163, v160, v161
	v_and_b32_e32 v165, 0xffff0000, v162
	global_store_dword v[174:175], v164, off offset:3584 sc1
	v_lshlrev_b32_e32 v164, 16, v162
	v_pk_add_f32 v[158:159], v[158:159], v[164:165] neg_lo:[0,1] neg_hi:[0,1]
	v_lshlrev_b32_e32 v164, 16, v163
	v_and_b32_e32 v165, 0xffff0000, v163
	v_pk_add_f32 v[160:161], v[160:161], v[164:165] neg_lo:[0,1] neg_hi:[0,1]
	v_cvt_pk_bf16_f32 v158, v158, v159
	v_cvt_pk_bf16_f32 v159, v160, v161
	v_pk_mul_f32 v[160:161], v[172:173], v[176:177] op_sel_hi:[1,0]
	v_pk_mul_f32 v[164:165], v[168:169], v[176:177] op_sel_hi:[1,0]
	v_pk_fma_f32 v[160:161], v[146:147], v[160:161], v[12:13]
	v_mov_b32_e32 v169, v65
	v_med3_f32 v167, v160, s55, v228
	v_med3_f32 v168, v161, s55, v228
	v_cvt_pk_fp8_f32 v169, v167, v168
	v_pk_fma_f32 v[164:165], v[144:145], v[164:165], v[14:15]
	ds_write2st64_b64 v166, v[156:157], v[158:159] offset0:1 offset1:2
	v_med3_f32 v167, v164, s55, v228
	v_med3_f32 v168, v165, s55, v228
	v_cvt_pk_fp8_f32 v169, v167, v168 op_sel:[0,0,1]
	v_cvt_pk_bf16_f32 v156, v160, v161
	v_cvt_pk_bf16_f32 v157, v164, v165
	v_lshlrev_b32_e32 v158, 16, v156
	v_and_b32_e32 v159, 0xffff0000, v156
	v_pk_add_f32 v[158:159], v[160:161], v[158:159] neg_lo:[0,1] neg_hi:[0,1]
	v_lshlrev_b32_e32 v160, 16, v157
	v_and_b32_e32 v161, 0xffff0000, v157
	v_pk_add_f32 v[160:161], v[164:165], v[160:161] neg_lo:[0,1] neg_hi:[0,1]
	global_store_dword v[174:175], v181, off offset:3072 sc1
	global_store_dword v[174:175], v178, off offset:3328 sc1
	global_store_dword v[174:175], v169, off offset:3840 sc1
	v_cvt_pk_bf16_f32 v158, v158, v159
	v_cvt_pk_bf16_f32 v159, v160, v161
	ds_write2st64_b64 v64, v[162:163], v[156:157] offset0:14 offset1:15
	ds_write_b64 v166, v[158:159] offset:1536
	v_add_u32_e32 v64, 0, v232
	s_waitcnt lgkmcnt(0)
	s_barrier
	ds_read_b128 v[156:159], v64
	ds_read_b128 v[160:163], v64 offset:33024
	s_waitcnt lgkmcnt(1)
	v_mfma_f32_16x16x32_bf16 v[164:167], v[156:159], v[32:35], 0
	v_add_u32_e32 v168, s61, v232
	ds_read_b128 v[168:171], v168
	ds_read_b128 v[172:175], v64 offset:192
	v_mfma_f32_16x16x32_bf16 v[176:179], v[156:159], v[44:47], 0
	v_mfma_f32_16x16x32_bf16 v[180:183], v[156:159], v[40:43], 0
	v_mfma_f32_16x16x32_bf16 v[164:167], v[156:159], v[94:97], v[164:167]
	v_mfma_f32_16x16x32_bf16 v[176:179], v[156:159], v[36:39], v[176:179]
	v_mfma_f32_16x16x32_bf16 v[156:159], v[156:159], v[118:121], v[180:183]
	s_waitcnt lgkmcnt(1)
	v_mfma_f32_16x16x32_bf16 v[164:167], v[168:171], v[32:35], v[164:167]
	s_nop 2
	v_add_u32_e32 v180, s61, v233
	ds_read_b128 v[180:183], v180
	ds_read_b128 v[184:187], v239
	v_mfma_f32_16x16x32_bf16 v[176:179], v[168:171], v[44:47], v[176:179]
	v_mfma_f32_16x16x32_bf16 v[156:159], v[168:171], v[40:43], v[156:159]
	v_mfma_f32_16x16x32_bf16 v[168:171], v[160:163], v[32:35], 0
	v_mfma_f32_16x16x32_bf16 v[188:191], v[160:163], v[44:47], 0
	v_mfma_f32_16x16x32_bf16 v[192:195], v[160:163], v[40:43], 0
	v_mfma_f32_16x16x32_bf16 v[168:171], v[160:163], v[94:97], v[168:171]
	v_mfma_f32_16x16x32_bf16 v[188:191], v[160:163], v[36:39], v[188:191]
	v_mfma_f32_16x16x32_bf16 v[160:163], v[160:163], v[118:121], v[192:195]
	s_waitcnt lgkmcnt(1)
	v_mfma_f32_16x16x32_bf16 v[168:171], v[180:183], v[32:35], v[168:171]
	v_mfma_f32_16x16x32_bf16 v[188:191], v[180:183], v[44:47], v[188:191]
	v_mfma_f32_16x16x32_bf16 v[160:163], v[180:183], v[40:43], v[160:163]
	ds_read_b128 v[180:183], v64 offset:64
	ds_read_b128 v[192:195], v64 offset:128
	v_add_u32_e32 v64, 0, v233
	s_waitcnt lgkmcnt(1)
	v_mfma_f32_16x16x32_bf16 v[164:167], v[180:183], v[60:63], v[164:167]
	v_mfma_f32_16x16x32_bf16 v[176:179], v[180:183], v[48:51], v[176:179]
	v_mfma_f32_16x16x32_bf16 v[156:159], v[180:183], v[78:81], v[156:159]
	v_mfma_f32_16x16x32_bf16 v[164:167], v[180:183], v[52:55], v[164:167]
	v_mfma_f32_16x16x32_bf16 v[176:179], v[180:183], v[56:59], v[176:179]
	v_mfma_f32_16x16x32_bf16 v[156:159], v[180:183], v[70:73], v[156:159]
	v_mfma_f32_16x16x32_bf16 v[164:167], v[184:187], v[60:63], v[164:167]
	v_mfma_f32_16x16x32_bf16 v[176:179], v[184:187], v[48:51], v[176:179]
	v_mfma_f32_16x16x32_bf16 v[156:159], v[184:187], v[78:81], v[156:159]
	ds_read_b128 v[180:183], v64 offset:64
	ds_read_b128 v[184:187], v64 offset:128
	ds_read_b128 v[196:199], v240
	ds_read_b128 v[200:203], v64 offset:192
	v_add_u32_e32 v64, 0xc00, v238
	s_waitcnt lgkmcnt(3)
	v_mfma_f32_16x16x32_bf16 v[168:171], v[180:183], v[60:63], v[168:171]
	v_mfma_f32_16x16x32_bf16 v[188:191], v[180:183], v[48:51], v[188:191]
	v_mfma_f32_16x16x32_bf16 v[160:163], v[180:183], v[78:81], v[160:163]
	v_mfma_f32_16x16x32_bf16 v[168:171], v[180:183], v[52:55], v[168:171]
	v_mfma_f32_16x16x32_bf16 v[188:191], v[180:183], v[56:59], v[188:191]
	v_mfma_f32_16x16x32_bf16 v[160:163], v[180:183], v[70:73], v[160:163]
	v_mfma_f32_16x16x32_bf16 v[164:167], v[192:195], v[66:69], v[164:167]
	v_mfma_f32_16x16x32_bf16 v[176:179], v[192:195], v[102:105], v[176:179]
	v_mfma_f32_16x16x32_bf16 v[156:159], v[192:195], v[82:85], v[156:159]
	s_waitcnt lgkmcnt(1)
	v_mfma_f32_16x16x32_bf16 v[168:171], v[196:199], v[60:63], v[168:171]
	v_mfma_f32_16x16x32_bf16 v[188:191], v[196:199], v[48:51], v[188:191]
	v_mfma_f32_16x16x32_bf16 v[160:163], v[196:199], v[78:81], v[160:163]
	ds_read_b128 v[180:183], v241
	ds_read_b128 v[196:199], v242
	v_mfma_f32_16x16x32_bf16 v[164:167], v[192:195], v[74:77], v[164:167]
	v_mfma_f32_16x16x32_bf16 v[176:179], v[192:195], v[86:89], v[176:179]
	v_mfma_f32_16x16x32_bf16 v[156:159], v[192:195], v[90:93], v[156:159]
	s_waitcnt lgkmcnt(1)
	v_mfma_f32_16x16x32_bf16 v[164:167], v[180:183], v[66:69], v[164:167]
	v_mfma_f32_16x16x32_bf16 v[176:179], v[180:183], v[102:105], v[176:179]
	v_mfma_f32_16x16x32_bf16 v[156:159], v[180:183], v[82:85], v[156:159]
	v_mfma_f32_16x16x32_bf16 v[168:171], v[184:187], v[66:69], v[168:171]
	v_mfma_f32_16x16x32_bf16 v[180:183], v[184:187], v[102:105], v[188:191]
	v_mfma_f32_16x16x32_bf16 v[160:163], v[184:187], v[82:85], v[160:163]
	v_mfma_f32_16x16x32_bf16 v[168:171], v[184:187], v[74:77], v[168:171]
	v_mfma_f32_16x16x32_bf16 v[180:183], v[184:187], v[86:89], v[180:183]
	v_mfma_f32_16x16x32_bf16 v[160:163], v[184:187], v[90:93], v[160:163]
	ds_read_b128 v[184:187], v243
	ds_read_b128 v[188:191], v244
	s_waitcnt lgkmcnt(0)
	s_barrier
	v_mfma_f32_16x16x32_bf16 v[168:171], v[196:199], v[66:69], v[168:171]
	v_mfma_f32_16x16x32_bf16 v[180:183], v[196:199], v[102:105], v[180:183]
	v_mfma_f32_16x16x32_bf16 v[164:167], v[172:175], v[98:101], v[164:167]
	v_mfma_f32_16x16x32_bf16 v[176:179], v[172:175], v[106:109], v[176:179]
	v_mfma_f32_16x16x32_bf16 v[156:159], v[172:175], v[122:125], v[156:159]
	v_mfma_f32_16x16x32_bf16 v[160:163], v[196:199], v[82:85], v[160:163]
	v_mfma_f32_16x16x32_bf16 v[164:167], v[172:175], v[110:113], v[164:167]
	v_mfma_f32_16x16x32_bf16 v[176:179], v[172:175], v[114:117], v[176:179]
	v_mfma_f32_16x16x32_bf16 v[156:159], v[172:175], v[126:129], v[156:159]
	v_mfma_f32_16x16x32_bf16 v[168:171], v[200:203], v[98:101], v[168:171]
	v_mfma_f32_16x16x32_bf16 v[172:175], v[200:203], v[106:109], v[180:183]
	v_mfma_f32_16x16x32_bf16 v[160:163], v[200:203], v[122:125], v[160:163]
	v_mfma_f32_16x16x32_bf16 v[168:171], v[200:203], v[110:113], v[168:171]
	v_mfma_f32_16x16x32_bf16 v[172:175], v[200:203], v[114:117], v[172:175]
	v_mfma_f32_16x16x32_bf16 v[160:163], v[200:203], v[126:129], v[160:163]
	v_mfma_f32_16x16x32_bf16 v[164:167], v[184:187], v[98:101], v[164:167]
	v_mfma_f32_16x16x32_bf16 v[176:179], v[184:187], v[106:109], v[176:179]
	v_mfma_f32_16x16x32_bf16 v[168:171], v[188:191], v[98:101], v[168:171]
	v_mfma_f32_16x16x32_bf16 v[172:175], v[188:191], v[106:109], v[172:175]
	v_mfma_f32_16x16x32_bf16 v[156:159], v[184:187], v[122:125], v[156:159]
	s_nop 4
	ds_write2_b32 v238, v164, v176 offset1:16
	ds_write2_b32 v238, v166, v178 offset0:96 offset1:112
	s_nop 0
	ds_write2_b32 v238, v156, v165 offset0:32 offset1:48
	ds_write2_b32 v238, v177, v157 offset0:64 offset1:80
	ds_write2_b32 v238, v158, v167 offset0:128 offset1:144
	ds_write2_b32 v238, v179, v159 offset0:160 offset1:176
	v_mfma_f32_16x16x32_bf16 v[160:163], v[188:191], v[122:125], v[160:163]
	ds_write2_b32 v64, v168, v172 offset1:16
	ds_write2_b32 v64, v170, v174 offset0:96 offset1:112
	s_nop 5
	ds_write2_b32 v64, v160, v169 offset0:32 offset1:48
	ds_write2_b32 v64, v173, v161 offset0:64 offset1:80
	ds_write2_b32 v64, v162, v171 offset0:128 offset1:144
	ds_write2_b32 v64, v175, v163 offset0:160 offset1:176
	s_waitcnt lgkmcnt(0)
	s_barrier
	ds_read2st64_b32 v[156:157], v234 offset1:8
	ds_read2st64_b32 v[158:159], v234 offset0:16 offset1:24
	ds_read2st64_b32 v[160:161], v234 offset0:48 offset1:56
	ds_read2st64_b32 v[162:163], v234 offset0:64 offset1:72
	ds_read2st64_b32 v[164:165], v234 offset0:96 offset1:104
	ds_read2st64_b32 v[166:167], v234 offset0:112 offset1:120
	ds_read2st64_b32 v[168:169], v234 offset0:144 offset1:152
	s_waitcnt lgkmcnt(6)
	v_add_f32_e32 v64, 0, v156
	s_waitcnt lgkmcnt(5)
	v_add_f32_e32 v64, v64, v159
	s_waitcnt lgkmcnt(4)
	v_add_f32_e32 v64, v64, v160
	ds_read2st64_b32 v[170:171], v234 offset0:160 offset1:168
	s_waitcnt lgkmcnt(4)
	v_add_f32_e32 v64, v64, v163
	s_waitcnt lgkmcnt(3)
	v_add_f32_e32 v64, v64, v164
	s_waitcnt lgkmcnt(2)
	v_add_f32_e32 v64, v64, v167
	s_waitcnt lgkmcnt(1)
	v_add_f32_e32 v64, v64, v168
	ds_read2st64_b32 v[172:173], v234 offset0:32 offset1:40
	s_waitcnt lgkmcnt(1)
	v_add_f32_e32 v64, v64, v171
	ds_write_b32 v235, v64
	v_add_f32_e32 v64, 0, v157
	ds_read2st64_b32 v[156:157], v234 offset0:80 offset1:88
	ds_read2st64_b32 v[174:175], v234 offset0:128 offset1:136
	s_waitcnt lgkmcnt(3)
	v_add_f32_e32 v64, v64, v172
	v_add_f32_e32 v64, v64, v161
	ds_read2st64_b32 v[160:161], v234 offset0:176 offset1:184
	s_waitcnt lgkmcnt(2)
	v_add_f32_e32 v64, v64, v156
	v_add_f32_e32 v64, v64, v165
	s_waitcnt lgkmcnt(1)
	v_add_f32_e32 v64, v64, v174
	v_add_f32_e32 v64, v64, v169
	s_waitcnt lgkmcnt(0)
	v_add_f32_e32 v64, v64, v160
	v_add_u32_e32 v156, 0x800, v235
	ds_write_b32 v156, v64
	v_add_f32_e32 v64, 0, v158
	v_add_f32_e32 v64, v64, v173
	v_add_f32_e32 v64, v64, v162
	v_add_f32_e32 v64, v64, v157
	v_add_f32_e32 v64, v64, v166
	v_add_f32_e32 v64, v64, v175
	v_add_f32_e32 v64, v64, v170
	v_add_f32_e32 v64, v64, v161
	v_add_u32_e32 v156, 0x1000, v235
	ds_write_b32 v156, v64
	s_waitcnt lgkmcnt(0)
	s_barrier
	s_and_saveexec_b64 s[22:23], s[6:7]
	s_cbranch_execz .LBB0_696
	v_mov_b32_e32 v160, 0x24000
	ds_read_b128 v[160:163], v160
	ds_read_b128 v[156:159], v231
	v_mov_b32_e32 v176, 0x7f800000
	s_waitcnt lgkmcnt(0)
	v_pk_add_f32 v[156:157], v[156:157], v[160:161]
	s_nop 0
	v_cmp_gt_f32_e64 s[10:11], v157, v156
	v_add_f32_e32 v64, v158, v162
	v_add_f32_e32 v158, v159, v163
	v_cndmask_b32_e64 v159, v156, v157, s[10:11]
	v_cmp_gt_f32_e32 vcc, v64, v159
	s_nop 1
	v_cndmask_b32_e32 v159, v159, v64, vcc
	v_cmp_gt_f32_e64 s[8:9], v158, v159
	s_nop 1
	v_cndmask_b32_e64 v159, v159, v158, s[8:9]
	v_sub_f32_e32 v172, v156, v159
	v_sub_f32_e32 v156, v157, v159
	v_mul_f32_e32 v157, 0x3fb8aa3b, v156
	v_fma_f32 v160, v156, s33, -v157
	v_rndne_f32_e32 v161, v157
	v_fmac_f32_e32 v160, 0x32a5705f, v156
	v_sub_f32_e32 v157, v157, v161
	v_add_f32_e32 v157, v157, v160
	v_exp_f32_e32 v157, v157
	v_cvt_i32_f32_e32 v160, v161
	v_cmp_ngt_f32_e64 s[12:13], s54, v156
	v_sub_f32_e32 v64, v64, v159
	v_ldexp_f32 v157, v157, v160
	v_cndmask_b32_e64 v157, 0, v157, s[12:13]
	v_cmp_nlt_f32_e64 s[12:13], s85, v156
	v_mul_f32_e32 v156, 0x3fb8aa3b, v64
	v_rndne_f32_e32 v160, v156
	v_cndmask_b32_e64 v173, v176, v157, s[12:13]
	v_fma_f32 v157, v64, s33, -v156
	v_fmac_f32_e32 v157, 0x32a5705f, v64
	v_sub_f32_e32 v156, v156, v160
	v_add_f32_e32 v156, v156, v157
	v_exp_f32_e32 v156, v156
	v_cvt_i32_f32_e32 v157, v160
	v_cmp_ngt_f32_e64 s[12:13], s54, v64
	v_ldexp_f32 v156, v156, v157
	s_nop 0
	v_cndmask_b32_e64 v156, 0, v156, s[12:13]
	v_cmp_nlt_f32_e64 s[12:13], s85, v64
	s_nop 1
	v_cndmask_b32_e64 v64, v176, v156, s[12:13]
	v_sub_f32_e32 v156, v158, v159
	v_mul_f32_e32 v157, 0x3fb8aa3b, v156
	v_fma_f32 v158, v156, s33, -v157
	v_rndne_f32_e32 v159, v157
	v_fmac_f32_e32 v158, 0x32a5705f, v156
	v_sub_f32_e32 v157, v157, v159
	v_add_f32_e32 v157, v157, v158
	v_exp_f32_e32 v157, v157
	v_cvt_i32_f32_e32 v158, v159
	v_cmp_ngt_f32_e64 s[12:13], s54, v156
	v_ldexp_f32 v157, v157, v158
	s_nop 0
	v_cndmask_b32_e64 v157, 0, v157, s[12:13]
	v_cmp_nlt_f32_e64 s[12:13], s85, v156
	v_cndmask_b32_e64 v156, 0, 8, s[10:11]
	v_cndmask_b32_e64 v156, v156, 16, vcc
	v_cndmask_b32_e64 v175, v156, 24, s[8:9]
	v_lshlrev_b32_e32 v168, 2, v175
	v_add_u32_e32 v160, v231, v168
	v_cndmask_b32_e64 v174, v176, v157, s[12:13]
	ds_read_b128 v[156:159], v160 offset:16
	ds_read_b128 v[160:163], v160 offset:32
	v_add_u32_e32 v164, 0x24000, v168
	ds_read_b128 v[168:171], v164 offset:16
	ds_read_b128 v[164:167], v164 offset:32
	v_cmp_ngt_f32_e32 vcc, s54, v172
	s_mov_b32 s12, 0xff61b1e6
	s_waitcnt lgkmcnt(0)
	v_add_f32_e32 v160, v160, v164
	v_mul_f32_e32 v164, 0x3fb8aa3b, v172
	v_add_f32_e32 v161, v161, v165
	v_add_f32_e32 v162, v162, v166
	v_fma_f32 v165, v172, s33, -v164
	v_rndne_f32_e32 v166, v164
	v_fmac_f32_e32 v165, 0x32a5705f, v172
	v_sub_f32_e32 v164, v164, v166
	v_add_f32_e32 v164, v164, v165
	v_exp_f32_e32 v164, v164
	v_cvt_i32_f32_e32 v165, v166
	v_pk_add_f32 v[156:157], v[156:157], v[168:169]
	v_add_f32_e32 v158, v158, v170
	v_add_f32_e32 v159, v159, v171
	v_ldexp_f32 v164, v164, v165
	v_cndmask_b32_e32 v164, 0, v164, vcc
	v_cmp_nlt_f32_e32 vcc, s85, v172
	v_add_f32_e32 v163, v163, v167
	v_cmp_nlt_f32_e64 s[12:13], s12, v156
	v_cndmask_b32_e32 v164, v176, v164, vcc
	v_cmp_gt_f32_e32 vcc, v157, v156
	v_add_f32_e32 v164, v164, v173
	v_add_f32_e32 v64, v64, v164
	v_cndmask_b32_e32 v165, v156, v157, vcc
	v_cndmask_b32_e64 v164, 0, 1, vcc
	v_cmp_gt_f32_e32 vcc, v158, v165
	v_mov_b32_e32 v166, 0xff61b1e6
	v_add_f32_e32 v64, v174, v64
	v_cndmask_b32_e32 v165, v165, v158, vcc
	v_cndmask_b32_e64 v164, v164, 2, vcc
	v_cmp_gt_f32_e32 vcc, v159, v165
	s_nop 1
	v_cndmask_b32_e32 v165, v165, v159, vcc
	v_cndmask_b32_e64 v164, v164, 3, vcc
	v_cmp_gt_f32_e32 vcc, v160, v165
	s_nop 1
	v_cndmask_b32_e32 v165, v165, v160, vcc
	v_cndmask_b32_e64 v164, v164, 4, vcc
	v_cmp_gt_f32_e32 vcc, v161, v165
	s_nop 1
	v_cndmask_b32_e32 v165, v165, v161, vcc
	v_cndmask_b32_e64 v164, v164, 5, vcc
	v_cmp_gt_f32_e32 vcc, v162, v165
	s_nop 1
	v_cndmask_b32_e32 v165, v165, v162, vcc
	v_cndmask_b32_e64 v164, v164, 6, vcc
	v_cmp_ngt_f32_e64 s[8:9], v163, v165
	s_nop 1
	v_cndmask_b32_e64 v164, 7, v164, s[8:9]
	v_cmp_eq_u32_e64 s[10:11], 0, v164
	s_or_b64 s[12:13], s[10:11], s[12:13]
	v_cndmask_b32_e64 v156, v156, v166, s[12:13]
	v_cmp_ne_u32_e64 s[12:13], 1, v164
	v_cmp_gt_f32_e64 s[14:15], v157, v156
	s_and_b64 s[12:13], s[12:13], s[14:15]
	s_or_b64 s[10:11], s[10:11], s[12:13]
	v_cndmask_b32_e64 v156, v156, v157, s[12:13]
	v_cndmask_b32_e64 v157, 0, 1, s[10:11]
	v_cmp_ne_u32_e64 s[10:11], 2, v164
	v_cmp_gt_f32_e64 s[12:13], v158, v156
	s_and_b64 s[10:11], s[10:11], s[12:13]
	v_cndmask_b32_e64 v156, v156, v158, s[10:11]
	v_cndmask_b32_e64 v157, v157, 2, s[10:11]
	v_cmp_ne_u32_e64 s[10:11], 3, v164
	v_cmp_gt_f32_e64 s[12:13], v159, v156
	s_and_b64 s[10:11], s[10:11], s[12:13]
	v_cndmask_b32_e64 v156, v156, v159, s[10:11]
	v_cndmask_b32_e64 v157, v157, 3, s[10:11]
	v_cmp_ne_u32_e64 s[10:11], 4, v164
	v_cmp_gt_f32_e64 s[12:13], v160, v156
	s_and_b64 s[10:11], s[10:11], s[12:13]
	v_cndmask_b32_e64 v156, v156, v160, s[10:11]
	v_cndmask_b32_e64 v157, v157, 4, s[10:11]
	v_cmp_ne_u32_e64 s[10:11], 5, v164
	v_cmp_gt_f32_e64 s[12:13], v161, v156
	s_and_b64 s[10:11], s[10:11], s[12:13]
	v_cndmask_b32_e64 v156, v156, v161, s[10:11]
	v_cndmask_b32_e64 v157, v157, 5, s[10:11]
	s_and_b64 s[10:11], vcc, s[8:9]
	v_cmp_ngt_f32_e32 vcc, v162, v156
	s_or_b64 vcc, s[10:11], vcc
	v_cndmask_b32_e64 v165, v163, v165, s[8:9]
	v_cndmask_b32_e32 v156, v162, v156, vcc
	v_cndmask_b32_e32 v157, 6, v157, vcc
	v_cmp_gt_f32_e32 vcc, v163, v156
	s_and_b64 vcc, s[8:9], vcc
	s_nop 0
	v_cndmask_b32_e64 v159, v157, 7, vcc
	v_div_scale_f32 v157, s[8:9], v64, v64, 1.0
	v_rcp_f32_e32 v158, v157
	v_cndmask_b32_e32 v156, v156, v163, vcc
	v_sub_f32_e32 v156, v156, v165
	v_add_u32_e32 v159, v159, v175
	v_fma_f32 v160, -v157, v158, 1.0
	v_fmac_f32_e32 v158, v160, v158
	v_div_scale_f32 v160, vcc, 1.0, v64, 1.0
	v_mul_f32_e32 v161, v160, v158
	v_fma_f32 v162, -v157, v161, v160
	v_fmac_f32_e32 v161, v162, v158
	v_fma_f32 v157, -v157, v161, v160
	v_div_fmas_f32 v157, v157, v158, v161
	v_div_fixup_f32 v64, v157, v64, 1.0
	v_mul_f32_e32 v157, 0x3fb8aa3b, v156
	v_fma_f32 v158, v156, s33, -v157
	v_rndne_f32_e32 v160, v157
	v_fmac_f32_e32 v158, 0x32a5705f, v156
	v_sub_f32_e32 v157, v157, v160
	v_add_f32_e32 v157, v157, v158
	v_exp_f32_e32 v157, v157
	v_cvt_i32_f32_e32 v158, v160
	v_cmp_ngt_f32_e32 vcc, s54, v156
	v_ldexp_f32 v157, v157, v158
	s_nop 0
	v_cndmask_b32_e32 v157, 0, v157, vcc
	v_cmp_nlt_f32_e32 vcc, s85, v156
	s_nop 1
	v_cndmask_b32_e32 v157, v176, v157, vcc
	v_add_f32_e32 v156, 1.0, v157
	v_div_scale_f32 v158, s[8:9], v156, v156, 1.0
	v_rcp_f32_e32 v160, v158
	s_add_i32 s8, 0, 0x22c00
	v_fma_f32 v161, -v158, v160, 1.0
	v_fmac_f32_e32 v160, v161, v160
	v_div_scale_f32 v161, vcc, 1.0, v156, 1.0
	v_mul_f32_e32 v162, v161, v160
	v_fma_f32 v163, -v158, v162, v161
	v_fmac_f32_e32 v162, v163, v160
	v_fma_f32 v158, -v158, v162, v161
	v_div_fmas_f32 v158, v158, v160, v162
	v_div_fixup_f32 v156, v158, v156, 1.0
	v_or_b32_e32 v158, v164, v175
	ds_write_b64 v237, v[158:159]
	v_lshl_add_u32 v158, v158, 2, s8
	v_mov_b32_e32 v160, 1
	ds_add_rtn_u32 v158, v158, v160
	v_mul_f32_e32 v157, v157, v156
	v_pk_mul_f32 v[156:157], v[64:65], v[156:157] op_sel_hi:[0,1]
	s_waitcnt lgkmcnt(0)
	ds_write_b32 v237, v158 offset:2048
	v_lshl_add_u32 v158, v159, 2, s8
	ds_add_rtn_u32 v158, v158, v160
	s_waitcnt lgkmcnt(0)
	ds_write_b32 v237, v158 offset:2052
	v_lshl_add_u64 v[158:159], s[42:43], 0, v[148:149]
	global_store_dwordx2 v[158:159], v[156:157], off sc1
	s_branch .LBB0_696

.LBB0_765:
	s_or_b64 exec, exec, s[4:5]
	v_add_u32_e32 v0, 0x21c00, v230
	s_waitcnt lgkmcnt(0)
	s_barrier
	ds_read_b32 v8, v0
	v_add_u32_e32 v0, 0x22400, v230
	ds_read_b32 v3, v0
	v_readlane_b32 s4, v254, 13
	v_lshrrev_b32_e32 v2, 1, v222
	s_waitcnt lgkmcnt(1)
	v_lshl_add_u32 v0, v8, 2, 0
	v_add_u32_e32 v0, 0x22c80, v0
	ds_read_b32 v4, v0
	v_ashrrev_i32_e32 v0, 6, v130
	v_add_u32_e32 v64, s4, v0
	v_lshlrev_b64 v[0:1], 5, v[64:65]
	v_and_or_b32 v0, v2, 31, v0
	s_waitcnt lgkmcnt(0)
	v_add_u32_e32 v2, v3, v4
	v_and_b32_e32 v3, 1, v222
	v_lshlrev_b64 v[4:5], 3, v[0:1]
	v_readlane_b32 s4, v254, 20
	v_lshl_or_b32 v4, v3, 2, v4
	v_readlane_b32 s5, v254, 21
	v_ashrrev_i32_e32 v3, 31, v2
	v_readlane_b32 s36, v254, 3
	v_lshl_add_u64 v[6:7], s[4:5], 0, v[4:5]
	v_readlane_b32 s4, v254, 22
	v_readlane_b32 s5, v254, 23
	v_readlane_b32 s49, v254, 5
	v_readlane_b32 s37, v254, 4
	v_lshl_add_u64 v[4:5], s[4:5], 0, v[4:5]
	v_readlane_b32 s4, v254, 46
	v_readlane_b32 s5, v254, 47
	global_store_dword v[4:5], v2, off sc1
	global_store_dword v[6:7], v8, off sc1
	v_mov_b64_e32 v[4:5], s[4:5]
	s_mov_b32 s4, 0x40400
	v_mad_i64_i32 v[4:5], s[4:5], v8, s4, v[4:5]
	v_lshl_add_u64 v[2:3], v[2:3], 2, v[4:5]
	v_readlane_b32 s4, v254, 12
	global_store_dword v[2:3], v0, off sc1
	s_barrier
	v_mbcnt_lo_u32_b32 v0, -1, 0
	v_mbcnt_hi_u32_b32 v0, -1, v0
	s_lshl_b32 s4, s4, 6
	s_waitcnt vmcnt(0)
	s_sub_i32 s4, 0, s4
	v_cmp_eq_u32_e32 vcc, s4, v0
	s_barrier
	s_and_saveexec_b64 s[4:5], vcc
	s_xor_b64 s[38:39], exec, s[4:5]
	s_cbranch_execz .LBB0_810
	v_readlane_b32 s4, v255, 1
	s_waitcnt vmcnt(0) expcnt(0) lgkmcnt(0)
	s_nop 0
	v_mov_b32_e32 v0, s4
	ds_read_b32 v2, v0
	v_readlane_b32 s4, v255, 2
	s_waitcnt lgkmcnt(0)
	v_cmp_ne_u32_e32 vcc, 0, v2
	v_mov_b32_e32 v0, s4
	ds_read_b32 v0, v0
	s_cbranch_vccnz .LBB0_780
	v_readlane_b32 s4, v254, 0
	v_readlane_b32 s5, v254, 1
	s_load_dwordx2 s[8:9], s[4:5], 0x4
	s_add_u32 s4, s36, 0x1000
	s_addc_u32 s5, s37, 0
	s_add_u32 s6, s36, 0x1100
	s_addc_u32 s7, s37, 0
	s_waitcnt lgkmcnt(0)
	s_mul_i32 s30, s8, s44
	s_add_u32 s8, s36, 0x1200
	s_mul_i32 s30, s30, s9
	s_addc_u32 s9, s37, 0
	s_add_u32 s10, s36, 0x1300
	s_addc_u32 s11, s37, 0
	s_mov_b32 s31, 1
	s_mov_b64 s[12:13], 0
	s_branch .LBB0_770

.LBB0_834:
	v_mov_b32_e32 v1, v207
	v_mov_b32_e32 v0, v206
	s_lshl_b32 s11, s16, 8
	s_add_i32 s11, s11, s36
	v_add_u32_e32 v0, s11, v0
	s_lshl_b32 s11, s18, 7
	s_and_b32 s11, s11, 0x180
	s_or_b32 s11, s11, s37
	v_lshl_add_u32 v2, v1, 3, s11
	v_ashrrev_i32_e32 v3, 31, v2
	s_mov_b64 s[16:17], -1
	v_ashrrev_i32_e32 v1, 31, v0
	v_lshlrev_b64 v[0:1], 9, v[0:1]
	v_lshl_add_u64 v[0:1], s[64:65], 0, v[0:1]
	v_lshl_add_u64 v[0:1], v[0:1], 0, v[2:3]
	s_mov_b32 s101, 0
	v_mul_f32_e32 v230, s48, v190
	v_mul_f32_e32 v231, s48, v191
	v_mul_f32_e32 v232, s48, v192
	v_mul_f32_e32 v233, s48, v193
	v_mul_f32_e32 v234, s48, v186
	v_mul_f32_e32 v235, s48, v187
	v_mul_f32_e32 v236, s48, v188
	v_mul_f32_e32 v237, s48, v189
	v_mul_f32_e32 v238, s48, v182
	v_mul_f32_e32 v239, s48, v183
	v_mul_f32_e32 v240, s48, v184
	v_mul_f32_e32 v241, s48, v185
	v_mul_f32_e32 v242, s48, v178
	v_mul_f32_e32 v243, s48, v179
	v_mul_f32_e32 v244, s48, v180
	v_mul_f32_e32 v245, s48, v181
	v_mul_f32_e32 v246, 0xbfb8aa3b, v230
	v_mul_f32_e32 v247, 0xbfb8aa3b, v231
	v_mul_f32_e32 v248, 0xbfb8aa3b, v232
	v_mul_f32_e32 v249, 0xbfb8aa3b, v233
	v_mul_f32_e32 v250, 0xbfb8aa3b, v234
	v_mul_f32_e32 v251, 0xbfb8aa3b, v235
	v_mul_f32_e32 v252, 0xbfb8aa3b, v236
	v_mul_f32_e32 v253, 0xbfb8aa3b, v237
	v_exp_f32_e32 v246, v246
	v_exp_f32_e32 v247, v247
	v_exp_f32_e32 v248, v248
	v_exp_f32_e32 v249, v249
	v_exp_f32_e32 v250, v250
	v_exp_f32_e32 v251, v251
	v_exp_f32_e32 v252, v252
	v_exp_f32_e32 v253, v253
	v_add_f32_e32 v246, 1.0, v246
	v_add_f32_e32 v247, 1.0, v247
	v_add_f32_e32 v248, 1.0, v248
	v_add_f32_e32 v249, 1.0, v249
	v_add_f32_e32 v250, 1.0, v250
	v_add_f32_e32 v251, 1.0, v251
	v_add_f32_e32 v252, 1.0, v252
	v_add_f32_e32 v253, 1.0, v253
	v_rcp_f32_e32 v246, v246
	v_rcp_f32_e32 v247, v247
	v_rcp_f32_e32 v248, v248
	v_rcp_f32_e32 v249, v249
	v_rcp_f32_e32 v250, v250
	v_rcp_f32_e32 v251, v251
	v_rcp_f32_e32 v252, v252
	v_rcp_f32_e32 v253, v253
	v_mul_f32_e32 v230, v230, v246
	v_mul_f32_e32 v231, v231, v247
	v_mul_f32_e32 v232, v232, v248
	v_mul_f32_e32 v233, v233, v249
	v_mul_f32_e32 v234, v234, v250
	v_mul_f32_e32 v235, v235, v251
	v_mul_f32_e32 v236, v236, v252
	v_mul_f32_e32 v237, v237, v253
	v_mul_f32_e32 v230, v230, v238
	v_mul_f32_e32 v231, v231, v239
	v_mul_f32_e32 v232, v232, v240
	v_mul_f32_e32 v233, v233, v241
	v_mul_f32_e32 v234, v234, v242
	v_mul_f32_e32 v235, v235, v243
	v_mul_f32_e32 v236, v236, v244
	v_mul_f32_e32 v237, v237, v245
	v_med3_f32 v230, v230, s55, v228
	v_med3_f32 v231, v231, s55, v228
	v_med3_f32 v232, v232, s55, v228
	v_med3_f32 v233, v233, s55, v228
	v_med3_f32 v234, v234, s55, v228
	v_med3_f32 v235, v235, s55, v228
	v_med3_f32 v236, v236, s55, v228
	v_med3_f32 v237, v237, s55, v228
	v_cvt_pk_fp8_f32 v216, v230, v231
	v_cvt_pk_fp8_f32 v217, v234, v235
	v_cvt_pk_fp8_f32 v216, v232, v233 op_sel:[0,0,1]
	v_cvt_pk_fp8_f32 v217, v236, v237 op_sel:[0,0,1]
	s_nop 1
	global_store_dwordx2 v[0:1], v[216:217], off sc1
	v_mul_f32_e32 v230, s48, v174
	v_mul_f32_e32 v231, s48, v175
	v_mul_f32_e32 v232, s48, v176
	v_mul_f32_e32 v233, s48, v177
	v_mul_f32_e32 v234, s48, v170
	v_mul_f32_e32 v235, s48, v171
	v_mul_f32_e32 v236, s48, v172
	v_mul_f32_e32 v237, s48, v173
	v_mul_f32_e32 v238, s48, v166
	v_mul_f32_e32 v239, s48, v167
	v_mul_f32_e32 v240, s48, v168
	v_mul_f32_e32 v241, s48, v169
	v_mul_f32_e32 v242, s48, v162
	v_mul_f32_e32 v243, s48, v163
	v_mul_f32_e32 v244, s48, v164
	v_mul_f32_e32 v245, s48, v165
	v_mul_f32_e32 v246, 0xbfb8aa3b, v230
	v_mul_f32_e32 v247, 0xbfb8aa3b, v231
	v_mul_f32_e32 v248, 0xbfb8aa3b, v232
	v_mul_f32_e32 v249, 0xbfb8aa3b, v233
	v_mul_f32_e32 v250, 0xbfb8aa3b, v234
	v_mul_f32_e32 v251, 0xbfb8aa3b, v235
	v_mul_f32_e32 v252, 0xbfb8aa3b, v236
	v_mul_f32_e32 v253, 0xbfb8aa3b, v237
	v_exp_f32_e32 v246, v246
	v_exp_f32_e32 v247, v247
	v_exp_f32_e32 v248, v248
	v_exp_f32_e32 v249, v249
	v_exp_f32_e32 v250, v250
	v_exp_f32_e32 v251, v251
	v_exp_f32_e32 v252, v252
	v_exp_f32_e32 v253, v253
	v_add_f32_e32 v246, 1.0, v246
	v_add_f32_e32 v247, 1.0, v247
	v_add_f32_e32 v248, 1.0, v248
	v_add_f32_e32 v249, 1.0, v249
	v_add_f32_e32 v250, 1.0, v250
	v_add_f32_e32 v251, 1.0, v251
	v_add_f32_e32 v252, 1.0, v252
	v_add_f32_e32 v253, 1.0, v253
	v_rcp_f32_e32 v246, v246
	v_rcp_f32_e32 v247, v247
	v_rcp_f32_e32 v248, v248
	v_rcp_f32_e32 v249, v249
	v_rcp_f32_e32 v250, v250
	v_rcp_f32_e32 v251, v251
	v_rcp_f32_e32 v252, v252
	v_rcp_f32_e32 v253, v253
	v_mul_f32_e32 v230, v230, v246
	v_mul_f32_e32 v231, v231, v247
	v_mul_f32_e32 v232, v232, v248
	v_mul_f32_e32 v233, v233, v249
	v_mul_f32_e32 v234, v234, v250
	v_mul_f32_e32 v235, v235, v251
	v_mul_f32_e32 v236, v236, v252
	v_mul_f32_e32 v237, v237, v253
	v_mul_f32_e32 v230, v230, v238
	v_mul_f32_e32 v231, v231, v239
	v_mul_f32_e32 v232, v232, v240
	v_mul_f32_e32 v233, v233, v241
	v_mul_f32_e32 v234, v234, v242
	v_mul_f32_e32 v235, v235, v243
	v_mul_f32_e32 v236, v236, v244
	v_mul_f32_e32 v237, v237, v245
	v_med3_f32 v230, v230, s55, v228
	v_med3_f32 v231, v231, s55, v228
	v_med3_f32 v232, v232, s55, v228
	v_med3_f32 v233, v233, s55, v228
	v_med3_f32 v234, v234, s55, v228
	v_med3_f32 v235, v235, s55, v228
	v_med3_f32 v236, v236, s55, v228
	v_med3_f32 v237, v237, s55, v228
	v_cvt_pk_fp8_f32 v216, v230, v231
	v_cvt_pk_fp8_f32 v217, v234, v235
	v_cvt_pk_fp8_f32 v216, v232, v233 op_sel:[0,0,1]
	v_cvt_pk_fp8_f32 v217, v236, v237 op_sel:[0,0,1]
	s_mov_b32 s100, 0x2000
	v_lshl_add_u64 v[218:219], v[0:1], 0, s[100:101]
	s_nop 0
	global_store_dwordx2 v[218:219], v[216:217], off sc1
	v_mul_f32_e32 v230, s48, v158
	v_mul_f32_e32 v231, s48, v159
	v_mul_f32_e32 v232, s48, v160
	v_mul_f32_e32 v233, s48, v161
	v_mul_f32_e32 v234, s48, v154
	v_mul_f32_e32 v235, s48, v155
	v_mul_f32_e32 v236, s48, v156
	v_mul_f32_e32 v237, s48, v157
	v_mul_f32_e32 v238, s48, v150
	v_mul_f32_e32 v239, s48, v151
	v_mul_f32_e32 v240, s48, v152
	v_mul_f32_e32 v241, s48, v153
	v_mul_f32_e32 v242, s48, v146
	v_mul_f32_e32 v243, s48, v147
	v_mul_f32_e32 v244, s48, v148
	v_mul_f32_e32 v245, s48, v149
	v_mul_f32_e32 v246, 0xbfb8aa3b, v230
	v_mul_f32_e32 v247, 0xbfb8aa3b, v231
	v_mul_f32_e32 v248, 0xbfb8aa3b, v232
	v_mul_f32_e32 v249, 0xbfb8aa3b, v233
	v_mul_f32_e32 v250, 0xbfb8aa3b, v234
	v_mul_f32_e32 v251, 0xbfb8aa3b, v235
	v_mul_f32_e32 v252, 0xbfb8aa3b, v236
	v_mul_f32_e32 v253, 0xbfb8aa3b, v237
	v_exp_f32_e32 v246, v246
	v_exp_f32_e32 v247, v247
	v_exp_f32_e32 v248, v248
	v_exp_f32_e32 v249, v249
	v_exp_f32_e32 v250, v250
	v_exp_f32_e32 v251, v251
	v_exp_f32_e32 v252, v252
	v_exp_f32_e32 v253, v253
	v_add_f32_e32 v246, 1.0, v246
	v_add_f32_e32 v247, 1.0, v247
	v_add_f32_e32 v248, 1.0, v248
	v_add_f32_e32 v249, 1.0, v249
	v_add_f32_e32 v250, 1.0, v250
	v_add_f32_e32 v251, 1.0, v251
	v_add_f32_e32 v252, 1.0, v252
	v_add_f32_e32 v253, 1.0, v253
	v_rcp_f32_e32 v246, v246
	v_rcp_f32_e32 v247, v247
	v_rcp_f32_e32 v248, v248
	v_rcp_f32_e32 v249, v249
	v_rcp_f32_e32 v250, v250
	v_rcp_f32_e32 v251, v251
	v_rcp_f32_e32 v252, v252
	v_rcp_f32_e32 v253, v253
	v_mul_f32_e32 v230, v230, v246
	v_mul_f32_e32 v231, v231, v247
	v_mul_f32_e32 v232, v232, v248
	v_mul_f32_e32 v233, v233, v249
	v_mul_f32_e32 v234, v234, v250
	v_mul_f32_e32 v235, v235, v251
	v_mul_f32_e32 v236, v236, v252
	v_mul_f32_e32 v237, v237, v253
	v_mul_f32_e32 v230, v230, v238
	v_mul_f32_e32 v231, v231, v239
	v_mul_f32_e32 v232, v232, v240
	v_mul_f32_e32 v233, v233, v241
	v_mul_f32_e32 v234, v234, v242
	v_mul_f32_e32 v235, v235, v243
	v_mul_f32_e32 v236, v236, v244
	v_mul_f32_e32 v237, v237, v245
	v_med3_f32 v230, v230, s55, v228
	v_med3_f32 v231, v231, s55, v228
	v_med3_f32 v232, v232, s55, v228
	v_med3_f32 v233, v233, s55, v228
	v_med3_f32 v234, v234, s55, v228
	v_med3_f32 v235, v235, s55, v228
	v_med3_f32 v236, v236, s55, v228
	v_med3_f32 v237, v237, s55, v228
	v_cvt_pk_fp8_f32 v216, v230, v231
	v_cvt_pk_fp8_f32 v217, v234, v235
	v_cvt_pk_fp8_f32 v216, v232, v233 op_sel:[0,0,1]
	v_cvt_pk_fp8_f32 v217, v236, v237 op_sel:[0,0,1]
	s_mov_b32 s100, 0x4000
	v_lshl_add_u64 v[218:219], v[0:1], 0, s[100:101]
	s_nop 0
	global_store_dwordx2 v[218:219], v[216:217], off sc1
	v_mul_f32_e32 v230, s48, v142
	v_mul_f32_e32 v231, s48, v143
	v_mul_f32_e32 v232, s48, v144
	v_mul_f32_e32 v233, s48, v145
	v_mul_f32_e32 v234, s48, v138
	v_mul_f32_e32 v235, s48, v139
	v_mul_f32_e32 v236, s48, v140
	v_mul_f32_e32 v237, s48, v141
	v_mul_f32_e32 v238, s48, v134
	v_mul_f32_e32 v239, s48, v135
	v_mul_f32_e32 v240, s48, v136
	v_mul_f32_e32 v241, s48, v137
	v_mul_f32_e32 v242, s48, v130
	v_mul_f32_e32 v243, s48, v131
	v_mul_f32_e32 v244, s48, v132
	v_mul_f32_e32 v245, s48, v133
	v_mul_f32_e32 v246, 0xbfb8aa3b, v230
	v_mul_f32_e32 v247, 0xbfb8aa3b, v231
	v_mul_f32_e32 v248, 0xbfb8aa3b, v232
	v_mul_f32_e32 v249, 0xbfb8aa3b, v233
	v_mul_f32_e32 v250, 0xbfb8aa3b, v234
	v_mul_f32_e32 v251, 0xbfb8aa3b, v235
	v_mul_f32_e32 v252, 0xbfb8aa3b, v236
	v_mul_f32_e32 v253, 0xbfb8aa3b, v237
	v_exp_f32_e32 v246, v246
	v_exp_f32_e32 v247, v247
	v_exp_f32_e32 v248, v248
	v_exp_f32_e32 v249, v249
	v_exp_f32_e32 v250, v250
	v_exp_f32_e32 v251, v251
	v_exp_f32_e32 v252, v252
	v_exp_f32_e32 v253, v253
	v_add_f32_e32 v246, 1.0, v246
	v_add_f32_e32 v247, 1.0, v247
	v_add_f32_e32 v248, 1.0, v248
	v_add_f32_e32 v249, 1.0, v249
	v_add_f32_e32 v250, 1.0, v250
	v_add_f32_e32 v251, 1.0, v251
	v_add_f32_e32 v252, 1.0, v252
	v_add_f32_e32 v253, 1.0, v253
	v_rcp_f32_e32 v246, v246
	v_rcp_f32_e32 v247, v247
	v_rcp_f32_e32 v248, v248
	v_rcp_f32_e32 v249, v249
	v_rcp_f32_e32 v250, v250
	v_rcp_f32_e32 v251, v251
	v_rcp_f32_e32 v252, v252
	v_rcp_f32_e32 v253, v253
	v_mul_f32_e32 v230, v230, v246
	v_mul_f32_e32 v231, v231, v247
	v_mul_f32_e32 v232, v232, v248
	v_mul_f32_e32 v233, v233, v249
	v_mul_f32_e32 v234, v234, v250
	v_mul_f32_e32 v235, v235, v251
	v_mul_f32_e32 v236, v236, v252
	v_mul_f32_e32 v237, v237, v253
	v_mul_f32_e32 v230, v230, v238
	v_mul_f32_e32 v231, v231, v239
	v_mul_f32_e32 v232, v232, v240
	v_mul_f32_e32 v233, v233, v241
	v_mul_f32_e32 v234, v234, v242
	v_mul_f32_e32 v235, v235, v243
	v_mul_f32_e32 v236, v236, v244
	v_mul_f32_e32 v237, v237, v245
	v_med3_f32 v230, v230, s55, v228
	v_med3_f32 v231, v231, s55, v228
	v_med3_f32 v232, v232, s55, v228
	v_med3_f32 v233, v233, s55, v228
	v_med3_f32 v234, v234, s55, v228
	v_med3_f32 v235, v235, s55, v228
	v_med3_f32 v236, v236, s55, v228
	v_med3_f32 v237, v237, s55, v228
	v_cvt_pk_fp8_f32 v216, v230, v231
	v_cvt_pk_fp8_f32 v217, v234, v235
	v_cvt_pk_fp8_f32 v216, v232, v233 op_sel:[0,0,1]
	v_cvt_pk_fp8_f32 v217, v236, v237 op_sel:[0,0,1]
	s_mov_b32 s100, 0x6000
	v_lshl_add_u64 v[218:219], v[0:1], 0, s[100:101]
	s_nop 0
	global_store_dwordx2 v[218:219], v[216:217], off sc1
	v_mul_f32_e32 v230, s48, v126
	v_mul_f32_e32 v231, s48, v127
	v_mul_f32_e32 v232, s48, v128
	v_mul_f32_e32 v233, s48, v129
	v_mul_f32_e32 v234, s48, v122
	v_mul_f32_e32 v235, s48, v123
	v_mul_f32_e32 v236, s48, v124
	v_mul_f32_e32 v237, s48, v125
	v_mul_f32_e32 v238, s48, v118
	v_mul_f32_e32 v239, s48, v119
	v_mul_f32_e32 v240, s48, v120
	v_mul_f32_e32 v241, s48, v121
	v_mul_f32_e32 v242, s48, v114
	v_mul_f32_e32 v243, s48, v115
	v_mul_f32_e32 v244, s48, v116
	v_mul_f32_e32 v245, s48, v117
	v_mul_f32_e32 v246, 0xbfb8aa3b, v230
	v_mul_f32_e32 v247, 0xbfb8aa3b, v231
	v_mul_f32_e32 v248, 0xbfb8aa3b, v232
	v_mul_f32_e32 v249, 0xbfb8aa3b, v233
	v_mul_f32_e32 v250, 0xbfb8aa3b, v234
	v_mul_f32_e32 v251, 0xbfb8aa3b, v235
	v_mul_f32_e32 v252, 0xbfb8aa3b, v236
	v_mul_f32_e32 v253, 0xbfb8aa3b, v237
	v_exp_f32_e32 v246, v246
	v_exp_f32_e32 v247, v247
	v_exp_f32_e32 v248, v248
	v_exp_f32_e32 v249, v249
	v_exp_f32_e32 v250, v250
	v_exp_f32_e32 v251, v251
	v_exp_f32_e32 v252, v252
	v_exp_f32_e32 v253, v253
	v_add_f32_e32 v246, 1.0, v246
	v_add_f32_e32 v247, 1.0, v247
	v_add_f32_e32 v248, 1.0, v248
	v_add_f32_e32 v249, 1.0, v249
	v_add_f32_e32 v250, 1.0, v250
	v_add_f32_e32 v251, 1.0, v251
	v_add_f32_e32 v252, 1.0, v252
	v_add_f32_e32 v253, 1.0, v253
	v_rcp_f32_e32 v246, v246
	v_rcp_f32_e32 v247, v247
	v_rcp_f32_e32 v248, v248
	v_rcp_f32_e32 v249, v249
	v_rcp_f32_e32 v250, v250
	v_rcp_f32_e32 v251, v251
	v_rcp_f32_e32 v252, v252
	v_rcp_f32_e32 v253, v253
	v_mul_f32_e32 v230, v230, v246
	v_mul_f32_e32 v231, v231, v247
	v_mul_f32_e32 v232, v232, v248
	v_mul_f32_e32 v233, v233, v249
	v_mul_f32_e32 v234, v234, v250
	v_mul_f32_e32 v235, v235, v251
	v_mul_f32_e32 v236, v236, v252
	v_mul_f32_e32 v237, v237, v253
	v_mul_f32_e32 v230, v230, v238
	v_mul_f32_e32 v231, v231, v239
	v_mul_f32_e32 v232, v232, v240
	v_mul_f32_e32 v233, v233, v241
	v_mul_f32_e32 v234, v234, v242
	v_mul_f32_e32 v235, v235, v243
	v_mul_f32_e32 v236, v236, v244
	v_mul_f32_e32 v237, v237, v245
	v_med3_f32 v230, v230, s55, v228
	v_med3_f32 v231, v231, s55, v228
	v_med3_f32 v232, v232, s55, v228
	v_med3_f32 v233, v233, s55, v228
	v_med3_f32 v234, v234, s55, v228
	v_med3_f32 v235, v235, s55, v228
	v_med3_f32 v236, v236, s55, v228
	v_med3_f32 v237, v237, s55, v228
	v_cvt_pk_fp8_f32 v216, v230, v231
	v_cvt_pk_fp8_f32 v217, v234, v235
	v_cvt_pk_fp8_f32 v216, v232, v233 op_sel:[0,0,1]
	v_cvt_pk_fp8_f32 v217, v236, v237 op_sel:[0,0,1]
	s_mov_b32 s100, 0x10000
	v_lshl_add_u64 v[218:219], v[0:1], 0, s[100:101]
	s_nop 0
	global_store_dwordx2 v[218:219], v[216:217], off sc1
	v_mul_f32_e32 v230, s48, v110
	v_mul_f32_e32 v231, s48, v111
	v_mul_f32_e32 v232, s48, v112
	v_mul_f32_e32 v233, s48, v113
	v_mul_f32_e32 v234, s48, v106
	v_mul_f32_e32 v235, s48, v107
	v_mul_f32_e32 v236, s48, v108
	v_mul_f32_e32 v237, s48, v109
	v_mul_f32_e32 v238, s48, v102
	v_mul_f32_e32 v239, s48, v103
	v_mul_f32_e32 v240, s48, v104
	v_mul_f32_e32 v241, s48, v105
	v_mul_f32_e32 v242, s48, v98
	v_mul_f32_e32 v243, s48, v99
	v_mul_f32_e32 v244, s48, v100
	v_mul_f32_e32 v245, s48, v101
	v_mul_f32_e32 v246, 0xbfb8aa3b, v230
	v_mul_f32_e32 v247, 0xbfb8aa3b, v231
	v_mul_f32_e32 v248, 0xbfb8aa3b, v232
	v_mul_f32_e32 v249, 0xbfb8aa3b, v233
	v_mul_f32_e32 v250, 0xbfb8aa3b, v234
	v_mul_f32_e32 v251, 0xbfb8aa3b, v235
	v_mul_f32_e32 v252, 0xbfb8aa3b, v236
	v_mul_f32_e32 v253, 0xbfb8aa3b, v237
	v_exp_f32_e32 v246, v246
	v_exp_f32_e32 v247, v247
	v_exp_f32_e32 v248, v248
	v_exp_f32_e32 v249, v249
	v_exp_f32_e32 v250, v250
	v_exp_f32_e32 v251, v251
	v_exp_f32_e32 v252, v252
	v_exp_f32_e32 v253, v253
	v_add_f32_e32 v246, 1.0, v246
	v_add_f32_e32 v247, 1.0, v247
	v_add_f32_e32 v248, 1.0, v248
	v_add_f32_e32 v249, 1.0, v249
	v_add_f32_e32 v250, 1.0, v250
	v_add_f32_e32 v251, 1.0, v251
	v_add_f32_e32 v252, 1.0, v252
	v_add_f32_e32 v253, 1.0, v253
	v_rcp_f32_e32 v246, v246
	v_rcp_f32_e32 v247, v247
	v_rcp_f32_e32 v248, v248
	v_rcp_f32_e32 v249, v249
	v_rcp_f32_e32 v250, v250
	v_rcp_f32_e32 v251, v251
	v_rcp_f32_e32 v252, v252
	v_rcp_f32_e32 v253, v253
	v_mul_f32_e32 v230, v230, v246
	v_mul_f32_e32 v231, v231, v247
	v_mul_f32_e32 v232, v232, v248
	v_mul_f32_e32 v233, v233, v249
	v_mul_f32_e32 v234, v234, v250
	v_mul_f32_e32 v235, v235, v251
	v_mul_f32_e32 v236, v236, v252
	v_mul_f32_e32 v237, v237, v253
	v_mul_f32_e32 v230, v230, v238
	v_mul_f32_e32 v231, v231, v239
	v_mul_f32_e32 v232, v232, v240
	v_mul_f32_e32 v233, v233, v241
	v_mul_f32_e32 v234, v234, v242
	v_mul_f32_e32 v235, v235, v243
	v_mul_f32_e32 v236, v236, v244
	v_mul_f32_e32 v237, v237, v245
	v_med3_f32 v230, v230, s55, v228
	v_med3_f32 v231, v231, s55, v228
	v_med3_f32 v232, v232, s55, v228
	v_med3_f32 v233, v233, s55, v228
	v_med3_f32 v234, v234, s55, v228
	v_med3_f32 v235, v235, s55, v228
	v_med3_f32 v236, v236, s55, v228
	v_med3_f32 v237, v237, s55, v228
	v_cvt_pk_fp8_f32 v216, v230, v231
	v_cvt_pk_fp8_f32 v217, v234, v235
	v_cvt_pk_fp8_f32 v216, v232, v233 op_sel:[0,0,1]
	v_cvt_pk_fp8_f32 v217, v236, v237 op_sel:[0,0,1]
	s_mov_b32 s100, 0x12000
	v_lshl_add_u64 v[218:219], v[0:1], 0, s[100:101]
	s_nop 0
	global_store_dwordx2 v[218:219], v[216:217], off sc1
	v_mul_f32_e32 v230, s48, v94
	v_mul_f32_e32 v231, s48, v95
	v_mul_f32_e32 v232, s48, v96
	v_mul_f32_e32 v233, s48, v97
	v_mul_f32_e32 v234, s48, v90
	v_mul_f32_e32 v235, s48, v91
	v_mul_f32_e32 v236, s48, v92
	v_mul_f32_e32 v237, s48, v93
	v_mul_f32_e32 v238, s48, v86
	v_mul_f32_e32 v239, s48, v87
	v_mul_f32_e32 v240, s48, v88
	v_mul_f32_e32 v241, s48, v89
	v_mul_f32_e32 v242, s48, v82
	v_mul_f32_e32 v243, s48, v83
	v_mul_f32_e32 v244, s48, v84
	v_mul_f32_e32 v245, s48, v85
	v_mul_f32_e32 v246, 0xbfb8aa3b, v230
	v_mul_f32_e32 v247, 0xbfb8aa3b, v231
	v_mul_f32_e32 v248, 0xbfb8aa3b, v232
	v_mul_f32_e32 v249, 0xbfb8aa3b, v233
	v_mul_f32_e32 v250, 0xbfb8aa3b, v234
	v_mul_f32_e32 v251, 0xbfb8aa3b, v235
	v_mul_f32_e32 v252, 0xbfb8aa3b, v236
	v_mul_f32_e32 v253, 0xbfb8aa3b, v237
	v_exp_f32_e32 v246, v246
	v_exp_f32_e32 v247, v247
	v_exp_f32_e32 v248, v248
	v_exp_f32_e32 v249, v249
	v_exp_f32_e32 v250, v250
	v_exp_f32_e32 v251, v251
	v_exp_f32_e32 v252, v252
	v_exp_f32_e32 v253, v253
	v_add_f32_e32 v246, 1.0, v246
	v_add_f32_e32 v247, 1.0, v247
	v_add_f32_e32 v248, 1.0, v248
	v_add_f32_e32 v249, 1.0, v249
	v_add_f32_e32 v250, 1.0, v250
	v_add_f32_e32 v251, 1.0, v251
	v_add_f32_e32 v252, 1.0, v252
	v_add_f32_e32 v253, 1.0, v253
	v_rcp_f32_e32 v246, v246
	v_rcp_f32_e32 v247, v247
	v_rcp_f32_e32 v248, v248
	v_rcp_f32_e32 v249, v249
	v_rcp_f32_e32 v250, v250
	v_rcp_f32_e32 v251, v251
	v_rcp_f32_e32 v252, v252
	v_rcp_f32_e32 v253, v253
	v_mul_f32_e32 v230, v230, v246
	v_mul_f32_e32 v231, v231, v247
	v_mul_f32_e32 v232, v232, v248
	v_mul_f32_e32 v233, v233, v249
	v_mul_f32_e32 v234, v234, v250
	v_mul_f32_e32 v235, v235, v251
	v_mul_f32_e32 v236, v236, v252
	v_mul_f32_e32 v237, v237, v253
	v_mul_f32_e32 v230, v230, v238
	v_mul_f32_e32 v231, v231, v239
	v_mul_f32_e32 v232, v232, v240
	v_mul_f32_e32 v233, v233, v241
	v_mul_f32_e32 v234, v234, v242
	v_mul_f32_e32 v235, v235, v243
	v_mul_f32_e32 v236, v236, v244
	v_mul_f32_e32 v237, v237, v245
	v_med3_f32 v230, v230, s55, v228
	v_med3_f32 v231, v231, s55, v228
	v_med3_f32 v232, v232, s55, v228
	v_med3_f32 v233, v233, s55, v228
	v_med3_f32 v234, v234, s55, v228
	v_med3_f32 v235, v235, s55, v228
	v_med3_f32 v236, v236, s55, v228
	v_med3_f32 v237, v237, s55, v228
	v_cvt_pk_fp8_f32 v216, v230, v231
	v_cvt_pk_fp8_f32 v217, v234, v235
	v_cvt_pk_fp8_f32 v216, v232, v233 op_sel:[0,0,1]
	v_cvt_pk_fp8_f32 v217, v236, v237 op_sel:[0,0,1]
	s_mov_b32 s100, 0x14000
	v_lshl_add_u64 v[218:219], v[0:1], 0, s[100:101]
	s_nop 0
	global_store_dwordx2 v[218:219], v[216:217], off sc1
	v_mul_f32_e32 v230, s48, v78
	v_mul_f32_e32 v231, s48, v79
	v_mul_f32_e32 v232, s48, v80
	v_mul_f32_e32 v233, s48, v81
	v_mul_f32_e32 v234, s48, v74
	v_mul_f32_e32 v235, s48, v75
	v_mul_f32_e32 v236, s48, v76
	v_mul_f32_e32 v237, s48, v77
	v_mul_f32_e32 v238, s48, v70
	v_mul_f32_e32 v239, s48, v71
	v_mul_f32_e32 v240, s48, v72
	v_mul_f32_e32 v241, s48, v73
	v_mul_f32_e32 v242, s48, v66
	v_mul_f32_e32 v243, s48, v67
	v_mul_f32_e32 v244, s48, v68
	v_mul_f32_e32 v245, s48, v69
	v_mul_f32_e32 v246, 0xbfb8aa3b, v230
	v_mul_f32_e32 v247, 0xbfb8aa3b, v231
	v_mul_f32_e32 v248, 0xbfb8aa3b, v232
	v_mul_f32_e32 v249, 0xbfb8aa3b, v233
	v_mul_f32_e32 v250, 0xbfb8aa3b, v234
	v_mul_f32_e32 v251, 0xbfb8aa3b, v235
	v_mul_f32_e32 v252, 0xbfb8aa3b, v236
	v_mul_f32_e32 v253, 0xbfb8aa3b, v237
	v_exp_f32_e32 v246, v246
	v_exp_f32_e32 v247, v247
	v_exp_f32_e32 v248, v248
	v_exp_f32_e32 v249, v249
	v_exp_f32_e32 v250, v250
	v_exp_f32_e32 v251, v251
	v_exp_f32_e32 v252, v252
	v_exp_f32_e32 v253, v253
	v_add_f32_e32 v246, 1.0, v246
	v_add_f32_e32 v247, 1.0, v247
	v_add_f32_e32 v248, 1.0, v248
	v_add_f32_e32 v249, 1.0, v249
	v_add_f32_e32 v250, 1.0, v250
	v_add_f32_e32 v251, 1.0, v251
	v_add_f32_e32 v252, 1.0, v252
	v_add_f32_e32 v253, 1.0, v253
	v_rcp_f32_e32 v246, v246
	v_rcp_f32_e32 v247, v247
	v_rcp_f32_e32 v248, v248
	v_rcp_f32_e32 v249, v249
	v_rcp_f32_e32 v250, v250
	v_rcp_f32_e32 v251, v251
	v_rcp_f32_e32 v252, v252
	v_rcp_f32_e32 v253, v253
	v_mul_f32_e32 v230, v230, v246
	v_mul_f32_e32 v231, v231, v247
	v_mul_f32_e32 v232, v232, v248
	v_mul_f32_e32 v233, v233, v249
	v_mul_f32_e32 v234, v234, v250
	v_mul_f32_e32 v235, v235, v251
	v_mul_f32_e32 v236, v236, v252
	v_mul_f32_e32 v237, v237, v253
	v_mul_f32_e32 v230, v230, v238
	v_mul_f32_e32 v231, v231, v239
	v_mul_f32_e32 v232, v232, v240
	v_mul_f32_e32 v233, v233, v241
	v_mul_f32_e32 v234, v234, v242
	v_mul_f32_e32 v235, v235, v243
	v_mul_f32_e32 v236, v236, v244
	v_mul_f32_e32 v237, v237, v245
	v_med3_f32 v230, v230, s55, v228
	v_med3_f32 v231, v231, s55, v228
	v_med3_f32 v232, v232, s55, v228
	v_med3_f32 v233, v233, s55, v228
	v_med3_f32 v234, v234, s55, v228
	v_med3_f32 v235, v235, s55, v228
	v_med3_f32 v236, v236, s55, v228
	v_med3_f32 v237, v237, s55, v228
	v_cvt_pk_fp8_f32 v216, v230, v231
	v_cvt_pk_fp8_f32 v217, v234, v235
	v_cvt_pk_fp8_f32 v216, v232, v233 op_sel:[0,0,1]
	v_cvt_pk_fp8_f32 v217, v236, v237 op_sel:[0,0,1]
	s_mov_b32 s100, 0x16000
	v_lshl_add_u64 v[218:219], v[0:1], 0, s[100:101]
	s_nop 0
	global_store_dwordx2 v[218:219], v[216:217], off sc1
	s_and_b64 vcc, exec, s[4:5]
	s_cbranch_vccnz .LBB0_823
	s_andn2_b64 vcc, exec, s[6:7]
	s_cbranch_vccnz .LBB0_822
	s_barrier
	s_branch .LBB0_822
